# P8 router step: the 8 waves split K eight ways and each covers all 64 rows, so router weight fragments are loaded once per workgroup (was 4x); partials summed through LDS; hand-written, double-buffere
# speedup vs baseline: 1.0151x; 1.0151x over previous
.LBB0_1038:
	s_or_b64 exec, exec, s[8:9]
	s_and_saveexec_b64 s[0:1], s[4:5]
	ds_write_b32 v141, v123 offset:57344
	s_or_b64 exec, exec, s[0:1]
	s_ashr_i32 s3, s2, 31
	s_lshl_b64 s[0:1], s[2:3], 6
	s_add_u32 s0, s0, s34
	s_addc_u32 s1, s1, 0
	s_lshl_b64 s[8:9], s[0:1], 12
	v_lshl_add_u64 v[0:1], v[130:131], 0, s[8:9]
	s_waitcnt lgkmcnt(0)
	s_barrier
	global_load_dwordx4 v[80:83], v[0:1], off
	global_load_dwordx4 v[88:91], v[0:1], off offset:1024
	global_load_dwordx4 v[92:95], v[0:1], off offset:2048
	global_load_dwordx4 v[158:161], v[0:1], off offset:3072
	s_lshl_b64 s[20:21], s[0:1], 13
	v_readlane_b32 s36, v253, 10
	v_readlane_b32 s37, v253, 11
	s_add_u32 s20, s36, s20
	s_addc_u32 s21, s37, s21
	global_load_dwordx4 v[72:75], v122, s[20:21] offset:16
	global_load_dwordx4 v[76:79], v122, s[20:21]
	global_load_dwordx4 v[64:67], v122, s[20:21] offset:2064
	global_load_dwordx4 v[68:71], v122, s[20:21] offset:2048
	global_load_dwordx4 v[56:59], v149, s[20:21] offset:16
	global_load_dwordx4 v[60:63], v149, s[20:21]
	global_load_dwordx4 v[48:51], v150, s[20:21] offset:16
	global_load_dwordx4 v[52:55], v150, s[20:21]
	s_or_b32 s20, s0, 1
	s_mov_b32 s21, s1
	s_lshl_b64 s[22:23], s[20:21], 12
	s_lshl_b64 s[24:25], s[20:21], 13
	s_add_u32 s24, s36, s24
	v_lshl_add_u64 v[0:1], v[130:131], 0, s[22:23]
	s_addc_u32 s25, s37, s25
	global_load_dwordx4 v[44:47], v[0:1], off
	global_load_dwordx4 v[40:43], v[0:1], off offset:1024
	global_load_dwordx4 v[36:39], v[0:1], off offset:2048
	global_load_dwordx4 v[32:35], v[0:1], off offset:3072
	global_load_dwordx4 v[24:27], v122, s[24:25] offset:16
	global_load_dwordx4 v[28:31], v122, s[24:25]
	global_load_dwordx4 v[16:19], v122, s[24:25] offset:2064
	global_load_dwordx4 v[20:23], v122, s[24:25] offset:2048
	global_load_dwordx4 v[8:11], v149, s[24:25] offset:16
	global_load_dwordx4 v[12:15], v149, s[24:25]
	global_load_dwordx4 v[0:3], v150, s[24:25] offset:16
	global_load_dwordx4 v[4:7], v150, s[24:25]
	v_readlane_b32 s38, v253, 12
	v_readlane_b32 s39, v253, 13
	v_readlane_b32 s40, v253, 14
	v_readlane_b32 s41, v253, 15
	v_readlane_b32 s42, v253, 16
	v_readlane_b32 s43, v253, 17
	v_readlane_b32 s44, v253, 18
	v_readlane_b32 s45, v253, 19
	v_readlane_b32 s46, v253, 20
	v_readlane_b32 s47, v253, 21
	v_readlane_b32 s48, v253, 22
	v_readlane_b32 s49, v253, 23
	v_readlane_b32 s50, v253, 24
	v_readlane_b32 s51, v253, 25
	s_waitcnt vmcnt(23)
	v_and_b32_e32 v87, 0xffff0000, v80
	v_lshlrev_b32_e32 v116, 16, v80
	v_lshlrev_b32_e32 v84, 16, v82
	v_and_b32_e32 v115, 0xffff0000, v82
	v_mul_f32_e32 v82, v87, v87
	v_lshlrev_b32_e32 v86, 16, v81
	v_fmac_f32_e32 v82, v116, v116
	v_and_b32_e32 v85, 0xffff0000, v81
	v_fmac_f32_e32 v82, v86, v86
	v_fmac_f32_e32 v82, v85, v85
	v_fmac_f32_e32 v82, v84, v84
	v_lshlrev_b32_e32 v114, 16, v83
	v_fmac_f32_e32 v82, v115, v115
	v_and_b32_e32 v113, 0xffff0000, v83
	v_fmac_f32_e32 v82, v114, v114
	v_fmac_f32_e32 v82, v113, v113
	s_waitcnt vmcnt(22)
	v_lshlrev_b32_e32 v112, 16, v88
	v_and_b32_e32 v111, 0xffff0000, v88
	v_fmac_f32_e32 v82, v112, v112
	v_lshlrev_b32_e32 v110, 16, v89
	v_fmac_f32_e32 v82, v111, v111
	v_and_b32_e32 v109, 0xffff0000, v89
	v_fmac_f32_e32 v82, v110, v110
	v_lshlrev_b32_e32 v108, 16, v90
	v_fmac_f32_e32 v82, v109, v109
	v_and_b32_e32 v107, 0xffff0000, v90
	v_fmac_f32_e32 v82, v108, v108
	v_lshlrev_b32_e32 v106, 16, v91
	v_fmac_f32_e32 v82, v107, v107
	v_and_b32_e32 v105, 0xffff0000, v91
	v_fmac_f32_e32 v82, v106, v106
	v_fmac_f32_e32 v82, v105, v105
	s_waitcnt vmcnt(21)
	v_lshlrev_b32_e32 v104, 16, v92
	v_and_b32_e32 v103, 0xffff0000, v92
	v_fmac_f32_e32 v82, v104, v104
	v_lshlrev_b32_e32 v102, 16, v93
	v_fmac_f32_e32 v82, v103, v103
	v_and_b32_e32 v101, 0xffff0000, v93
	v_fmac_f32_e32 v82, v102, v102
	v_lshlrev_b32_e32 v100, 16, v94
	v_fmac_f32_e32 v82, v101, v101
	v_and_b32_e32 v99, 0xffff0000, v94
	v_fmac_f32_e32 v82, v100, v100
	v_lshlrev_b32_e32 v98, 16, v95
	v_fmac_f32_e32 v82, v99, v99
	v_and_b32_e32 v97, 0xffff0000, v95
	v_fmac_f32_e32 v82, v98, v98
	v_fmac_f32_e32 v82, v97, v97
	s_waitcnt vmcnt(20)
	v_lshlrev_b32_e32 v96, 16, v158
	v_and_b32_e32 v91, 0xffff0000, v158
	v_fmac_f32_e32 v82, v96, v96
	v_and_b32_e32 v94, 0xffff0000, v159
	v_lshlrev_b32_e32 v95, 16, v159
	v_fmac_f32_e32 v82, v91, v91
	v_pk_mul_f32 v[80:81], v[94:95], v[94:95]
	v_and_b32_e32 v92, 0xffff0000, v160
	v_add_f32_e32 v81, v81, v82
	v_lshlrev_b32_e32 v93, 16, v160
	v_add_f32_e32 v82, v80, v81
	v_pk_mul_f32 v[80:81], v[92:93], v[92:93]
	v_and_b32_e32 v88, 0xffff0000, v161
	v_add_f32_e32 v81, v81, v82
	v_lshlrev_b32_e32 v89, 16, v161
	v_add_f32_e32 v82, v80, v81
	v_pk_mul_f32 v[80:81], v[88:89], v[88:89]
	s_nop 0
	v_add_f32_e32 v81, v81, v82
	v_add_f32_e32 v80, v80, v81
	s_nop 1
	v_add_f32_dpp v80, v80, v80 quad_perm:[1,0,3,2] row_mask:0xf bank_mask:0xf bound_ctrl:1
	s_nop 1
	v_add_f32_dpp v80, v80, v80 quad_perm:[2,3,0,1] row_mask:0xf bank_mask:0xf bound_ctrl:1
	s_nop 1
	v_add_f32_dpp v80, v80, v80 row_ror:4 row_mask:0xf bank_mask:0xf bound_ctrl:1
	s_nop 1
	v_add_f32_dpp v80, v80, v80 row_ror:8 row_mask:0xf bank_mask:0xf bound_ctrl:1
	s_nop 0
	v_readlane_b32 s3, v80, 16
	v_readlane_b32 s26, v80, 48
	v_readlane_b32 s24, v80, 0
	v_readlane_b32 s25, v80, 32
	v_mov_b32_e32 v80, s3
	v_mov_b32_e32 v81, s26
	v_pk_add_f32 v[80:81], s[24:25], v[80:81]
	s_nop 0
	v_add_f32_e32 v80, v80, v81
	v_fmamk_f32 v80, v80, 0x3a000000, v151
	v_cmp_gt_f32_e32 vcc, s11, v80
	v_mul_f32_e32 v81, 0x4b800000, v80
	s_nop 0
	v_cndmask_b32_e32 v80, v80, v81, vcc
	v_rsq_f32_e32 v80, v80
	s_nop 0
	v_mul_f32_e32 v81, 0x45800000, v80
	v_cndmask_b32_e32 v90, v80, v81, vcc
	ds_read_b128 v[158:161], v144
	ds_read_b128 v[80:83], v144 offset:16
	v_mul_f32_e32 v129, v90, v116
	ds_read_b128 v[116:119], v144 offset:8192
	v_mul_f32_e32 v87, v90, v87
	v_mul_f32_e32 v86, v90, v86
	v_mul_f32_e32 v85, v90, v85
	s_waitcnt lgkmcnt(0)
	v_mul_f32_e32 v87, v117, v87
	v_mul_f32_e32 v86, v118, v86
	v_mul_f32_e32 v85, v119, v85
	s_waitcnt vmcnt(18)
	v_fma_f32 v77, v159, v87, v77
	v_fma_f32 v78, v160, v86, v78
	v_fmac_f32_e32 v79, v161, v85
	v_mul_f32_e32 v117, v90, v84
	ds_read_b128 v[84:87], v144 offset:8208
	v_mul_f32_e32 v116, v116, v129
	v_fma_f32 v76, v158, v116, v76
	v_mul_f32_e32 v116, v77, v77
	v_fmac_f32_e32 v116, v76, v76
	s_waitcnt lgkmcnt(0)
	v_mul_f32_e32 v84, v117, v84
	v_fma_f32 v80, v80, v84, v72
	v_mul_f32_e32 v72, v90, v115
	v_mul_f32_e32 v72, v72, v85
	v_fmac_f32_e32 v116, v78, v78
	v_fma_f32 v81, v81, v72, v73
	v_mul_f32_e32 v72, v90, v114
	v_fmac_f32_e32 v116, v79, v79
	v_mul_f32_e32 v72, v72, v86
	v_fmac_f32_e32 v116, v80, v80
	v_fma_f32 v82, v82, v72, v74
	v_mul_f32_e32 v72, v90, v113
	v_fmac_f32_e32 v116, v81, v81
	v_mul_f32_e32 v72, v72, v87
	v_fmac_f32_e32 v116, v82, v82
	v_fmac_f32_e32 v75, v83, v72
	v_cvt_pk_bf16_f32 v72, v76, v77
	v_lshl_add_u64 v[76:77], v[132:133], 0, s[8:9]
	v_fmac_f32_e32 v116, v75, v75
	v_cvt_pk_bf16_f32 v73, v78, v79
	v_cvt_pk_bf16_f32 v74, v80, v81
	v_cvt_pk_bf16_f32 v75, v82, v75
	global_store_dwordx4 v[76:77], v[72:75], off
	ds_read_b128 v[78:81], v144 offset:2048
	ds_read_b128 v[82:85], v144 offset:2064
	v_mul_f32_e32 v86, v90, v112
	ds_read_b128 v[112:115], v144 offset:10240
	s_waitcnt lgkmcnt(0)
	v_mul_f32_e32 v86, v86, v112
	s_waitcnt vmcnt(17)
	v_fma_f32 v68, v78, v86, v68
	v_mul_f32_e32 v78, v90, v111
	v_mul_f32_e32 v78, v78, v113
	v_fma_f32 v69, v79, v78, v69
	v_mul_f32_e32 v78, v90, v110
	v_mul_f32_e32 v78, v78, v114
	v_fma_f32 v70, v80, v78, v70
	v_mul_f32_e32 v78, v90, v109
	v_mul_f32_e32 v78, v78, v115
	v_fmac_f32_e32 v71, v81, v78
	ds_read_b128 v[78:81], v144 offset:10256
	v_mul_f32_e32 v86, v90, v108
	v_fmac_f32_e32 v116, v68, v68
	v_fmac_f32_e32 v116, v69, v69
	v_fmac_f32_e32 v116, v70, v70
	s_waitcnt lgkmcnt(0)
	v_mul_f32_e32 v78, v86, v78
	v_fma_f32 v78, v82, v78, v64
	v_mul_f32_e32 v64, v90, v107
	v_mul_f32_e32 v64, v64, v79
	v_fma_f32 v79, v83, v64, v65
	v_mul_f32_e32 v64, v90, v106
	v_fmac_f32_e32 v116, v71, v71
	v_mul_f32_e32 v64, v64, v80
	v_fmac_f32_e32 v116, v78, v78
	v_fma_f32 v80, v84, v64, v66
	v_mul_f32_e32 v64, v90, v105
	v_fmac_f32_e32 v116, v79, v79
	v_mul_f32_e32 v64, v64, v81
	v_fmac_f32_e32 v116, v80, v80
	v_fmac_f32_e32 v67, v85, v64
	v_fmac_f32_e32 v116, v67, v67
	v_cvt_pk_bf16_f32 v64, v68, v69
	v_cvt_pk_bf16_f32 v65, v70, v71
	v_cvt_pk_bf16_f32 v66, v78, v79
	v_cvt_pk_bf16_f32 v67, v80, v67
	global_store_dwordx4 v[76:77], v[64:67], off offset:1024
	ds_read_b128 v[68:71], v144 offset:4096
	ds_read_b128 v[78:81], v144 offset:4112
	ds_read_b128 v[82:85], v144 offset:12288
	v_mul_f32_e32 v86, v90, v104
	s_waitcnt lgkmcnt(0)
	v_mul_f32_e32 v82, v86, v82
	s_waitcnt vmcnt(16)
	v_fma_f32 v60, v68, v82, v60
	v_mul_f32_e32 v68, v90, v103
	v_mul_f32_e32 v68, v68, v83
	v_fma_f32 v61, v69, v68, v61
	v_mul_f32_e32 v68, v90, v102
	v_mul_f32_e32 v68, v68, v84
	v_fma_f32 v62, v70, v68, v62
	v_mul_f32_e32 v68, v90, v101
	v_mul_f32_e32 v68, v68, v85
	v_fmac_f32_e32 v63, v71, v68
	ds_read_b128 v[68:71], v144 offset:12304
	v_mul_f32_e32 v82, v90, v100
	v_fmac_f32_e32 v116, v60, v60
	v_fmac_f32_e32 v116, v61, v61
	v_fmac_f32_e32 v116, v62, v62
	s_waitcnt lgkmcnt(0)
	v_mul_f32_e32 v68, v82, v68
	v_fma_f32 v68, v78, v68, v56
	v_mul_f32_e32 v56, v90, v99
	v_mul_f32_e32 v56, v56, v69
	v_fma_f32 v69, v79, v56, v57
	v_mul_f32_e32 v56, v90, v98
	v_fmac_f32_e32 v116, v63, v63
	v_mul_f32_e32 v56, v56, v70
	v_fmac_f32_e32 v116, v68, v68
	v_fma_f32 v70, v80, v56, v58
	v_mul_f32_e32 v56, v90, v97
	v_fmac_f32_e32 v116, v69, v69
	v_mul_f32_e32 v56, v56, v71
	v_fmac_f32_e32 v116, v70, v70
	v_fmac_f32_e32 v59, v81, v56
	v_fmac_f32_e32 v116, v59, v59
	v_cvt_pk_bf16_f32 v56, v60, v61
	v_cvt_pk_bf16_f32 v57, v62, v63
	v_cvt_pk_bf16_f32 v58, v68, v69
	v_cvt_pk_bf16_f32 v59, v70, v59
	global_store_dwordx4 v[76:77], v[56:59], off offset:2048
	ds_read_b128 v[60:63], v144 offset:6144
	ds_read_b128 v[68:71], v144 offset:6160
	ds_read_b128 v[78:81], v144 offset:14336
	v_mul_f32_e32 v82, v90, v96
	s_waitcnt lgkmcnt(0)
	v_mul_f32_e32 v78, v82, v78
	s_waitcnt vmcnt(15)
	v_fma_f32 v78, v60, v78, v52
	v_mul_f32_e32 v52, v90, v91
	v_mul_f32_e32 v52, v52, v79
	v_fma_f32 v79, v61, v52, v53
	v_pk_mul_f32 v[52:53], v[90:91], v[94:95] op_sel_hi:[0,1]
	v_pk_mul_f32 v[52:53], v[52:53], v[80:81] op_sel:[1,0] op_sel_hi:[0,1]
	v_fmac_f32_e32 v116, v78, v78
	v_pk_fma_f32 v[60:61], v[62:63], v[52:53], v[54:55]
	v_fmac_f32_e32 v116, v79, v79
	v_pk_mul_f32 v[52:53], v[60:61], v[60:61]
	v_pk_mul_f32 v[62:63], v[90:91], v[92:93] op_sel_hi:[0,1]
	v_add_f32_e32 v52, v116, v52
	v_add_f32_e32 v80, v52, v53
	ds_read_b128 v[52:55], v144 offset:14352
	s_waitcnt lgkmcnt(0)
	v_pk_mul_f32 v[52:53], v[62:63], v[52:53] op_sel:[1,0] op_sel_hi:[0,1]
	v_pk_fma_f32 v[52:53], v[68:69], v[52:53], v[48:49]
	s_nop 0
	v_pk_mul_f32 v[48:49], v[52:53], v[52:53]
	s_nop 0
	v_add_f32_e32 v48, v80, v48
	v_add_f32_e32 v62, v48, v49
	v_pk_mul_f32 v[48:49], v[90:91], v[88:89] op_sel_hi:[0,1]
	v_pk_mul_f32 v[48:49], v[48:49], v[54:55] op_sel:[1,0] op_sel_hi:[0,1]
	v_pk_fma_f32 v[54:55], v[70:71], v[48:49], v[50:51]
	s_nop 0
	v_pk_mul_f32 v[48:49], v[54:55], v[54:55]
	s_nop 0
	v_add_f32_e32 v48, v62, v48
	v_add_f32_e32 v62, v48, v49
	v_cvt_pk_bf16_f32 v48, v78, v79
	v_cvt_pk_bf16_f32 v49, v60, v61
	v_cvt_pk_bf16_f32 v50, v52, v53
	v_cvt_pk_bf16_f32 v51, v54, v55
	global_store_dwordx4 v[76:77], v[48:51], off offset:3072
	s_nop 0
	v_add_f32_dpp v52, v62, v62 quad_perm:[1,0,3,2] row_mask:0xf bank_mask:0xf bound_ctrl:1
	s_nop 1
	v_add_f32_dpp v52, v52, v52 quad_perm:[2,3,0,1] row_mask:0xf bank_mask:0xf bound_ctrl:1
	s_nop 1
	v_add_f32_dpp v52, v52, v52 row_ror:4 row_mask:0xf bank_mask:0xf bound_ctrl:1
	s_nop 1
	v_add_f32_dpp v52, v52, v52 row_ror:8 row_mask:0xf bank_mask:0xf bound_ctrl:1
	s_nop 0
	v_readlane_b32 s3, v52, 16
	v_readlane_b32 s24, v52, 48
	v_readlane_b32 s8, v52, 0
	v_readlane_b32 s9, v52, 32
	v_mov_b32_e32 v52, s3
	v_mov_b32_e32 v53, s24
	v_pk_add_f32 v[52:53], s[8:9], v[52:53]
	s_nop 0
	v_add_f32_e32 v52, v52, v53
	v_fmamk_f32 v52, v52, 0x3a000000, v151
	v_cmp_gt_f32_e32 vcc, s11, v52
	v_mul_f32_e32 v53, 0x4b800000, v52
	s_nop 0
	v_cndmask_b32_e32 v52, v52, v53, vcc
	v_rsq_f32_e32 v52, v52
	s_nop 0
	v_mul_f32_e32 v53, 0x45800000, v52
	v_cndmask_b32_e32 v54, v52, v53, vcc
	s_and_saveexec_b64 s[8:9], s[6:7]
	v_mov_b32_e32 v52, s10
	ds_write_b32 v52, v54 offset:60672
	s_or_b64 exec, exec, s[8:9]
	v_lshlrev_b32_e32 v52, 16, v72
	v_and_b32_e32 v53, 0xffff0000, v72
	v_lshlrev_b32_e32 v55, 16, v73
	v_and_b32_e32 v76, 0xffff0000, v73
	v_lshlrev_b32_e32 v77, 16, v74
	v_and_b32_e32 v78, 0xffff0000, v74
	v_lshlrev_b32_e32 v79, 16, v75
	v_and_b32_e32 v80, 0xffff0000, v75
	ds_read_b128 v[60:63], v144 offset:16384
	ds_read_b128 v[68:71], v144 offset:16400
	ds_read_b128 v[72:75], v144 offset:32768
	v_mul_f32_e32 v52, v54, v52
	v_mul_f32_e32 v53, v54, v53
	v_mul_f32_e32 v55, v54, v55
	s_lshl_b64 s[8:9], s[0:1], 11
	s_waitcnt lgkmcnt(0)
	v_fma_f32 v52, v52, v60, v72
	v_mul_f32_e32 v60, v54, v76
	v_fma_f32 v53, v53, v61, v73
	v_fma_f32 v55, v55, v62, v74
	v_fmac_f32_e32 v75, v60, v63
	ds_read_b128 v[60:63], v144 offset:32784
	v_mul_f32_e32 v72, v54, v77
	v_med3_f32 v52, v52, s12, v154
	v_med3_f32 v53, v53, s12, v154
	v_med3_f32 v55, v55, s12, v154
	s_waitcnt lgkmcnt(0)
	v_fma_f32 v68, v72, v68, v60
	v_mul_f32_e32 v60, v54, v78
	v_fma_f32 v61, v60, v69, v61
	v_mul_f32_e32 v60, v54, v79
	v_fma_f32 v62, v60, v70, v62
	v_mul_f32_e32 v60, v54, v80
	v_fmac_f32_e32 v63, v60, v71
	v_mov_b32_e32 v60, 0
	v_cvt_pk_fp8_f32 v60, v52, v53
	v_med3_f32 v52, v68, s12, v154
	v_med3_f32 v53, v61, s12, v154
	v_mov_b32_e32 v61, 0
	v_cvt_pk_fp8_f32 v61, v52, v53
	v_med3_f32 v69, v75, s12, v154
	v_cvt_pk_fp8_f32 v60, v55, v69 op_sel:[0,0,1]
	v_med3_f32 v55, v62, s12, v154
	v_med3_f32 v62, v63, s12, v154
	v_cvt_pk_fp8_f32 v61, v55, v62 op_sel:[0,0,1]
	v_lshl_add_u64 v[52:53], v[134:135], 0, s[8:9]
	v_lshlrev_b32_e32 v55, 16, v64
	v_and_b32_e32 v68, 0xffff0000, v64
	global_store_dwordx2 v[52:53], v[60:61], off
	v_lshlrev_b32_e32 v69, 16, v65
	v_and_b32_e32 v70, 0xffff0000, v65
	v_lshlrev_b32_e32 v71, 16, v66
	v_and_b32_e32 v72, 0xffff0000, v66
	v_lshlrev_b32_e32 v73, 16, v67
	v_and_b32_e32 v74, 0xffff0000, v67
	ds_read_b128 v[60:63], v144 offset:18432
	ds_read_b128 v[64:67], v144 offset:34816
	v_mul_f32_e32 v55, v54, v55
	s_waitcnt vmcnt(16)
	v_and_b32_e32 v100, 0xffff0000, v44
	v_lshlrev_b32_e32 v92, 16, v44
	v_mul_f32_e32 v76, v100, v100
	s_waitcnt lgkmcnt(0)
	v_fma_f32 v55, v55, v60, v64
	v_mul_f32_e32 v60, v54, v68
	v_fma_f32 v64, v60, v61, v65
	v_mul_f32_e32 v60, v54, v69
	v_fma_f32 v65, v60, v62, v66
	v_mul_f32_e32 v60, v54, v70
	v_fmac_f32_e32 v67, v60, v63
	v_mul_f32_e32 v66, v54, v71
	ds_read_b128 v[60:63], v144 offset:18448
	ds_read_b128 v[68:71], v144 offset:34832
	v_med3_f32 v55, v55, s12, v154
	v_lshlrev_b32_e32 v101, 16, v45
	v_fmac_f32_e32 v76, v92, v92
	v_and_b32_e32 v45, 0xffff0000, v45
	s_waitcnt lgkmcnt(0)
	v_fma_f32 v66, v66, v60, v68
	v_mul_f32_e32 v60, v54, v72
	v_fma_f32 v61, v60, v61, v69
	v_mul_f32_e32 v60, v54, v73
	v_fma_f32 v62, v60, v62, v70
	v_mul_f32_e32 v60, v54, v74
	v_fmac_f32_e32 v71, v60, v63
	v_med3_f32 v63, v64, s12, v154
	v_mov_b32_e32 v60, 0
	v_cvt_pk_fp8_f32 v60, v55, v63
	v_med3_f32 v55, v66, s12, v154
	v_med3_f32 v63, v61, s12, v154
	v_mov_b32_e32 v61, 0
	v_cvt_pk_fp8_f32 v61, v55, v63
	v_med3_f32 v64, v65, s12, v154
	v_med3_f32 v65, v67, s12, v154
	v_cvt_pk_fp8_f32 v60, v64, v65 op_sel:[0,0,1]
	v_med3_f32 v62, v62, s12, v154
	v_med3_f32 v64, v71, s12, v154
	v_cvt_pk_fp8_f32 v61, v62, v64 op_sel:[0,0,1]
	v_lshlrev_b32_e32 v55, 16, v56
	v_and_b32_e32 v64, 0xffff0000, v56
	v_lshlrev_b32_e32 v65, 16, v57
	global_store_dwordx2 v[52:53], v[60:61], off offset:512
	v_and_b32_e32 v66, 0xffff0000, v57
	v_lshlrev_b32_e32 v67, 16, v58
	v_and_b32_e32 v68, 0xffff0000, v58
	v_lshlrev_b32_e32 v69, 16, v59
	v_and_b32_e32 v70, 0xffff0000, v59
	ds_read_b128 v[56:59], v144 offset:20480
	ds_read_b128 v[60:63], v144 offset:36864
	v_mul_f32_e32 v55, v54, v55
	v_fmac_f32_e32 v76, v101, v101
	v_lshlrev_b32_e32 v102, 16, v46
	v_fmac_f32_e32 v76, v45, v45
	s_waitcnt lgkmcnt(0)
	v_fma_f32 v55, v55, v56, v60
	v_mul_f32_e32 v56, v54, v64
	v_fma_f32 v60, v56, v57, v61
	v_mul_f32_e32 v56, v54, v65
	v_fma_f32 v61, v56, v58, v62
	v_mul_f32_e32 v56, v54, v66
	v_fmac_f32_e32 v63, v56, v59
	v_mul_f32_e32 v62, v54, v67
	ds_read_b128 v[56:59], v144 offset:20496
	ds_read_b128 v[64:67], v144 offset:36880
	v_med3_f32 v55, v55, s12, v154
	v_and_b32_e32 v46, 0xffff0000, v46
	v_fmac_f32_e32 v76, v102, v102
	v_lshlrev_b32_e32 v103, 16, v47
	s_waitcnt lgkmcnt(0)
	v_fma_f32 v62, v62, v56, v64
	v_mul_f32_e32 v56, v54, v68
	v_fma_f32 v57, v56, v57, v65
	v_mul_f32_e32 v56, v54, v69
	v_fma_f32 v58, v56, v58, v66
	v_mul_f32_e32 v56, v54, v70
	v_fmac_f32_e32 v67, v56, v59
	v_med3_f32 v59, v60, s12, v154
	v_mov_b32_e32 v56, 0
	v_cvt_pk_fp8_f32 v56, v55, v59
	v_med3_f32 v55, v62, s12, v154
	v_med3_f32 v59, v57, s12, v154
	v_mov_b32_e32 v57, 0
	v_cvt_pk_fp8_f32 v57, v55, v59
	v_med3_f32 v60, v61, s12, v154
	v_med3_f32 v61, v63, s12, v154
	v_cvt_pk_fp8_f32 v56, v60, v61 op_sel:[0,0,1]
	v_med3_f32 v58, v58, s12, v154
	v_med3_f32 v60, v67, s12, v154
	v_fmac_f32_e32 v76, v46, v46
	v_cvt_pk_fp8_f32 v57, v58, v60 op_sel:[0,0,1]
	v_and_b32_e32 v47, 0xffff0000, v47
	v_fmac_f32_e32 v76, v103, v103
	v_fmac_f32_e32 v76, v47, v47
	s_waitcnt vmcnt(16)
	v_lshlrev_b32_e32 v108, 16, v40
	v_and_b32_e32 v109, 0xffff0000, v40
	v_fmac_f32_e32 v76, v108, v108
	v_lshlrev_b32_e32 v110, 16, v41
	v_fmac_f32_e32 v76, v109, v109
	global_store_dwordx2 v[52:53], v[56:57], off offset:1024
	v_and_b32_e32 v111, 0xffff0000, v41
	v_fmac_f32_e32 v76, v110, v110
	v_lshlrev_b32_e32 v55, 16, v48
	v_and_b32_e32 v60, 0xffff0000, v48
	v_lshlrev_b32_e32 v61, 16, v49
	v_and_b32_e32 v62, 0xffff0000, v49
	v_lshlrev_b32_e32 v63, 16, v50
	v_and_b32_e32 v64, 0xffff0000, v50
	v_lshlrev_b32_e32 v65, 16, v51
	v_and_b32_e32 v66, 0xffff0000, v51
	ds_read_b128 v[48:51], v144 offset:22528
	ds_read_b128 v[56:59], v144 offset:38912
	v_lshlrev_b32_e32 v116, 16, v42
	v_fmac_f32_e32 v76, v111, v111
	v_and_b32_e32 v117, 0xffff0000, v42
	v_fmac_f32_e32 v76, v116, v116
	v_lshlrev_b32_e32 v118, 16, v43
	v_fmac_f32_e32 v76, v117, v117
	v_and_b32_e32 v119, 0xffff0000, v43
	v_fmac_f32_e32 v76, v118, v118
	v_mul_f32_e32 v55, v54, v55
	v_fmac_f32_e32 v76, v119, v119
	s_waitcnt vmcnt(16)
	v_lshlrev_b32_e32 v129, 16, v36
	s_waitcnt lgkmcnt(0)
	v_fma_f32 v55, v55, v48, v56
	v_mul_f32_e32 v48, v54, v60
	v_and_b32_e32 v157, 0xffff0000, v36
	v_fmac_f32_e32 v76, v129, v129
	v_fma_f32 v56, v48, v49, v57
	v_mul_f32_e32 v48, v54, v61
	v_lshlrev_b32_e32 v158, 16, v37
	v_fmac_f32_e32 v76, v157, v157
	v_fma_f32 v57, v48, v50, v58
	v_mul_f32_e32 v48, v54, v62
	v_and_b32_e32 v159, 0xffff0000, v37
	v_fmac_f32_e32 v76, v158, v158
	v_fmac_f32_e32 v59, v48, v51
	v_mul_f32_e32 v58, v54, v63
	ds_read_b128 v[48:51], v144 offset:22544
	ds_read_b128 v[60:63], v144 offset:38928
	v_lshlrev_b32_e32 v160, 16, v38
	v_fmac_f32_e32 v76, v159, v159
	v_and_b32_e32 v44, 0xffff0000, v38
	v_fmac_f32_e32 v76, v160, v160
	v_lshlrev_b32_e32 v42, 16, v39
	v_fmac_f32_e32 v76, v44, v44
	v_and_b32_e32 v41, 0xffff0000, v39
	v_fmac_f32_e32 v76, v42, v42
	v_fmac_f32_e32 v76, v41, v41
	s_waitcnt vmcnt(15)
	v_lshlrev_b32_e32 v43, 16, v32
	s_waitcnt lgkmcnt(0)
	v_fma_f32 v58, v58, v48, v60
	v_mul_f32_e32 v48, v54, v64
	v_and_b32_e32 v40, 0xffff0000, v32
	v_fmac_f32_e32 v76, v43, v43
	v_and_b32_e32 v36, 0xffff0000, v33
	v_lshlrev_b32_e32 v37, 16, v33
	v_fma_f32 v49, v48, v49, v61
	v_mul_f32_e32 v48, v54, v65
	v_fmac_f32_e32 v76, v40, v40
	v_pk_mul_f32 v[32:33], v[36:37], v[36:37]
	v_fma_f32 v50, v48, v50, v62
	v_mul_f32_e32 v48, v54, v66
	v_add_f32_e32 v33, v33, v76
	v_and_b32_e32 v38, 0xffff0000, v34
	v_lshlrev_b32_e32 v39, 16, v34
	v_fmac_f32_e32 v63, v48, v51
	v_med3_f32 v51, v55, s12, v154
	v_med3_f32 v54, v56, s12, v154
	v_mov_b32_e32 v48, 0
	v_add_f32_e32 v76, v32, v33
	v_pk_mul_f32 v[32:33], v[38:39], v[38:39]
	v_cvt_pk_fp8_f32 v48, v51, v54
	v_med3_f32 v51, v58, s12, v154
	v_med3_f32 v54, v49, s12, v154
	v_mov_b32_e32 v49, 0
	v_add_f32_e32 v33, v33, v76
	v_cvt_pk_fp8_f32 v49, v51, v54
	v_add_f32_e32 v76, v32, v33
	v_and_b32_e32 v32, 0xffff0000, v35
	v_lshlrev_b32_e32 v33, 16, v35
	v_pk_mul_f32 v[34:35], v[32:33], v[32:33]
	v_med3_f32 v55, v57, s12, v154
	v_med3_f32 v56, v59, s12, v154
	v_add_f32_e32 v35, v35, v76
	v_cvt_pk_fp8_f32 v48, v55, v56 op_sel:[0,0,1]
	v_med3_f32 v50, v50, s12, v154
	v_med3_f32 v55, v63, s12, v154
	v_add_f32_e32 v34, v34, v35
	v_cvt_pk_fp8_f32 v49, v50, v55 op_sel:[0,0,1]
	s_or_b32 s24, s0, 2
	v_add_f32_dpp v34, v34, v34 quad_perm:[1,0,3,2] row_mask:0xf bank_mask:0xf bound_ctrl:1
	s_mov_b32 s25, s1
	s_lshl_b64 s[8:9], s[24:25], 12
	v_add_f32_dpp v34, v34, v34 quad_perm:[2,3,0,1] row_mask:0xf bank_mask:0xf bound_ctrl:1
	s_lshl_b64 s[26:27], s[24:25], 13
	v_readlane_b32 s36, v253, 10
	v_add_f32_dpp v34, v34, v34 row_ror:4 row_mask:0xf bank_mask:0xf bound_ctrl:1
	v_readlane_b32 s37, v253, 11
	s_add_u32 s26, s36, s26
	v_add_f32_dpp v34, v34, v34 row_ror:8 row_mask:0xf bank_mask:0xf bound_ctrl:1
	global_store_dwordx2 v[52:53], v[48:49], off offset:1536
	v_lshl_add_u64 v[48:49], v[130:131], 0, s[8:9]
	s_addc_u32 s27, s37, s27
	v_readlane_b32 s3, v34, 16
	v_readlane_b32 s28, v34, 48
	global_load_dwordx4 v[112:115], v[48:49], off
	global_load_dwordx4 v[104:107], v[48:49], off offset:1024
	global_load_dwordx4 v[96:99], v[48:49], off offset:2048
	global_load_dwordx4 v[88:91], v[48:49], off offset:3072
	global_load_dwordx4 v[72:75], v122, s[26:27] offset:16
	global_load_dwordx4 v[80:83], v122, s[26:27]
	global_load_dwordx4 v[64:67], v122, s[26:27] offset:2064
	global_load_dwordx4 v[68:71], v122, s[26:27] offset:2048
	global_load_dwordx4 v[56:59], v149, s[26:27] offset:16
	global_load_dwordx4 v[60:63], v149, s[26:27]
	global_load_dwordx4 v[48:51], v150, s[26:27] offset:16
	global_load_dwordx4 v[52:55], v150, s[26:27]
	v_readlane_b32 s26, v34, 0
	v_readlane_b32 s27, v34, 32
	v_mov_b32_e32 v34, s3
	v_mov_b32_e32 v35, s28
	v_pk_add_f32 v[34:35], s[26:27], v[34:35]
	ds_read_b128 v[76:79], v144
	ds_read_b128 v[84:87], v144 offset:16
	v_add_f32_e32 v34, v34, v35
	v_fmamk_f32 v34, v34, 0x3a000000, v151
	v_cmp_gt_f32_e32 vcc, s11, v34
	v_mul_f32_e32 v35, 0x4b800000, v34
	v_readlane_b32 s38, v253, 12
	v_cndmask_b32_e32 v34, v34, v35, vcc
	v_rsq_f32_e32 v34, v34
	v_readlane_b32 s39, v253, 13
	v_readlane_b32 s40, v253, 14
	v_readlane_b32 s41, v253, 15
	v_mul_f32_e32 v35, 0x45800000, v34
	v_cndmask_b32_e32 v34, v34, v35, vcc
	v_mul_f32_e32 v35, v34, v92
	ds_read_b128 v[92:95], v144 offset:8192
	v_mul_f32_e32 v45, v34, v45
	v_readlane_b32 s42, v253, 16
	v_readlane_b32 s43, v253, 17
	v_readlane_b32 s44, v253, 18
	s_waitcnt lgkmcnt(0)
	v_mul_f32_e32 v35, v92, v35
	s_waitcnt vmcnt(26)
	v_fma_f32 v28, v76, v35, v28
	v_mul_f32_e32 v35, v34, v100
	v_mul_f32_e32 v76, v34, v101
	v_mul_f32_e32 v35, v93, v35
	v_mul_f32_e32 v76, v94, v76
	v_mul_f32_e32 v45, v95, v45
	v_fma_f32 v29, v77, v35, v29
	v_fma_f32 v30, v78, v76, v30
	v_fmac_f32_e32 v31, v79, v45
	ds_read_b128 v[76:79], v144 offset:8208
	v_mul_f32_e32 v45, v34, v102
	v_mul_f32_e32 v35, v29, v29
	v_fmac_f32_e32 v35, v28, v28
	v_fmac_f32_e32 v35, v30, v30
	s_waitcnt lgkmcnt(0)
	v_mul_f32_e32 v45, v45, v76
	v_fma_f32 v45, v84, v45, v24
	v_mul_f32_e32 v24, v34, v46
	v_mul_f32_e32 v24, v24, v77
	v_fma_f32 v46, v85, v24, v25
	v_mul_f32_e32 v24, v34, v103
	v_fmac_f32_e32 v35, v31, v31
	v_mul_f32_e32 v24, v24, v78
	v_fmac_f32_e32 v35, v45, v45
	v_fma_f32 v76, v86, v24, v26
	v_mul_f32_e32 v24, v34, v47
	v_fmac_f32_e32 v35, v46, v46
	v_mul_f32_e32 v24, v24, v79
	v_fmac_f32_e32 v35, v76, v76
	v_fmac_f32_e32 v27, v87, v24
	v_cvt_pk_bf16_f32 v24, v28, v29
	v_lshl_add_u64 v[28:29], v[132:133], 0, s[22:23]
	v_fmac_f32_e32 v35, v27, v27
	v_cvt_pk_bf16_f32 v25, v30, v31
	v_cvt_pk_bf16_f32 v26, v45, v46
	v_cvt_pk_bf16_f32 v27, v76, v27
	global_store_dwordx4 v[28:29], v[24:27], off
	ds_read_b128 v[76:79], v144 offset:2048
	ds_read_b128 v[84:87], v144 offset:2064
	ds_read_b128 v[92:95], v144 offset:10240
	v_mul_f32_e32 v30, v34, v108
	v_readlane_b32 s45, v253, 19
	v_readlane_b32 s46, v253, 20
	v_readlane_b32 s47, v253, 21
	s_waitcnt lgkmcnt(0)
	v_mul_f32_e32 v30, v30, v92
	s_waitcnt vmcnt(25)
	v_fma_f32 v20, v76, v30, v20
	v_mul_f32_e32 v30, v34, v109
	v_mul_f32_e32 v30, v30, v93
	v_fma_f32 v21, v77, v30, v21
	v_mul_f32_e32 v30, v34, v110
	v_mul_f32_e32 v30, v30, v94
	v_fma_f32 v22, v78, v30, v22
	v_mul_f32_e32 v30, v34, v111
	v_mul_f32_e32 v30, v30, v95
	v_fmac_f32_e32 v23, v79, v30
	ds_read_b128 v[76:79], v144 offset:10256
	v_mul_f32_e32 v30, v34, v116
	v_fmac_f32_e32 v35, v20, v20
	v_fmac_f32_e32 v35, v21, v21
	v_fmac_f32_e32 v35, v22, v22
	s_waitcnt lgkmcnt(0)
	v_mul_f32_e32 v30, v30, v76
	v_fma_f32 v30, v84, v30, v16
	v_mul_f32_e32 v16, v34, v117
	v_mul_f32_e32 v16, v16, v77
	v_fma_f32 v31, v85, v16, v17
	v_mul_f32_e32 v16, v34, v118
	v_fmac_f32_e32 v35, v23, v23
	v_mul_f32_e32 v16, v16, v78
	v_fmac_f32_e32 v35, v30, v30
	v_fma_f32 v45, v86, v16, v18
	v_mul_f32_e32 v16, v34, v119
	v_fmac_f32_e32 v35, v31, v31
	v_mul_f32_e32 v16, v16, v79
	v_fmac_f32_e32 v35, v45, v45
	v_fmac_f32_e32 v19, v87, v16
	v_fmac_f32_e32 v35, v19, v19
	v_cvt_pk_bf16_f32 v16, v20, v21
	v_cvt_pk_bf16_f32 v17, v22, v23
	v_cvt_pk_bf16_f32 v18, v30, v31
	v_cvt_pk_bf16_f32 v19, v45, v19
	global_store_dwordx4 v[28:29], v[16:19], off offset:1024
	ds_read_b128 v[20:23], v144 offset:4096
	ds_read_b128 v[76:79], v144 offset:4112
	ds_read_b128 v[84:87], v144 offset:12288
	v_mul_f32_e32 v30, v34, v129
	v_readlane_b32 s48, v253, 22
	v_readlane_b32 s49, v253, 23
	v_readlane_b32 s50, v253, 24
	s_waitcnt lgkmcnt(0)
	v_mul_f32_e32 v30, v30, v84
	s_waitcnt vmcnt(24)
	v_fma_f32 v12, v20, v30, v12
	v_mul_f32_e32 v20, v34, v157
	v_mul_f32_e32 v20, v20, v85
	v_fma_f32 v13, v21, v20, v13
	v_mul_f32_e32 v20, v34, v158
	v_mul_f32_e32 v20, v20, v86
	v_fma_f32 v14, v22, v20, v14
	v_mul_f32_e32 v20, v34, v159
	v_mul_f32_e32 v20, v20, v87
	v_fmac_f32_e32 v15, v23, v20
	ds_read_b128 v[20:23], v144 offset:12304
	v_mul_f32_e32 v30, v34, v160
	v_fmac_f32_e32 v35, v12, v12
	v_fmac_f32_e32 v35, v13, v13
	v_fmac_f32_e32 v35, v14, v14
	s_waitcnt lgkmcnt(0)
	v_mul_f32_e32 v20, v30, v20
	v_fma_f32 v20, v76, v20, v8
	v_mul_f32_e32 v8, v34, v44
	v_mul_f32_e32 v8, v8, v21
	v_fma_f32 v21, v77, v8, v9
	v_mul_f32_e32 v8, v34, v42
	v_fmac_f32_e32 v35, v15, v15
	v_mul_f32_e32 v8, v8, v22
	v_fmac_f32_e32 v35, v20, v20
	v_fma_f32 v22, v78, v8, v10
	v_mul_f32_e32 v8, v34, v41
	v_fmac_f32_e32 v35, v21, v21
	v_mul_f32_e32 v8, v8, v23
	v_fmac_f32_e32 v35, v22, v22
	v_fmac_f32_e32 v11, v79, v8
	v_fmac_f32_e32 v35, v11, v11
	v_cvt_pk_bf16_f32 v8, v12, v13
	v_cvt_pk_bf16_f32 v9, v14, v15
	v_cvt_pk_bf16_f32 v10, v20, v21
	v_cvt_pk_bf16_f32 v11, v22, v11
	global_store_dwordx4 v[28:29], v[8:11], off offset:2048
	ds_read_b128 v[12:15], v144 offset:6144
	ds_read_b128 v[20:23], v144 offset:6160
	v_mul_f32_e32 v30, v34, v43
	ds_read_b128 v[42:45], v144 offset:14336
	v_readlane_b32 s51, v253, 25
	s_waitcnt lgkmcnt(0)
	v_mul_f32_e32 v30, v30, v42
	s_waitcnt vmcnt(23)
	v_fma_f32 v30, v12, v30, v4
	v_mul_f32_e32 v4, v34, v40
	v_mul_f32_e32 v4, v4, v43
	v_fmac_f32_e32 v35, v30, v30
	v_fma_f32 v31, v13, v4, v5
	v_fmac_f32_e32 v35, v31, v31
	v_pk_mul_f32 v[4:5], v[34:35], v[36:37] op_sel_hi:[0,1]
	v_pk_mul_f32 v[4:5], v[4:5], v[44:45] op_sel:[1,0] op_sel_hi:[0,1]
	v_pk_fma_f32 v[12:13], v[14:15], v[4:5], v[6:7]
	s_nop 0
	v_pk_mul_f32 v[4:5], v[12:13], v[12:13]
	s_nop 0
	v_add_f32_e32 v4, v35, v4
	v_add_f32_e32 v35, v4, v5
	ds_read_b128 v[4:7], v144 offset:14352
	v_pk_mul_f32 v[14:15], v[34:35], v[38:39] op_sel_hi:[0,1]
	s_waitcnt lgkmcnt(0)
	v_pk_mul_f32 v[4:5], v[14:15], v[4:5] op_sel:[1,0] op_sel_hi:[0,1]
	v_pk_fma_f32 v[4:5], v[20:21], v[4:5], v[0:1]
	s_nop 0
	v_pk_mul_f32 v[0:1], v[4:5], v[4:5]
	s_nop 0
	v_add_f32_e32 v0, v35, v0
	v_add_f32_e32 v14, v0, v1
	v_pk_mul_f32 v[0:1], v[34:35], v[32:33] op_sel_hi:[0,1]
	v_pk_mul_f32 v[0:1], v[0:1], v[6:7] op_sel:[1,0] op_sel_hi:[0,1]
	v_pk_fma_f32 v[6:7], v[22:23], v[0:1], v[2:3]
	s_nop 0
	v_pk_mul_f32 v[0:1], v[6:7], v[6:7]
	s_nop 0
	v_add_f32_e32 v0, v14, v0
	v_add_f32_e32 v14, v0, v1
	v_cvt_pk_bf16_f32 v0, v30, v31
	v_cvt_pk_bf16_f32 v1, v12, v13
	v_cvt_pk_bf16_f32 v2, v4, v5
	v_cvt_pk_bf16_f32 v3, v6, v7
	global_store_dwordx4 v[28:29], v[0:3], off offset:3072
	s_nop 0
	v_add_f32_dpp v4, v14, v14 quad_perm:[1,0,3,2] row_mask:0xf bank_mask:0xf bound_ctrl:1
	s_nop 1
	v_add_f32_dpp v4, v4, v4 quad_perm:[2,3,0,1] row_mask:0xf bank_mask:0xf bound_ctrl:1
	s_nop 1
	v_add_f32_dpp v4, v4, v4 row_ror:4 row_mask:0xf bank_mask:0xf bound_ctrl:1
	s_nop 1
	v_add_f32_dpp v4, v4, v4 row_ror:8 row_mask:0xf bank_mask:0xf bound_ctrl:1
	s_nop 0
	v_readlane_b32 s3, v4, 16
	v_readlane_b32 s26, v4, 48
	v_readlane_b32 s22, v4, 0
	v_readlane_b32 s23, v4, 32
	v_mov_b32_e32 v4, s3
	v_mov_b32_e32 v5, s26
	v_pk_add_f32 v[4:5], s[22:23], v[4:5]
	s_nop 0
	v_add_f32_e32 v4, v4, v5
	v_fmamk_f32 v4, v4, 0x3a000000, v151
	v_cmp_gt_f32_e32 vcc, s11, v4
	v_mul_f32_e32 v5, 0x4b800000, v4
	s_nop 0
	v_cndmask_b32_e32 v4, v4, v5, vcc
	v_rsq_f32_e32 v4, v4
	s_nop 0
	v_mul_f32_e32 v5, 0x45800000, v4
	v_cndmask_b32_e32 v6, v4, v5, vcc
	s_and_saveexec_b64 s[22:23], s[6:7]
	v_mov_b32_e32 v4, s10
	ds_write_b32 v4, v6 offset:60676
	s_or_b64 exec, exec, s[22:23]
	v_lshlrev_b32_e32 v4, 16, v24
	v_and_b32_e32 v5, 0xffff0000, v24
	v_lshlrev_b32_e32 v7, 16, v25
	v_and_b32_e32 v28, 0xffff0000, v25
	v_lshlrev_b32_e32 v29, 16, v26
	v_and_b32_e32 v30, 0xffff0000, v26
	v_lshlrev_b32_e32 v31, 16, v27
	v_and_b32_e32 v32, 0xffff0000, v27
	ds_read_b128 v[12:15], v144 offset:16384
	ds_read_b128 v[20:23], v144 offset:16400
	ds_read_b128 v[24:27], v144 offset:32768
	v_mul_f32_e32 v4, v6, v4
	v_mul_f32_e32 v5, v6, v5
	v_mul_f32_e32 v7, v6, v7
	s_lshl_b64 s[20:21], s[20:21], 11
	s_waitcnt lgkmcnt(0)
	v_fma_f32 v4, v4, v12, v24
	v_mul_f32_e32 v12, v6, v28
	v_fma_f32 v5, v5, v13, v25
	v_fma_f32 v7, v7, v14, v26
	v_fmac_f32_e32 v27, v12, v15
	ds_read_b128 v[12:15], v144 offset:32784
	v_mul_f32_e32 v24, v6, v29
	v_med3_f32 v4, v4, s12, v154
	v_med3_f32 v5, v5, s12, v154
	v_med3_f32 v7, v7, s12, v154
	s_waitcnt lgkmcnt(0)
	v_fma_f32 v20, v24, v20, v12
	v_mul_f32_e32 v12, v6, v30
	v_fma_f32 v13, v12, v21, v13
	v_mul_f32_e32 v12, v6, v31
	v_fma_f32 v14, v12, v22, v14
	v_mul_f32_e32 v12, v6, v32
	v_fmac_f32_e32 v15, v12, v23
	v_mov_b32_e32 v12, 0
	v_cvt_pk_fp8_f32 v12, v4, v5
	v_med3_f32 v4, v20, s12, v154
	v_med3_f32 v5, v13, s12, v154
	v_mov_b32_e32 v13, 0
	v_cvt_pk_fp8_f32 v13, v4, v5
	v_med3_f32 v21, v27, s12, v154
	v_cvt_pk_fp8_f32 v12, v7, v21 op_sel:[0,0,1]
	v_med3_f32 v7, v14, s12, v154
	v_med3_f32 v14, v15, s12, v154
	v_cvt_pk_fp8_f32 v13, v7, v14 op_sel:[0,0,1]
	v_lshl_add_u64 v[4:5], v[134:135], 0, s[20:21]
	v_lshlrev_b32_e32 v7, 16, v16
	v_and_b32_e32 v20, 0xffff0000, v16
	global_store_dwordx2 v[4:5], v[12:13], off
	v_lshlrev_b32_e32 v21, 16, v17
	v_and_b32_e32 v22, 0xffff0000, v17
	v_lshlrev_b32_e32 v23, 16, v18
	v_and_b32_e32 v24, 0xffff0000, v18
	v_lshlrev_b32_e32 v25, 16, v19
	v_and_b32_e32 v26, 0xffff0000, v19
	ds_read_b128 v[12:15], v144 offset:18432
	ds_read_b128 v[16:19], v144 offset:34816
	v_mul_f32_e32 v7, v6, v7
	s_waitcnt vmcnt(16)
	v_and_b32_e32 v44, 0xffff0000, v112
	v_lshlrev_b32_e32 v45, 16, v113
	v_lshlrev_b32_e32 v129, 16, v115
	s_waitcnt lgkmcnt(0)
	v_fma_f32 v7, v7, v12, v16
	v_mul_f32_e32 v12, v6, v20
	v_fma_f32 v16, v12, v13, v17
	v_mul_f32_e32 v12, v6, v21
	v_fma_f32 v17, v12, v14, v18
	v_mul_f32_e32 v12, v6, v22
	v_fmac_f32_e32 v19, v12, v15
	v_mul_f32_e32 v18, v6, v23
	ds_read_b128 v[12:15], v144 offset:18448
	ds_read_b128 v[20:23], v144 offset:34832
	v_med3_f32 v7, v7, s12, v154
	v_and_b32_e32 v115, 0xffff0000, v115
	s_waitcnt vmcnt(15)
	v_lshlrev_b32_e32 v157, 16, v104
	v_and_b32_e32 v104, 0xffff0000, v104
	s_waitcnt lgkmcnt(0)
	v_fma_f32 v18, v18, v12, v20
	v_mul_f32_e32 v12, v6, v24
	v_fma_f32 v13, v12, v13, v21
	v_mul_f32_e32 v12, v6, v25
	v_fma_f32 v14, v12, v14, v22
	v_mul_f32_e32 v12, v6, v26
	v_fmac_f32_e32 v23, v12, v15
	v_med3_f32 v15, v16, s12, v154
	v_mov_b32_e32 v12, 0
	v_cvt_pk_fp8_f32 v12, v7, v15
	v_med3_f32 v7, v18, s12, v154
	v_med3_f32 v15, v13, s12, v154
	v_mov_b32_e32 v13, 0
	v_cvt_pk_fp8_f32 v13, v7, v15
	v_med3_f32 v16, v17, s12, v154
	v_med3_f32 v17, v19, s12, v154
	v_cvt_pk_fp8_f32 v12, v16, v17 op_sel:[0,0,1]
	v_med3_f32 v14, v14, s12, v154
	v_med3_f32 v16, v23, s12, v154
	v_cvt_pk_fp8_f32 v13, v14, v16 op_sel:[0,0,1]
	v_lshlrev_b32_e32 v7, 16, v8
	v_and_b32_e32 v16, 0xffff0000, v8
	v_lshlrev_b32_e32 v17, 16, v9
	global_store_dwordx2 v[4:5], v[12:13], off offset:512
	v_and_b32_e32 v18, 0xffff0000, v9
	v_lshlrev_b32_e32 v19, 16, v10
	v_and_b32_e32 v20, 0xffff0000, v10
	v_lshlrev_b32_e32 v21, 16, v11
	v_and_b32_e32 v22, 0xffff0000, v11
	ds_read_b128 v[8:11], v144 offset:20480
	ds_read_b128 v[12:15], v144 offset:36864
	v_mul_f32_e32 v7, v6, v7
	v_lshlrev_b32_e32 v23, 16, v112
	v_and_b32_e32 v112, 0xffff0000, v113
	v_lshlrev_b32_e32 v113, 16, v114
	s_waitcnt lgkmcnt(0)
	v_fma_f32 v7, v7, v8, v12
	v_mul_f32_e32 v8, v6, v16
	v_fma_f32 v12, v8, v9, v13
	v_mul_f32_e32 v8, v6, v17
	v_fma_f32 v13, v8, v10, v14
	v_mul_f32_e32 v8, v6, v18
	v_fmac_f32_e32 v15, v8, v11
	v_mul_f32_e32 v14, v6, v19
	ds_read_b128 v[8:11], v144 offset:20496
	ds_read_b128 v[16:19], v144 offset:36880
	v_med3_f32 v7, v7, s12, v154
	v_and_b32_e32 v114, 0xffff0000, v114
	v_lshlrev_b32_e32 v158, 16, v105
	v_and_b32_e32 v105, 0xffff0000, v105
	s_waitcnt lgkmcnt(0)
	v_fma_f32 v14, v14, v8, v16
	v_mul_f32_e32 v8, v6, v20
	v_fma_f32 v9, v8, v9, v17
	v_mul_f32_e32 v8, v6, v21
	v_fma_f32 v10, v8, v10, v18
	v_mul_f32_e32 v8, v6, v22
	v_fmac_f32_e32 v19, v8, v11
	v_med3_f32 v11, v12, s12, v154
	v_mov_b32_e32 v8, 0
	v_cvt_pk_fp8_f32 v8, v7, v11
	v_med3_f32 v7, v14, s12, v154
	v_med3_f32 v11, v9, s12, v154
	v_mov_b32_e32 v9, 0
	v_cvt_pk_fp8_f32 v9, v7, v11
	v_med3_f32 v12, v13, s12, v154
	v_med3_f32 v13, v15, s12, v154
	v_cvt_pk_fp8_f32 v8, v12, v13 op_sel:[0,0,1]
	v_med3_f32 v10, v10, s12, v154
	v_med3_f32 v12, v19, s12, v154
	v_cvt_pk_fp8_f32 v9, v10, v12 op_sel:[0,0,1]
	v_lshlrev_b32_e32 v7, 16, v0
	v_and_b32_e32 v12, 0xffff0000, v0
	v_lshlrev_b32_e32 v13, 16, v1
	global_store_dwordx2 v[4:5], v[8:9], off offset:1024
	v_and_b32_e32 v14, 0xffff0000, v1
	v_lshlrev_b32_e32 v15, 16, v2
	v_and_b32_e32 v16, 0xffff0000, v2
	v_lshlrev_b32_e32 v17, 16, v3
	v_and_b32_e32 v18, 0xffff0000, v3
	ds_read_b128 v[0:3], v144 offset:22528
	ds_read_b128 v[8:11], v144 offset:38912
	v_mul_f32_e32 v7, v6, v7
	v_lshlrev_b32_e32 v159, 16, v106
	v_and_b32_e32 v106, 0xffff0000, v106
	v_lshlrev_b32_e32 v160, 16, v107
	s_waitcnt lgkmcnt(0)
	v_fma_f32 v7, v7, v0, v8
	v_mul_f32_e32 v0, v6, v12
	v_fma_f32 v8, v0, v1, v9
	v_mul_f32_e32 v0, v6, v13
	v_fma_f32 v9, v0, v2, v10
	v_mul_f32_e32 v0, v6, v14
	v_fmac_f32_e32 v11, v0, v3
	v_mul_f32_e32 v10, v6, v15
	ds_read_b128 v[0:3], v144 offset:22544
	ds_read_b128 v[12:15], v144 offset:38928
	v_and_b32_e32 v107, 0xffff0000, v107
	s_waitcnt vmcnt(16)
	v_lshlrev_b32_e32 v161, 16, v96
	v_and_b32_e32 v96, 0xffff0000, v96
	v_lshlrev_b32_e32 v162, 16, v97
	s_waitcnt lgkmcnt(0)
	v_fma_f32 v10, v10, v0, v12
	v_mul_f32_e32 v0, v6, v16
	v_fma_f32 v1, v0, v1, v13
	v_mul_f32_e32 v0, v6, v17
	v_fma_f32 v2, v0, v2, v14
	v_mul_f32_e32 v0, v6, v18
	v_fmac_f32_e32 v15, v0, v3
	v_med3_f32 v3, v7, s12, v154
	v_med3_f32 v6, v8, s12, v154
	v_mov_b32_e32 v0, 0
	v_cvt_pk_fp8_f32 v0, v3, v6
	v_med3_f32 v3, v10, s12, v154
	v_med3_f32 v6, v1, s12, v154
	v_mov_b32_e32 v1, 0
	v_cvt_pk_fp8_f32 v1, v3, v6
	v_mul_f32_e32 v6, v44, v44
	v_fmac_f32_e32 v6, v23, v23
	v_fmac_f32_e32 v6, v45, v45
	v_fmac_f32_e32 v6, v112, v112
	v_fmac_f32_e32 v6, v113, v113
	v_fmac_f32_e32 v6, v114, v114
	v_fmac_f32_e32 v6, v129, v129
	v_fmac_f32_e32 v6, v115, v115
	v_fmac_f32_e32 v6, v157, v157
	v_fmac_f32_e32 v6, v104, v104
	v_fmac_f32_e32 v6, v158, v158
	v_fmac_f32_e32 v6, v105, v105
	v_fmac_f32_e32 v6, v159, v159
	v_fmac_f32_e32 v6, v106, v106
	v_fmac_f32_e32 v6, v160, v160
	v_fmac_f32_e32 v6, v107, v107
	v_fmac_f32_e32 v6, v161, v161
	v_fmac_f32_e32 v6, v96, v96
	v_and_b32_e32 v97, 0xffff0000, v97
	v_fmac_f32_e32 v6, v162, v162
	v_med3_f32 v7, v9, s12, v154
	v_med3_f32 v8, v11, s12, v154
	v_lshlrev_b32_e32 v163, 16, v98
	v_fmac_f32_e32 v6, v97, v97
	v_cvt_pk_fp8_f32 v0, v7, v8 op_sel:[0,0,1]
	v_med3_f32 v2, v2, s12, v154
	v_med3_f32 v7, v15, s12, v154
	v_and_b32_e32 v22, 0xffff0000, v98
	v_fmac_f32_e32 v6, v163, v163
	v_cvt_pk_fp8_f32 v1, v2, v7 op_sel:[0,0,1]
	v_lshlrev_b32_e32 v21, 16, v99
	v_fmac_f32_e32 v6, v22, v22
	v_and_b32_e32 v20, 0xffff0000, v99
	v_fmac_f32_e32 v6, v21, v21
	v_fmac_f32_e32 v6, v20, v20
	s_waitcnt vmcnt(15)
	v_lshlrev_b32_e32 v46, 16, v88
	v_and_b32_e32 v31, 0xffff0000, v88
	v_fmac_f32_e32 v6, v46, v46
	v_and_b32_e32 v36, 0xffff0000, v89
	v_lshlrev_b32_e32 v37, 16, v89
	global_store_dwordx2 v[4:5], v[0:1], off offset:1536
	v_fmac_f32_e32 v6, v31, v31
	v_pk_mul_f32 v[4:5], v[36:37], v[36:37]
	v_and_b32_e32 v38, 0xffff0000, v90
	v_add_f32_e32 v5, v5, v6
	v_lshlrev_b32_e32 v39, 16, v90
	v_add_f32_e32 v6, v4, v5
	v_pk_mul_f32 v[4:5], v[38:39], v[38:39]
	v_and_b32_e32 v28, 0xffff0000, v91
	v_add_f32_e32 v5, v5, v6
	v_lshlrev_b32_e32 v29, 16, v91
	v_add_f32_e32 v6, v4, v5
	v_pk_mul_f32 v[4:5], v[28:29], v[28:29]
	s_or_b32 s20, s0, 3
	v_add_f32_e32 v5, v5, v6
	v_add_f32_e32 v4, v4, v5
	s_mov_b32 s21, s1
	s_lshl_b64 s[26:27], s[20:21], 12
	v_add_f32_dpp v4, v4, v4 quad_perm:[1,0,3,2] row_mask:0xf bank_mask:0xf bound_ctrl:1
	s_lshl_b64 s[22:23], s[20:21], 13
	v_readlane_b32 s36, v253, 10
	v_add_f32_dpp v4, v4, v4 quad_perm:[2,3,0,1] row_mask:0xf bank_mask:0xf bound_ctrl:1
	v_readlane_b32 s37, v253, 11
	s_add_u32 s22, s36, s22
	v_add_f32_dpp v4, v4, v4 row_ror:4 row_mask:0xf bank_mask:0xf bound_ctrl:1
	v_lshl_add_u64 v[0:1], v[130:131], 0, s[26:27]
	s_addc_u32 s23, s37, s23
	v_add_f32_dpp v4, v4, v4 row_ror:8 row_mask:0xf bank_mask:0xf bound_ctrl:1
	global_load_dwordx4 v[116:119], v[0:1], off
	global_load_dwordx4 v[108:111], v[0:1], off offset:1024
	global_load_dwordx4 v[100:103], v[0:1], off offset:2048
	global_load_dwordx4 v[92:95], v[0:1], off offset:3072
	v_readlane_b32 s3, v4, 16
	v_readlane_b32 s28, v4, 48
	global_load_dwordx4 v[76:79], v122, s[22:23] offset:16
	global_load_dwordx4 v[84:87], v122, s[22:23]
	global_load_dwordx4 v[32:35], v122, s[22:23] offset:2064
	global_load_dwordx4 v[40:43], v122, s[22:23] offset:2048
	global_load_dwordx4 v[16:19], v149, s[22:23] offset:16
	global_load_dwordx4 v[24:27], v149, s[22:23]
	global_load_dwordx4 v[0:3], v150, s[22:23] offset:16
	global_load_dwordx4 v[8:11], v150, s[22:23]
	v_readlane_b32 s22, v4, 0
	v_readlane_b32 s23, v4, 32
	v_mov_b32_e32 v4, s3
	v_mov_b32_e32 v5, s28
	v_pk_add_f32 v[4:5], s[22:23], v[4:5]
	v_readlane_b32 s38, v253, 12
	v_add_f32_e32 v4, v4, v5
	v_fmamk_f32 v4, v4, 0x3a000000, v151
	v_cmp_gt_f32_e32 vcc, s11, v4
	v_mul_f32_e32 v5, 0x4b800000, v4
	v_readlane_b32 s39, v253, 13
	v_cndmask_b32_e32 v4, v4, v5, vcc
	v_rsq_f32_e32 v4, v4
	v_readlane_b32 s40, v253, 14
	v_readlane_b32 s41, v253, 15
	v_readlane_b32 s42, v253, 16
	v_mul_f32_e32 v5, 0x45800000, v4
	v_cndmask_b32_e32 v30, v4, v5, vcc
	ds_read_b128 v[4:7], v144
	ds_read_b128 v[12:15], v144 offset:16
	ds_read_b128 v[88:91], v144 offset:8192
	v_mul_f32_e32 v23, v30, v23
	v_mul_f32_e32 v22, v30, v22
	v_mul_f32_e32 v21, v30, v21
	v_mul_f32_e32 v20, v30, v20
	s_waitcnt lgkmcnt(0)
	v_mul_f32_e32 v23, v88, v23
	s_waitcnt vmcnt(26)
	v_fma_f32 v23, v4, v23, v80
	v_mul_f32_e32 v4, v30, v44
	v_mul_f32_e32 v4, v89, v4
	v_fma_f32 v44, v5, v4, v81
	v_mul_f32_e32 v4, v30, v45
	v_mul_f32_e32 v4, v90, v4
	v_fma_f32 v45, v6, v4, v82
	v_mul_f32_e32 v4, v30, v112
	v_mul_f32_e32 v4, v91, v4
	v_fmac_f32_e32 v83, v7, v4
	ds_read_b128 v[4:7], v144 offset:8208
	v_mul_f32_e32 v80, v30, v113
	v_mul_f32_e32 v47, v44, v44
	v_fmac_f32_e32 v47, v23, v23
	v_fmac_f32_e32 v47, v45, v45
	s_waitcnt lgkmcnt(0)
	v_mul_f32_e32 v4, v80, v4
	v_fma_f32 v12, v12, v4, v72
	v_mul_f32_e32 v4, v30, v114
	v_mul_f32_e32 v4, v4, v5
	v_fma_f32 v13, v13, v4, v73
	v_mul_f32_e32 v4, v30, v129
	v_mul_f32_e32 v4, v4, v6
	v_fmac_f32_e32 v47, v83, v83
	v_fma_f32 v14, v14, v4, v74
	v_mul_f32_e32 v4, v30, v115
	v_fmac_f32_e32 v47, v12, v12
	v_mul_f32_e32 v4, v4, v7
	v_fmac_f32_e32 v47, v13, v13
	v_fmac_f32_e32 v75, v15, v4
	v_cvt_pk_bf16_f32 v4, v23, v44
	v_cvt_pk_bf16_f32 v5, v45, v83
	v_lshl_add_u64 v[44:45], v[132:133], 0, s[8:9]
	v_fmac_f32_e32 v47, v14, v14
	v_cvt_pk_bf16_f32 v6, v12, v13
	v_cvt_pk_bf16_f32 v7, v14, v75
	global_store_dwordx4 v[44:45], v[4:7], off
	v_fmac_f32_e32 v47, v75, v75
	ds_read_b128 v[12:15], v144 offset:2048
	ds_read_b128 v[72:75], v144 offset:2064
	ds_read_b128 v[80:83], v144 offset:10240
	v_mul_f32_e32 v23, v30, v157
	v_mul_f32_e32 v31, v30, v31
	v_mul_f32_e32 v46, v30, v46
	v_readlane_b32 s43, v253, 17
	s_waitcnt lgkmcnt(0)
	v_mul_f32_e32 v23, v23, v80
	s_waitcnt vmcnt(25)
	v_fma_f32 v23, v12, v23, v68
	v_mul_f32_e32 v12, v30, v104
	v_mul_f32_e32 v12, v12, v81
	v_fma_f32 v68, v13, v12, v69
	v_mul_f32_e32 v12, v30, v158
	v_mul_f32_e32 v12, v12, v82
	v_fma_f32 v69, v14, v12, v70
	v_mul_f32_e32 v12, v30, v105
	v_mul_f32_e32 v12, v12, v83
	v_fmac_f32_e32 v71, v15, v12
	ds_read_b128 v[12:15], v144 offset:10256
	v_mul_f32_e32 v70, v30, v159
	v_fmac_f32_e32 v47, v23, v23
	v_fmac_f32_e32 v47, v68, v68
	v_fmac_f32_e32 v47, v69, v69
	s_waitcnt lgkmcnt(0)
	v_mul_f32_e32 v12, v70, v12
	v_fma_f32 v64, v72, v12, v64
	v_mul_f32_e32 v12, v30, v106
	v_mul_f32_e32 v12, v12, v13
	v_fma_f32 v65, v73, v12, v65
	v_mul_f32_e32 v12, v30, v160
	v_fmac_f32_e32 v47, v71, v71
	v_mul_f32_e32 v12, v12, v14
	v_fmac_f32_e32 v47, v64, v64
	v_fma_f32 v66, v74, v12, v66
	v_mul_f32_e32 v12, v30, v107
	v_fmac_f32_e32 v47, v65, v65
	v_mul_f32_e32 v12, v12, v15
	v_fmac_f32_e32 v47, v66, v66
	v_fmac_f32_e32 v67, v75, v12
	v_cvt_pk_bf16_f32 v12, v23, v68
	v_cvt_pk_bf16_f32 v13, v69, v71
	v_cvt_pk_bf16_f32 v14, v64, v65
	v_cvt_pk_bf16_f32 v15, v66, v67
	global_store_dwordx4 v[44:45], v[12:15], off offset:1024
	v_fmac_f32_e32 v47, v67, v67
	ds_read_b128 v[64:67], v144 offset:4096
	ds_read_b128 v[68:71], v144 offset:4112
	ds_read_b128 v[72:75], v144 offset:12288
	v_mul_f32_e32 v23, v30, v161
	v_readlane_b32 s44, v253, 18
	v_readlane_b32 s45, v253, 19
	v_readlane_b32 s46, v253, 20
	s_waitcnt lgkmcnt(0)
	v_mul_f32_e32 v23, v23, v72
	s_waitcnt vmcnt(24)
	v_fma_f32 v23, v64, v23, v60
	v_mul_f32_e32 v60, v30, v96
	v_mul_f32_e32 v60, v60, v73
	v_fma_f32 v60, v65, v60, v61
	v_mul_f32_e32 v61, v30, v162
	v_mul_f32_e32 v61, v61, v74
	v_fma_f32 v61, v66, v61, v62
	v_mul_f32_e32 v62, v30, v97
	v_mul_f32_e32 v62, v62, v75
	v_fmac_f32_e32 v63, v67, v62
	ds_read_b128 v[64:67], v144 offset:12304
	v_fmac_f32_e32 v47, v23, v23
	v_fmac_f32_e32 v47, v60, v60
	v_mul_f32_e32 v62, v30, v163
	v_fmac_f32_e32 v47, v61, v61
	s_waitcnt lgkmcnt(0)
	v_mul_f32_e32 v62, v62, v64
	v_fmac_f32_e32 v47, v63, v63
	v_fma_f32 v56, v68, v62, v56
	v_mul_f32_e32 v22, v22, v65
	v_fmac_f32_e32 v47, v56, v56
	v_fma_f32 v22, v69, v22, v57
	v_mul_f32_e32 v21, v21, v66
	v_fmac_f32_e32 v47, v22, v22
	v_fma_f32 v57, v70, v21, v58
	v_mul_f32_e32 v20, v20, v67
	v_fmac_f32_e32 v47, v57, v57
	v_fmac_f32_e32 v59, v71, v20
	v_cvt_pk_bf16_f32 v20, v23, v60
	v_cvt_pk_bf16_f32 v21, v61, v63
	v_cvt_pk_bf16_f32 v22, v56, v22
	v_cvt_pk_bf16_f32 v23, v57, v59
	global_store_dwordx4 v[44:45], v[20:23], off offset:2048
	v_fmac_f32_e32 v47, v59, v59
	ds_read_b128 v[56:59], v144 offset:6144
	ds_read_b128 v[60:63], v144 offset:6160
	ds_read_b128 v[64:67], v144 offset:14336
	v_readlane_b32 s47, v253, 21
	v_readlane_b32 s48, v253, 22
	v_readlane_b32 s49, v253, 23
	v_readlane_b32 s50, v253, 24
	s_waitcnt lgkmcnt(0)
	v_mul_f32_e32 v31, v31, v65
	s_waitcnt vmcnt(23)
	v_fma_f32 v31, v57, v31, v53
	v_mul_f32_e32 v46, v46, v64
	v_pk_mul_f32 v[36:37], v[30:31], v[36:37] op_sel_hi:[0,1]
	v_fma_f32 v56, v56, v46, v52
	v_pk_mul_f32 v[36:37], v[36:37], v[66:67] op_sel:[1,0] op_sel_hi:[0,1]
	v_fmac_f32_e32 v47, v56, v56
	v_pk_fma_f32 v[52:53], v[58:59], v[36:37], v[54:55]
	v_fmac_f32_e32 v47, v31, v31
	v_pk_mul_f32 v[36:37], v[52:53], v[52:53]
	v_pk_mul_f32 v[28:29], v[30:31], v[28:29] op_sel_hi:[0,1]
	v_add_f32_e32 v36, v47, v36
	v_add_f32_e32 v54, v36, v37
	v_pk_mul_f32 v[46:47], v[30:31], v[38:39] op_sel_hi:[0,1]
	ds_read_b128 v[36:39], v144 offset:14352
	v_readlane_b32 s51, v253, 25
	s_waitcnt lgkmcnt(0)
	v_pk_mul_f32 v[36:37], v[46:47], v[36:37] op_sel:[1,0] op_sel_hi:[0,1]
	v_pk_fma_f32 v[36:37], v[60:61], v[36:37], v[48:49]
	v_pk_mul_f32 v[28:29], v[28:29], v[38:39] op_sel:[1,0] op_sel_hi:[0,1]
	v_pk_mul_f32 v[46:47], v[36:37], v[36:37]
	v_pk_fma_f32 v[38:39], v[62:63], v[28:29], v[50:51]
	v_add_f32_e32 v46, v54, v46
	v_add_f32_e32 v46, v46, v47
	v_pk_mul_f32 v[28:29], v[38:39], v[38:39]
	s_nop 0
	v_add_f32_e32 v28, v46, v28
	v_add_f32_e32 v46, v28, v29
	v_cvt_pk_bf16_f32 v28, v56, v31
	v_cvt_pk_bf16_f32 v29, v52, v53
	v_cvt_pk_bf16_f32 v30, v36, v37
	v_cvt_pk_bf16_f32 v31, v38, v39
	global_store_dwordx4 v[44:45], v[28:31], off offset:3072
	s_nop 0
	v_add_f32_dpp v36, v46, v46 quad_perm:[1,0,3,2] row_mask:0xf bank_mask:0xf bound_ctrl:1
	s_nop 1
	v_add_f32_dpp v36, v36, v36 quad_perm:[2,3,0,1] row_mask:0xf bank_mask:0xf bound_ctrl:1
	s_nop 1
	v_add_f32_dpp v36, v36, v36 row_ror:4 row_mask:0xf bank_mask:0xf bound_ctrl:1
	s_nop 1
	v_add_f32_dpp v36, v36, v36 row_ror:8 row_mask:0xf bank_mask:0xf bound_ctrl:1
	s_nop 0
	v_readlane_b32 s3, v36, 16
	v_readlane_b32 s22, v36, 48
	v_readlane_b32 s8, v36, 0
	v_readlane_b32 s9, v36, 32
	v_mov_b32_e32 v36, s3
	v_mov_b32_e32 v37, s22
	v_pk_add_f32 v[36:37], s[8:9], v[36:37]
	s_nop 0
	v_add_f32_e32 v36, v36, v37
	v_fmamk_f32 v36, v36, 0x3a000000, v151
	v_cmp_gt_f32_e32 vcc, s11, v36
	v_mul_f32_e32 v37, 0x4b800000, v36
	s_nop 0
	v_cndmask_b32_e32 v36, v36, v37, vcc
	v_rsq_f32_e32 v36, v36
	s_nop 0
	v_mul_f32_e32 v37, 0x45800000, v36
	v_cndmask_b32_e32 v36, v36, v37, vcc
	s_and_saveexec_b64 s[8:9], s[6:7]
	v_mov_b32_e32 v37, s10
	ds_write_b32 v37, v36 offset:60680
	s_or_b64 exec, exec, s[8:9]
	v_lshlrev_b32_e32 v37, 16, v4
	v_and_b32_e32 v38, 0xffff0000, v4
	v_lshlrev_b32_e32 v39, 16, v5
	v_and_b32_e32 v52, 0xffff0000, v5
	v_lshlrev_b32_e32 v53, 16, v6
	v_and_b32_e32 v54, 0xffff0000, v6
	v_lshlrev_b32_e32 v55, 16, v7
	v_and_b32_e32 v56, 0xffff0000, v7
	ds_read_b128 v[4:7], v144 offset:16384
	ds_read_b128 v[44:47], v144 offset:16400
	ds_read_b128 v[48:51], v144 offset:32768
	v_mul_f32_e32 v37, v36, v37
	s_lshl_b64 s[8:9], s[24:25], 11
	s_waitcnt vmcnt(15)
	v_and_b32_e32 v105, 0xffff0000, v116
	v_lshlrev_b32_e32 v104, 16, v116
	s_waitcnt lgkmcnt(0)
	v_fma_f32 v37, v37, v4, v48
	v_mul_f32_e32 v4, v36, v38
	v_fma_f32 v38, v4, v5, v49
	v_mul_f32_e32 v4, v36, v39
	v_fma_f32 v39, v4, v6, v50
	v_mul_f32_e32 v4, v36, v52
	v_fmac_f32_e32 v51, v4, v7
	ds_read_b128 v[4:7], v144 offset:32784
	v_mul_f32_e32 v48, v36, v53
	v_med3_f32 v37, v37, s12, v154
	v_med3_f32 v38, v38, s12, v154
	v_med3_f32 v39, v39, s12, v154
	s_waitcnt lgkmcnt(0)
	v_fma_f32 v4, v48, v44, v4
	v_mul_f32_e32 v44, v36, v54
	v_fma_f32 v5, v44, v45, v5
	v_mul_f32_e32 v44, v36, v55
	v_fma_f32 v44, v44, v46, v6
	v_mul_f32_e32 v6, v36, v56
	v_fmac_f32_e32 v7, v6, v47
	v_mov_b32_e32 v6, 0
	v_cvt_pk_fp8_f32 v6, v37, v38
	v_med3_f32 v4, v4, s12, v154
	v_med3_f32 v5, v5, s12, v154
	v_med3_f32 v38, v7, s12, v154
	v_mov_b32_e32 v7, 0
	v_cvt_pk_fp8_f32 v7, v4, v5
	v_med3_f32 v45, v51, s12, v154
	v_med3_f32 v37, v44, s12, v154
	v_cvt_pk_fp8_f32 v6, v39, v45 op_sel:[0,0,1]
	v_cvt_pk_fp8_f32 v7, v37, v38 op_sel:[0,0,1]
	v_lshl_add_u64 v[4:5], v[134:135], 0, s[8:9]
	v_lshlrev_b32_e32 v37, 16, v13
	v_and_b32_e32 v38, 0xffff0000, v13
	global_store_dwordx2 v[4:5], v[6:7], off
	v_lshlrev_b32_e32 v6, 16, v12
	v_and_b32_e32 v7, 0xffff0000, v12
	v_lshlrev_b32_e32 v39, 16, v14
	v_and_b32_e32 v52, 0xffff0000, v14
	v_lshlrev_b32_e32 v53, 16, v15
	v_and_b32_e32 v54, 0xffff0000, v15
	ds_read_b128 v[12:15], v144 offset:18432
	ds_read_b128 v[44:47], v144 offset:34816
	v_mul_f32_e32 v6, v36, v6
	v_mul_f32_e32 v7, v36, v7
	v_lshlrev_b32_e32 v106, 16, v117
	v_and_b32_e32 v107, 0xffff0000, v117
	s_waitcnt lgkmcnt(0)
	v_fma_f32 v6, v6, v12, v44
	v_mul_f32_e32 v12, v36, v37
	v_fma_f32 v37, v12, v14, v46
	v_mul_f32_e32 v12, v36, v38
	v_fma_f32 v7, v7, v13, v45
	v_fmac_f32_e32 v47, v12, v15
	ds_read_b128 v[12:15], v144 offset:18448
	ds_read_b128 v[48:51], v144 offset:34832
	v_mul_f32_e32 v38, v36, v39
	v_med3_f32 v7, v7, s12, v154
	v_med3_f32 v37, v37, s12, v154
	v_lshlrev_b32_e32 v39, 16, v22
	s_waitcnt lgkmcnt(0)
	v_fma_f32 v12, v38, v12, v48
	v_mul_f32_e32 v38, v36, v52
	v_fma_f32 v13, v38, v13, v49
	v_mul_f32_e32 v38, v36, v53
	v_fma_f32 v14, v38, v14, v50
	v_mul_f32_e32 v38, v36, v54
	v_fmac_f32_e32 v51, v38, v15
	v_med3_f32 v15, v6, s12, v154
	v_mov_b32_e32 v6, 0
	v_cvt_pk_fp8_f32 v6, v15, v7
	v_med3_f32 v12, v12, s12, v154
	v_med3_f32 v13, v13, s12, v154
	v_mov_b32_e32 v7, 0
	v_cvt_pk_fp8_f32 v7, v12, v13
	v_med3_f32 v38, v47, s12, v154
	v_med3_f32 v14, v14, s12, v154
	v_med3_f32 v15, v51, s12, v154
	v_cvt_pk_fp8_f32 v6, v37, v38 op_sel:[0,0,1]
	v_cvt_pk_fp8_f32 v7, v14, v15 op_sel:[0,0,1]
	v_lshlrev_b32_e32 v37, 16, v21
	v_and_b32_e32 v38, 0xffff0000, v21
	v_and_b32_e32 v48, 0xffff0000, v22
	global_store_dwordx2 v[4:5], v[6:7], off offset:512
	v_lshlrev_b32_e32 v6, 16, v20
	v_and_b32_e32 v7, 0xffff0000, v20
	v_lshlrev_b32_e32 v49, 16, v23
	v_and_b32_e32 v50, 0xffff0000, v23
	ds_read_b128 v[12:15], v144 offset:20480
	ds_read_b128 v[20:23], v144 offset:36864
	v_mul_f32_e32 v6, v36, v6
	v_mul_f32_e32 v7, v36, v7
	v_mul_f32_e32 v54, v105, v105
	v_fmac_f32_e32 v54, v104, v104
	s_waitcnt lgkmcnt(0)
	v_fma_f32 v6, v6, v12, v20
	v_mul_f32_e32 v12, v36, v37
	v_fma_f32 v20, v12, v14, v22
	v_mul_f32_e32 v12, v36, v38
	v_fma_f32 v7, v7, v13, v21
	v_fmac_f32_e32 v23, v12, v15
	ds_read_b128 v[12:15], v144 offset:20496
	ds_read_b128 v[44:47], v144 offset:36880
	v_mul_f32_e32 v21, v36, v39
	v_med3_f32 v7, v7, s12, v154
	v_fmac_f32_e32 v54, v106, v106
	v_lshlrev_b32_e32 v112, 16, v118
	s_waitcnt lgkmcnt(0)
	v_fma_f32 v12, v21, v12, v44
	v_mul_f32_e32 v21, v36, v48
	v_fma_f32 v13, v21, v13, v45
	v_mul_f32_e32 v21, v36, v49
	v_fma_f32 v14, v21, v14, v46
	v_mul_f32_e32 v21, v36, v50
	v_fmac_f32_e32 v47, v21, v15
	v_med3_f32 v15, v6, s12, v154
	v_mov_b32_e32 v6, 0
	v_cvt_pk_fp8_f32 v6, v15, v7
	v_med3_f32 v12, v12, s12, v154
	v_med3_f32 v13, v13, s12, v154
	v_mov_b32_e32 v7, 0
	v_cvt_pk_fp8_f32 v7, v12, v13
	v_fmac_f32_e32 v54, v107, v107
	v_and_b32_e32 v113, 0xffff0000, v118
	v_fmac_f32_e32 v54, v112, v112
	v_med3_f32 v20, v20, s12, v154
	v_med3_f32 v21, v23, s12, v154
	v_med3_f32 v14, v14, s12, v154
	v_med3_f32 v15, v47, s12, v154
	v_lshlrev_b32_e32 v114, 16, v119
	v_fmac_f32_e32 v54, v113, v113
	v_cvt_pk_fp8_f32 v6, v20, v21 op_sel:[0,0,1]
	v_cvt_pk_fp8_f32 v7, v14, v15 op_sel:[0,0,1]
	v_and_b32_e32 v115, 0xffff0000, v119
	v_fmac_f32_e32 v54, v114, v114
	v_fmac_f32_e32 v54, v115, v115
	s_waitcnt vmcnt(16)
	v_lshlrev_b32_e32 v116, 16, v108
	v_and_b32_e32 v108, 0xffff0000, v108
	v_fmac_f32_e32 v54, v116, v116
	v_lshlrev_b32_e32 v117, 16, v109
	v_fmac_f32_e32 v54, v108, v108
	global_store_dwordx2 v[4:5], v[6:7], off offset:1024
	v_and_b32_e32 v109, 0xffff0000, v109
	v_fmac_f32_e32 v54, v117, v117
	ds_read_b128 v[12:15], v144 offset:22528
	ds_read_b128 v[20:23], v144 offset:38912
	v_lshlrev_b32_e32 v118, 16, v110
	v_fmac_f32_e32 v54, v109, v109
	v_and_b32_e32 v110, 0xffff0000, v110
	v_fmac_f32_e32 v54, v118, v118
	v_lshlrev_b32_e32 v119, 16, v111
	v_fmac_f32_e32 v54, v110, v110
	v_lshlrev_b32_e32 v6, 16, v28
	v_and_b32_e32 v111, 0xffff0000, v111
	v_fmac_f32_e32 v54, v119, v119
	v_and_b32_e32 v7, 0xffff0000, v28
	v_lshlrev_b32_e32 v28, 16, v29
	v_mul_f32_e32 v6, v36, v6
	v_fmac_f32_e32 v54, v111, v111
	s_waitcnt vmcnt(16)
	v_lshlrev_b32_e32 v129, 16, v100
	v_and_b32_e32 v29, 0xffff0000, v29
	s_waitcnt lgkmcnt(0)
	v_fma_f32 v6, v6, v12, v20
	v_mul_f32_e32 v12, v36, v28
	v_and_b32_e32 v157, 0xffff0000, v100
	v_fmac_f32_e32 v54, v129, v129
	v_mul_f32_e32 v7, v36, v7
	v_fma_f32 v20, v12, v14, v22
	v_mul_f32_e32 v12, v36, v29
	v_lshlrev_b32_e32 v158, 16, v101
	v_fmac_f32_e32 v54, v157, v157
	v_lshlrev_b32_e32 v37, 16, v30
	v_and_b32_e32 v38, 0xffff0000, v30
	v_lshlrev_b32_e32 v39, 16, v31
	v_and_b32_e32 v44, 0xffff0000, v31
	v_fma_f32 v7, v7, v13, v21
	v_fmac_f32_e32 v23, v12, v15
	ds_read_b128 v[12:15], v144 offset:22544
	ds_read_b128 v[28:31], v144 offset:38928
	v_and_b32_e32 v159, 0xffff0000, v101
	v_fmac_f32_e32 v54, v158, v158
	v_lshlrev_b32_e32 v160, 16, v102
	v_fmac_f32_e32 v54, v159, v159
	v_and_b32_e32 v99, 0xffff0000, v102
	v_fmac_f32_e32 v54, v160, v160
	v_lshlrev_b32_e32 v97, 16, v103
	v_fmac_f32_e32 v54, v99, v99
	v_mul_f32_e32 v21, v36, v37
	v_and_b32_e32 v96, 0xffff0000, v103
	v_fmac_f32_e32 v54, v97, v97
	s_waitcnt lgkmcnt(0)
	v_fma_f32 v12, v21, v12, v28
	v_mul_f32_e32 v21, v36, v38
	v_fmac_f32_e32 v54, v96, v96
	s_waitcnt vmcnt(15)
	v_lshlrev_b32_e32 v98, 16, v92
	v_fma_f32 v13, v21, v13, v29
	v_mul_f32_e32 v21, v36, v39
	v_and_b32_e32 v63, 0xffff0000, v92
	v_fmac_f32_e32 v54, v98, v98
	v_and_b32_e32 v68, 0xffff0000, v93
	v_lshlrev_b32_e32 v69, 16, v93
	v_fma_f32 v14, v21, v14, v30
	v_mul_f32_e32 v21, v36, v44
	v_fmac_f32_e32 v54, v63, v63
	v_pk_mul_f32 v[52:53], v[68:69], v[68:69]
	v_fmac_f32_e32 v31, v21, v15
	v_med3_f32 v15, v6, s12, v154
	v_med3_f32 v7, v7, s12, v154
	v_mov_b32_e32 v6, 0
	v_add_f32_e32 v53, v53, v54
	v_and_b32_e32 v70, 0xffff0000, v94
	v_lshlrev_b32_e32 v71, 16, v94
	v_cvt_pk_fp8_f32 v6, v15, v7
	v_med3_f32 v12, v12, s12, v154
	v_med3_f32 v13, v13, s12, v154
	v_mov_b32_e32 v7, 0
	v_add_f32_e32 v54, v52, v53
	v_pk_mul_f32 v[52:53], v[70:71], v[70:71]
	v_cvt_pk_fp8_f32 v7, v12, v13
	v_add_f32_e32 v53, v53, v54
	v_and_b32_e32 v60, 0xffff0000, v95
	v_lshlrev_b32_e32 v61, 16, v95
	v_add_f32_e32 v54, v52, v53
	v_pk_mul_f32 v[52:53], v[60:61], v[60:61]
	v_med3_f32 v20, v20, s12, v154
	v_add_f32_e32 v53, v53, v54
	v_med3_f32 v21, v23, s12, v154
	v_med3_f32 v14, v14, s12, v154
	v_med3_f32 v15, v31, s12, v154
	v_add_f32_e32 v52, v52, v53
	v_cvt_pk_fp8_f32 v6, v20, v21 op_sel:[0,0,1]
	v_cvt_pk_fp8_f32 v7, v14, v15 op_sel:[0,0,1]
	v_add_f32_dpp v52, v52, v52 quad_perm:[1,0,3,2] row_mask:0xf bank_mask:0xf bound_ctrl:1
	s_or_b32 s22, s0, 4
	s_mov_b32 s23, s1
	v_add_f32_dpp v52, v52, v52 quad_perm:[2,3,0,1] row_mask:0xf bank_mask:0xf bound_ctrl:1
	s_lshl_b64 s[8:9], s[22:23], 12
	s_lshl_b64 s[24:25], s[22:23], 13
	v_readlane_b32 s36, v253, 10
	v_add_f32_dpp v52, v52, v52 row_ror:4 row_mask:0xf bank_mask:0xf bound_ctrl:1
	v_readlane_b32 s37, v253, 11
	s_add_u32 s24, s36, s24
	v_add_f32_dpp v52, v52, v52 row_ror:8 row_mask:0xf bank_mask:0xf bound_ctrl:1
	global_store_dwordx2 v[4:5], v[6:7], off offset:1536
	v_lshl_add_u64 v[4:5], v[130:131], 0, s[8:9]
	s_addc_u32 s25, s37, s25
	v_readlane_b32 s3, v52, 16
	v_readlane_b32 s28, v52, 48
	global_load_dwordx4 v[88:91], v[4:5], off
	global_load_dwordx4 v[80:83], v[4:5], off offset:1024
	global_load_dwordx4 v[72:75], v[4:5], off offset:2048
	global_load_dwordx4 v[64:67], v[4:5], off offset:3072
	global_load_dwordx4 v[48:51], v122, s[24:25] offset:16
	global_load_dwordx4 v[56:59], v122, s[24:25]
	global_load_dwordx4 v[36:39], v122, s[24:25] offset:2064
	global_load_dwordx4 v[44:47], v122, s[24:25] offset:2048
	global_load_dwordx4 v[20:23], v149, s[24:25] offset:16
	global_load_dwordx4 v[28:31], v149, s[24:25]
	global_load_dwordx4 v[4:7], v150, s[24:25] offset:16
	global_load_dwordx4 v[12:15], v150, s[24:25]
	v_readlane_b32 s24, v52, 0
	v_readlane_b32 s25, v52, 32
	v_mov_b32_e32 v52, s3
	v_mov_b32_e32 v53, s28
	v_pk_add_f32 v[52:53], s[24:25], v[52:53]
	v_readlane_b32 s38, v253, 12
	v_add_f32_e32 v52, v52, v53
	v_fmamk_f32 v52, v52, 0x3a000000, v151
	v_cmp_gt_f32_e32 vcc, s11, v52
	v_mul_f32_e32 v53, 0x4b800000, v52
	v_readlane_b32 s39, v253, 13
	v_cndmask_b32_e32 v52, v52, v53, vcc
	v_rsq_f32_e32 v52, v52
	v_readlane_b32 s40, v253, 14
	v_readlane_b32 s41, v253, 15
	v_readlane_b32 s42, v253, 16
	v_mul_f32_e32 v53, 0x45800000, v52
	v_cndmask_b32_e32 v62, v52, v53, vcc
	ds_read_b128 v[52:55], v144
	ds_read_b128 v[92:95], v144 offset:16
	ds_read_b128 v[100:103], v144 offset:8192
	v_mul_f32_e32 v104, v62, v104
	v_readlane_b32 s43, v253, 17
	v_readlane_b32 s44, v253, 18
	v_readlane_b32 s45, v253, 19
	s_waitcnt lgkmcnt(0)
	v_mul_f32_e32 v100, v100, v104
	s_waitcnt vmcnt(26)
	v_fma_f32 v100, v52, v100, v84
	v_mul_f32_e32 v52, v62, v105
	v_mul_f32_e32 v52, v101, v52
	v_fma_f32 v85, v53, v52, v85
	v_mul_f32_e32 v52, v62, v106
	v_mul_f32_e32 v52, v102, v52
	v_fma_f32 v86, v54, v52, v86
	v_mul_f32_e32 v52, v62, v107
	v_mul_f32_e32 v52, v103, v52
	v_fmac_f32_e32 v87, v55, v52
	ds_read_b128 v[52:55], v144 offset:8208
	v_mul_f32_e32 v101, v62, v112
	v_mul_f32_e32 v84, v85, v85
	v_fmac_f32_e32 v84, v100, v100
	v_fmac_f32_e32 v84, v86, v86
	s_waitcnt lgkmcnt(0)
	v_mul_f32_e32 v52, v101, v52
	v_fma_f32 v76, v92, v52, v76
	v_mul_f32_e32 v52, v62, v113
	v_mul_f32_e32 v52, v52, v53
	v_fma_f32 v77, v93, v52, v77
	v_mul_f32_e32 v52, v62, v114
	v_mul_f32_e32 v52, v52, v54
	v_fmac_f32_e32 v84, v87, v87
	v_fma_f32 v78, v94, v52, v78
	v_mul_f32_e32 v52, v62, v115
	v_fmac_f32_e32 v84, v76, v76
	v_mul_f32_e32 v52, v52, v55
	v_fmac_f32_e32 v84, v77, v77
	v_fmac_f32_e32 v79, v95, v52
	v_cvt_pk_bf16_f32 v52, v100, v85
	v_cvt_pk_bf16_f32 v53, v86, v87
	v_cvt_pk_bf16_f32 v54, v76, v77
	v_lshl_add_u64 v[76:77], v[132:133], 0, s[26:27]
	v_cvt_pk_bf16_f32 v55, v78, v79
	global_store_dwordx4 v[76:77], v[52:55], off
	ds_read_b128 v[92:95], v144 offset:2048
	ds_read_b128 v[100:103], v144 offset:2064
	ds_read_b128 v[104:107], v144 offset:10240
	v_fmac_f32_e32 v84, v78, v78
	v_mul_f32_e32 v78, v62, v116
	v_fmac_f32_e32 v84, v79, v79
	v_readlane_b32 s46, v253, 20
	s_waitcnt lgkmcnt(0)
	v_mul_f32_e32 v78, v78, v104
	s_waitcnt vmcnt(25)
	v_fma_f32 v40, v92, v78, v40
	v_mul_f32_e32 v78, v62, v108
	v_mul_f32_e32 v78, v78, v105
	v_fma_f32 v41, v93, v78, v41
	v_mul_f32_e32 v78, v62, v117
	v_mul_f32_e32 v78, v78, v106
	v_fma_f32 v42, v94, v78, v42
	v_mul_f32_e32 v78, v62, v109
	v_mul_f32_e32 v78, v78, v107
	v_fmac_f32_e32 v43, v95, v78
	ds_read_b128 v[92:95], v144 offset:10256
	v_mul_f32_e32 v78, v62, v118
	v_fmac_f32_e32 v84, v40, v40
	v_fmac_f32_e32 v84, v41, v41
	v_fmac_f32_e32 v84, v42, v42
	s_waitcnt lgkmcnt(0)
	v_mul_f32_e32 v78, v78, v92
	v_fma_f32 v78, v100, v78, v32
	v_mul_f32_e32 v32, v62, v110
	v_mul_f32_e32 v32, v32, v93
	v_fma_f32 v79, v101, v32, v33
	v_mul_f32_e32 v32, v62, v119
	v_fmac_f32_e32 v84, v43, v43
	v_mul_f32_e32 v32, v32, v94
	v_fmac_f32_e32 v84, v78, v78
	v_fma_f32 v85, v102, v32, v34
	v_mul_f32_e32 v32, v62, v111
	v_fmac_f32_e32 v84, v79, v79
	v_mul_f32_e32 v32, v32, v95
	v_fmac_f32_e32 v84, v85, v85
	v_fmac_f32_e32 v35, v103, v32
	v_fmac_f32_e32 v84, v35, v35
	v_cvt_pk_bf16_f32 v32, v40, v41
	v_cvt_pk_bf16_f32 v33, v42, v43
	v_cvt_pk_bf16_f32 v34, v78, v79
	v_cvt_pk_bf16_f32 v35, v85, v35
	global_store_dwordx4 v[76:77], v[32:35], off offset:1024
	ds_read_b128 v[40:43], v144 offset:4096
	ds_read_b128 v[92:95], v144 offset:4112
	ds_read_b128 v[100:103], v144 offset:12288
	v_mul_f32_e32 v78, v62, v129
	v_readlane_b32 s47, v253, 21
	v_readlane_b32 s48, v253, 22
	v_readlane_b32 s49, v253, 23
	s_waitcnt lgkmcnt(0)
	v_mul_f32_e32 v78, v78, v100
	s_waitcnt vmcnt(24)
	v_fma_f32 v24, v40, v78, v24
	v_mul_f32_e32 v40, v62, v157
	v_mul_f32_e32 v40, v40, v101
	v_fma_f32 v25, v41, v40, v25
	v_mul_f32_e32 v40, v62, v158
	v_mul_f32_e32 v40, v40, v102
	v_fma_f32 v26, v42, v40, v26
	v_mul_f32_e32 v40, v62, v159
	v_mul_f32_e32 v40, v40, v103
	v_fmac_f32_e32 v27, v43, v40
	ds_read_b128 v[40:43], v144 offset:12304
	v_mul_f32_e32 v78, v62, v160
	v_fmac_f32_e32 v84, v24, v24
	v_fmac_f32_e32 v84, v25, v25
	v_fmac_f32_e32 v84, v26, v26
	s_waitcnt lgkmcnt(0)
	v_mul_f32_e32 v40, v78, v40
	v_fma_f32 v40, v92, v40, v16
	v_mul_f32_e32 v16, v62, v99
	v_mul_f32_e32 v16, v16, v41
	v_fma_f32 v41, v93, v16, v17
	v_mul_f32_e32 v16, v62, v97
	v_fmac_f32_e32 v84, v27, v27
	v_mul_f32_e32 v16, v16, v42
	v_fmac_f32_e32 v84, v40, v40
	v_fma_f32 v42, v94, v16, v18
	v_mul_f32_e32 v16, v62, v96
	v_fmac_f32_e32 v84, v41, v41
	v_mul_f32_e32 v16, v16, v43
	v_fmac_f32_e32 v84, v42, v42
	v_fmac_f32_e32 v19, v95, v16
	v_fmac_f32_e32 v84, v19, v19
	v_cvt_pk_bf16_f32 v16, v24, v25
	v_cvt_pk_bf16_f32 v17, v26, v27
	v_cvt_pk_bf16_f32 v18, v40, v41
	v_cvt_pk_bf16_f32 v19, v42, v19
	global_store_dwordx4 v[76:77], v[16:19], off offset:2048
	ds_read_b128 v[24:27], v144 offset:6144
	ds_read_b128 v[40:43], v144 offset:6160
	ds_read_b128 v[92:95], v144 offset:14336
	v_mul_f32_e32 v78, v62, v98
	v_readlane_b32 s50, v253, 24
	v_readlane_b32 s51, v253, 25
	s_waitcnt lgkmcnt(0)
	v_mul_f32_e32 v78, v78, v92
	s_waitcnt vmcnt(23)
	v_fma_f32 v78, v24, v78, v8
	v_mul_f32_e32 v8, v62, v63
	v_mul_f32_e32 v8, v8, v93
	v_fma_f32 v63, v25, v8, v9
	v_pk_mul_f32 v[8:9], v[62:63], v[68:69] op_sel_hi:[0,1]
	v_pk_mul_f32 v[8:9], v[8:9], v[94:95] op_sel:[1,0] op_sel_hi:[0,1]
	v_fmac_f32_e32 v84, v78, v78
	v_pk_fma_f32 v[24:25], v[26:27], v[8:9], v[10:11]
	v_fmac_f32_e32 v84, v63, v63
	v_pk_mul_f32 v[8:9], v[24:25], v[24:25]
	v_pk_mul_f32 v[26:27], v[62:63], v[70:71] op_sel_hi:[0,1]
	v_add_f32_e32 v8, v84, v8
	v_add_f32_e32 v68, v8, v9
	ds_read_b128 v[8:11], v144 offset:14352
	s_waitcnt lgkmcnt(0)
	v_pk_mul_f32 v[8:9], v[26:27], v[8:9] op_sel:[1,0] op_sel_hi:[0,1]
	v_pk_fma_f32 v[8:9], v[40:41], v[8:9], v[0:1]
	s_nop 0
	v_pk_mul_f32 v[0:1], v[8:9], v[8:9]
	s_nop 0
	v_add_f32_e32 v0, v68, v0
	v_add_f32_e32 v26, v0, v1
	v_pk_mul_f32 v[0:1], v[62:63], v[60:61] op_sel_hi:[0,1]
	v_pk_mul_f32 v[0:1], v[0:1], v[10:11] op_sel:[1,0] op_sel_hi:[0,1]
	v_pk_fma_f32 v[10:11], v[42:43], v[0:1], v[2:3]
	s_nop 0
	v_pk_mul_f32 v[0:1], v[10:11], v[10:11]
	s_nop 0
	v_add_f32_e32 v0, v26, v0
	v_add_f32_e32 v26, v0, v1
	v_cvt_pk_bf16_f32 v0, v78, v63
	v_cvt_pk_bf16_f32 v1, v24, v25
	v_cvt_pk_bf16_f32 v2, v8, v9
	v_cvt_pk_bf16_f32 v3, v10, v11
	global_store_dwordx4 v[76:77], v[0:3], off offset:3072
	s_nop 0
	v_add_f32_dpp v8, v26, v26 quad_perm:[1,0,3,2] row_mask:0xf bank_mask:0xf bound_ctrl:1
	s_nop 1
	v_add_f32_dpp v8, v8, v8 quad_perm:[2,3,0,1] row_mask:0xf bank_mask:0xf bound_ctrl:1
	s_nop 1
	v_add_f32_dpp v8, v8, v8 row_ror:4 row_mask:0xf bank_mask:0xf bound_ctrl:1
	s_nop 1
	v_add_f32_dpp v8, v8, v8 row_ror:8 row_mask:0xf bank_mask:0xf bound_ctrl:1
	s_nop 0
	v_readlane_b32 s3, v8, 16
	v_readlane_b32 s26, v8, 48
	v_readlane_b32 s24, v8, 0
	v_readlane_b32 s25, v8, 32
	v_mov_b32_e32 v8, s3
	v_mov_b32_e32 v9, s26
	v_pk_add_f32 v[8:9], s[24:25], v[8:9]
	s_nop 0
	v_add_f32_e32 v8, v8, v9
	v_fmamk_f32 v8, v8, 0x3a000000, v151
	v_cmp_gt_f32_e32 vcc, s11, v8
	v_mul_f32_e32 v9, 0x4b800000, v8
	s_nop 0
	v_cndmask_b32_e32 v8, v8, v9, vcc
	v_rsq_f32_e32 v8, v8
	s_nop 0
	v_mul_f32_e32 v9, 0x45800000, v8
	v_cndmask_b32_e32 v10, v8, v9, vcc
	s_and_saveexec_b64 s[24:25], s[6:7]
	v_mov_b32_e32 v8, s10
	ds_write_b32 v8, v10 offset:60684
	s_or_b64 exec, exec, s[24:25]
	v_lshlrev_b32_e32 v8, 16, v52
	v_and_b32_e32 v9, 0xffff0000, v52
	v_lshlrev_b32_e32 v11, 16, v53
	v_and_b32_e32 v60, 0xffff0000, v53
	v_lshlrev_b32_e32 v61, 16, v54
	v_and_b32_e32 v62, 0xffff0000, v54
	v_lshlrev_b32_e32 v63, 16, v55
	v_and_b32_e32 v68, 0xffff0000, v55
	ds_read_b128 v[24:27], v144 offset:16384
	ds_read_b128 v[40:43], v144 offset:16400
	ds_read_b128 v[52:55], v144 offset:32768
	v_mul_f32_e32 v8, v10, v8
	v_mul_f32_e32 v9, v10, v9
	v_mul_f32_e32 v11, v10, v11
	s_lshl_b64 s[20:21], s[20:21], 11
	s_waitcnt lgkmcnt(0)
	v_fma_f32 v8, v8, v24, v52
	v_mul_f32_e32 v24, v10, v60
	v_fma_f32 v9, v9, v25, v53
	v_fma_f32 v11, v11, v26, v54
	v_fmac_f32_e32 v55, v24, v27
	ds_read_b128 v[24:27], v144 offset:32784
	v_mul_f32_e32 v52, v10, v61
	v_med3_f32 v8, v8, s12, v154
	v_med3_f32 v9, v9, s12, v154
	v_med3_f32 v11, v11, s12, v154
	s_waitcnt lgkmcnt(0)
	v_fma_f32 v40, v52, v40, v24
	v_mul_f32_e32 v24, v10, v62
	v_fma_f32 v25, v24, v41, v25
	v_mul_f32_e32 v24, v10, v63
	v_fma_f32 v26, v24, v42, v26
	v_mul_f32_e32 v24, v10, v68
	v_fmac_f32_e32 v27, v24, v43
	v_mov_b32_e32 v24, 0
	v_cvt_pk_fp8_f32 v24, v8, v9
	v_med3_f32 v8, v40, s12, v154
	v_med3_f32 v9, v25, s12, v154
	v_mov_b32_e32 v25, 0
	v_cvt_pk_fp8_f32 v25, v8, v9
	v_med3_f32 v41, v55, s12, v154
	v_cvt_pk_fp8_f32 v24, v11, v41 op_sel:[0,0,1]
	v_med3_f32 v11, v26, s12, v154
	v_med3_f32 v26, v27, s12, v154
	v_cvt_pk_fp8_f32 v25, v11, v26 op_sel:[0,0,1]
	v_lshl_add_u64 v[8:9], v[134:135], 0, s[20:21]
	v_lshlrev_b32_e32 v11, 16, v32
	v_and_b32_e32 v40, 0xffff0000, v32
	global_store_dwordx2 v[8:9], v[24:25], off
	v_lshlrev_b32_e32 v41, 16, v33
	v_and_b32_e32 v42, 0xffff0000, v33
	v_lshlrev_b32_e32 v43, 16, v34
	v_and_b32_e32 v52, 0xffff0000, v34
	v_lshlrev_b32_e32 v53, 16, v35
	v_and_b32_e32 v54, 0xffff0000, v35
	ds_read_b128 v[24:27], v144 offset:18432
	ds_read_b128 v[32:35], v144 offset:34816
	v_mul_f32_e32 v11, v10, v11
	s_waitcnt vmcnt(16)
	v_and_b32_e32 v108, 0xffff0000, v88
	v_lshlrev_b32_e32 v104, 16, v88
	v_mul_f32_e32 v96, v108, v108
	s_waitcnt lgkmcnt(0)
	v_fma_f32 v11, v11, v24, v32
	v_mul_f32_e32 v24, v10, v40
	v_fma_f32 v32, v24, v25, v33
	v_mul_f32_e32 v24, v10, v41
	v_fma_f32 v33, v24, v26, v34
	v_mul_f32_e32 v24, v10, v42
	v_fmac_f32_e32 v35, v24, v27
	v_mul_f32_e32 v34, v10, v43
	ds_read_b128 v[24:27], v144 offset:18448
	ds_read_b128 v[40:43], v144 offset:34832
	v_med3_f32 v11, v11, s12, v154
	v_lshlrev_b32_e32 v109, 16, v89
	v_fmac_f32_e32 v96, v104, v104
	v_and_b32_e32 v89, 0xffff0000, v89
	s_waitcnt lgkmcnt(0)
	v_fma_f32 v34, v34, v24, v40
	v_mul_f32_e32 v24, v10, v52
	v_fma_f32 v25, v24, v25, v41
	v_mul_f32_e32 v24, v10, v53
	v_fma_f32 v26, v24, v26, v42
	v_mul_f32_e32 v24, v10, v54
	v_fmac_f32_e32 v43, v24, v27
	v_med3_f32 v27, v32, s12, v154
	v_mov_b32_e32 v24, 0
	v_cvt_pk_fp8_f32 v24, v11, v27
	v_med3_f32 v11, v34, s12, v154
	v_med3_f32 v27, v25, s12, v154
	v_mov_b32_e32 v25, 0
	v_cvt_pk_fp8_f32 v25, v11, v27
	v_med3_f32 v32, v33, s12, v154
	v_med3_f32 v33, v35, s12, v154
	v_cvt_pk_fp8_f32 v24, v32, v33 op_sel:[0,0,1]
	v_med3_f32 v26, v26, s12, v154
	v_med3_f32 v32, v43, s12, v154
	v_cvt_pk_fp8_f32 v25, v26, v32 op_sel:[0,0,1]
	v_lshlrev_b32_e32 v11, 16, v16
	v_and_b32_e32 v32, 0xffff0000, v16
	v_lshlrev_b32_e32 v33, 16, v17
	global_store_dwordx2 v[8:9], v[24:25], off offset:512
	v_and_b32_e32 v34, 0xffff0000, v17
	v_lshlrev_b32_e32 v35, 16, v18
	v_and_b32_e32 v40, 0xffff0000, v18
	v_lshlrev_b32_e32 v41, 16, v19
	v_and_b32_e32 v42, 0xffff0000, v19
	ds_read_b128 v[16:19], v144 offset:20480
	ds_read_b128 v[24:27], v144 offset:36864
	v_mul_f32_e32 v11, v10, v11
	v_fmac_f32_e32 v96, v109, v109
	v_lshlrev_b32_e32 v110, 16, v90
	v_fmac_f32_e32 v96, v89, v89
	s_waitcnt lgkmcnt(0)
	v_fma_f32 v11, v11, v16, v24
	v_mul_f32_e32 v16, v10, v32
	v_fma_f32 v24, v16, v17, v25
	v_mul_f32_e32 v16, v10, v33
	v_fma_f32 v25, v16, v18, v26
	v_mul_f32_e32 v16, v10, v34
	v_fmac_f32_e32 v27, v16, v19
	v_mul_f32_e32 v26, v10, v35
	ds_read_b128 v[16:19], v144 offset:20496
	ds_read_b128 v[32:35], v144 offset:36880
	v_med3_f32 v11, v11, s12, v154
	v_and_b32_e32 v90, 0xffff0000, v90
	v_fmac_f32_e32 v96, v110, v110
	v_lshlrev_b32_e32 v111, 16, v91
	s_waitcnt lgkmcnt(0)
	v_fma_f32 v26, v26, v16, v32
	v_mul_f32_e32 v16, v10, v40
	v_fma_f32 v17, v16, v17, v33
	v_mul_f32_e32 v16, v10, v41
	v_fma_f32 v18, v16, v18, v34
	v_mul_f32_e32 v16, v10, v42
	v_fmac_f32_e32 v35, v16, v19
	v_med3_f32 v19, v24, s12, v154
	v_mov_b32_e32 v16, 0
	v_cvt_pk_fp8_f32 v16, v11, v19
	v_med3_f32 v11, v26, s12, v154
	v_med3_f32 v19, v17, s12, v154
	v_mov_b32_e32 v17, 0
	v_cvt_pk_fp8_f32 v17, v11, v19
	v_med3_f32 v24, v25, s12, v154
	v_med3_f32 v25, v27, s12, v154
	v_cvt_pk_fp8_f32 v16, v24, v25 op_sel:[0,0,1]
	v_med3_f32 v18, v18, s12, v154
	v_med3_f32 v24, v35, s12, v154
	v_fmac_f32_e32 v96, v90, v90
	v_cvt_pk_fp8_f32 v17, v18, v24 op_sel:[0,0,1]
	v_and_b32_e32 v91, 0xffff0000, v91
	v_fmac_f32_e32 v96, v111, v111
	v_fmac_f32_e32 v96, v91, v91
	s_waitcnt vmcnt(16)
	v_lshlrev_b32_e32 v112, 16, v80
	v_and_b32_e32 v113, 0xffff0000, v80
	v_fmac_f32_e32 v96, v112, v112
	v_lshlrev_b32_e32 v114, 16, v81
	v_fmac_f32_e32 v96, v113, v113
	global_store_dwordx2 v[8:9], v[16:17], off offset:1024
	v_and_b32_e32 v115, 0xffff0000, v81
	v_fmac_f32_e32 v96, v114, v114
	v_lshlrev_b32_e32 v11, 16, v0
	v_and_b32_e32 v24, 0xffff0000, v0
	v_lshlrev_b32_e32 v25, 16, v1
	v_and_b32_e32 v26, 0xffff0000, v1
	v_lshlrev_b32_e32 v27, 16, v2
	v_and_b32_e32 v32, 0xffff0000, v2
	v_lshlrev_b32_e32 v33, 16, v3
	v_and_b32_e32 v34, 0xffff0000, v3
	ds_read_b128 v[0:3], v144 offset:22528
	ds_read_b128 v[16:19], v144 offset:38912
	v_lshlrev_b32_e32 v116, 16, v82
	v_fmac_f32_e32 v96, v115, v115
	v_and_b32_e32 v117, 0xffff0000, v82
	v_fmac_f32_e32 v96, v116, v116
	v_lshlrev_b32_e32 v118, 16, v83
	v_fmac_f32_e32 v96, v117, v117
	v_and_b32_e32 v119, 0xffff0000, v83
	v_fmac_f32_e32 v96, v118, v118
	v_mul_f32_e32 v11, v10, v11
	v_fmac_f32_e32 v96, v119, v119
	s_waitcnt vmcnt(16)
	v_lshlrev_b32_e32 v129, 16, v72
	s_waitcnt lgkmcnt(0)
	v_fma_f32 v11, v11, v0, v16
	v_mul_f32_e32 v0, v10, v24
	v_and_b32_e32 v157, 0xffff0000, v72
	v_fmac_f32_e32 v96, v129, v129
	v_fma_f32 v16, v0, v1, v17
	v_mul_f32_e32 v0, v10, v25
	v_lshlrev_b32_e32 v158, 16, v73
	v_fmac_f32_e32 v96, v157, v157
	v_fma_f32 v17, v0, v2, v18
	v_mul_f32_e32 v0, v10, v26
	v_and_b32_e32 v159, 0xffff0000, v73
	v_fmac_f32_e32 v96, v158, v158
	v_fmac_f32_e32 v19, v0, v3
	v_mul_f32_e32 v18, v10, v27
	ds_read_b128 v[0:3], v144 offset:22544
	ds_read_b128 v[24:27], v144 offset:38928
	v_lshlrev_b32_e32 v160, 16, v74
	v_fmac_f32_e32 v96, v159, v159
	v_and_b32_e32 v88, 0xffff0000, v74
	v_fmac_f32_e32 v96, v160, v160
	v_lshlrev_b32_e32 v82, 16, v75
	v_fmac_f32_e32 v96, v88, v88
	v_and_b32_e32 v81, 0xffff0000, v75
	v_fmac_f32_e32 v96, v82, v82
	v_fmac_f32_e32 v96, v81, v81
	s_waitcnt vmcnt(15)
	v_lshlrev_b32_e32 v83, 16, v64
	s_waitcnt lgkmcnt(0)
	v_fma_f32 v18, v18, v0, v24
	v_mul_f32_e32 v0, v10, v32
	v_and_b32_e32 v80, 0xffff0000, v64
	v_fmac_f32_e32 v96, v83, v83
	v_and_b32_e32 v72, 0xffff0000, v65
	v_lshlrev_b32_e32 v73, 16, v65
	v_fma_f32 v1, v0, v1, v25
	v_mul_f32_e32 v0, v10, v33
	v_fmac_f32_e32 v96, v80, v80
	v_pk_mul_f32 v[64:65], v[72:73], v[72:73]
	v_fma_f32 v2, v0, v2, v26
	v_mul_f32_e32 v0, v10, v34
	v_add_f32_e32 v65, v65, v96
	v_and_b32_e32 v74, 0xffff0000, v66
	v_lshlrev_b32_e32 v75, 16, v66
	v_fmac_f32_e32 v27, v0, v3
	v_med3_f32 v3, v11, s12, v154
	v_med3_f32 v10, v16, s12, v154
	v_mov_b32_e32 v0, 0
	v_add_f32_e32 v96, v64, v65
	v_pk_mul_f32 v[64:65], v[74:75], v[74:75]
	v_cvt_pk_fp8_f32 v0, v3, v10
	v_med3_f32 v3, v18, s12, v154
	v_med3_f32 v10, v1, s12, v154
	v_mov_b32_e32 v1, 0
	v_add_f32_e32 v65, v65, v96
	v_cvt_pk_fp8_f32 v1, v3, v10
	v_add_f32_e32 v96, v64, v65
	v_and_b32_e32 v64, 0xffff0000, v67
	v_lshlrev_b32_e32 v65, 16, v67
	v_pk_mul_f32 v[66:67], v[64:65], v[64:65]
	v_med3_f32 v11, v17, s12, v154
	v_med3_f32 v16, v19, s12, v154
	v_add_f32_e32 v67, v67, v96
	v_cvt_pk_fp8_f32 v0, v11, v16 op_sel:[0,0,1]
	v_med3_f32 v2, v2, s12, v154
	v_med3_f32 v11, v27, s12, v154
	v_add_f32_e32 v66, v66, v67
	v_cvt_pk_fp8_f32 v1, v2, v11 op_sel:[0,0,1]
	s_or_b32 s24, s0, 5
	v_add_f32_dpp v66, v66, v66 quad_perm:[1,0,3,2] row_mask:0xf bank_mask:0xf bound_ctrl:1
	s_mov_b32 s25, s1
	s_lshl_b64 s[26:27], s[24:25], 12
	v_add_f32_dpp v66, v66, v66 quad_perm:[2,3,0,1] row_mask:0xf bank_mask:0xf bound_ctrl:1
	s_lshl_b64 s[20:21], s[24:25], 13
	v_readlane_b32 s36, v253, 10
	v_add_f32_dpp v66, v66, v66 row_ror:4 row_mask:0xf bank_mask:0xf bound_ctrl:1
	v_readlane_b32 s37, v253, 11
	s_add_u32 s20, s36, s20
	v_add_f32_dpp v66, v66, v66 row_ror:8 row_mask:0xf bank_mask:0xf bound_ctrl:1
	global_store_dwordx2 v[8:9], v[0:1], off offset:1536
	v_lshl_add_u64 v[0:1], v[130:131], 0, s[26:27]
	s_addc_u32 s21, s37, s21
	v_readlane_b32 s3, v66, 16
	v_readlane_b32 s28, v66, 48
	global_load_dwordx4 v[92:95], v[0:1], off
	global_load_dwordx4 v[84:87], v[0:1], off offset:1024
	global_load_dwordx4 v[76:79], v[0:1], off offset:2048
	global_load_dwordx4 v[68:71], v[0:1], off offset:3072
	global_load_dwordx4 v[52:55], v122, s[20:21] offset:16
	global_load_dwordx4 v[60:63], v122, s[20:21]
	global_load_dwordx4 v[32:35], v122, s[20:21] offset:2064
	global_load_dwordx4 v[40:43], v122, s[20:21] offset:2048
	global_load_dwordx4 v[16:19], v149, s[20:21] offset:16
	global_load_dwordx4 v[24:27], v149, s[20:21]
	global_load_dwordx4 v[0:3], v150, s[20:21] offset:16
	global_load_dwordx4 v[8:11], v150, s[20:21]
	v_readlane_b32 s20, v66, 0
	v_readlane_b32 s21, v66, 32
	v_mov_b32_e32 v66, s3
	v_mov_b32_e32 v67, s28
	v_pk_add_f32 v[66:67], s[20:21], v[66:67]
	ds_read_b128 v[96:99], v144
	ds_read_b128 v[100:103], v144 offset:16
	v_add_f32_e32 v66, v66, v67
	v_fmamk_f32 v66, v66, 0x3a000000, v151
	v_cmp_gt_f32_e32 vcc, s11, v66
	v_mul_f32_e32 v67, 0x4b800000, v66
	v_readlane_b32 s38, v253, 12
	v_cndmask_b32_e32 v66, v66, v67, vcc
	v_rsq_f32_e32 v66, v66
	v_readlane_b32 s39, v253, 13
	v_readlane_b32 s40, v253, 14
	v_readlane_b32 s41, v253, 15
	v_mul_f32_e32 v67, 0x45800000, v66
	v_cndmask_b32_e32 v66, v66, v67, vcc
	v_mul_f32_e32 v67, v66, v104
	ds_read_b128 v[104:107], v144 offset:8192
	v_mul_f32_e32 v89, v66, v89
	v_readlane_b32 s42, v253, 16
	v_readlane_b32 s43, v253, 17
	v_readlane_b32 s44, v253, 18
	s_waitcnt lgkmcnt(0)
	v_mul_f32_e32 v67, v104, v67
	s_waitcnt vmcnt(26)
	v_fma_f32 v56, v96, v67, v56
	v_mul_f32_e32 v67, v66, v108
	v_mul_f32_e32 v96, v66, v109
	v_mul_f32_e32 v67, v105, v67
	v_mul_f32_e32 v96, v106, v96
	v_mul_f32_e32 v89, v107, v89
	v_fma_f32 v57, v97, v67, v57
	v_fma_f32 v58, v98, v96, v58
	v_fmac_f32_e32 v59, v99, v89
	ds_read_b128 v[96:99], v144 offset:8208
	v_mul_f32_e32 v89, v66, v110
	v_mul_f32_e32 v67, v57, v57
	v_fmac_f32_e32 v67, v56, v56
	v_fmac_f32_e32 v67, v58, v58
	s_waitcnt lgkmcnt(0)
	v_mul_f32_e32 v89, v89, v96
	v_fma_f32 v89, v100, v89, v48
	v_mul_f32_e32 v48, v66, v90
	v_mul_f32_e32 v48, v48, v97
	v_fma_f32 v90, v101, v48, v49
	v_mul_f32_e32 v48, v66, v111
	v_fmac_f32_e32 v67, v59, v59
	v_mul_f32_e32 v48, v48, v98
	v_fmac_f32_e32 v67, v89, v89
	v_fma_f32 v96, v102, v48, v50
	v_mul_f32_e32 v48, v66, v91
	v_fmac_f32_e32 v67, v90, v90
	v_mul_f32_e32 v48, v48, v99
	v_fmac_f32_e32 v67, v96, v96
	v_fmac_f32_e32 v51, v103, v48
	v_cvt_pk_bf16_f32 v48, v56, v57
	v_lshl_add_u64 v[56:57], v[132:133], 0, s[8:9]
	v_fmac_f32_e32 v67, v51, v51
	v_cvt_pk_bf16_f32 v49, v58, v59
	v_cvt_pk_bf16_f32 v50, v89, v90
	v_cvt_pk_bf16_f32 v51, v96, v51
	global_store_dwordx4 v[56:57], v[48:51], off
	ds_read_b128 v[96:99], v144 offset:2048
	ds_read_b128 v[100:103], v144 offset:2064
	ds_read_b128 v[104:107], v144 offset:10240
	v_mul_f32_e32 v58, v66, v112
	v_readlane_b32 s45, v253, 19
	v_readlane_b32 s46, v253, 20
	v_readlane_b32 s47, v253, 21
	s_waitcnt lgkmcnt(0)
	v_mul_f32_e32 v58, v58, v104
	s_waitcnt vmcnt(25)
	v_fma_f32 v44, v96, v58, v44
	v_mul_f32_e32 v58, v66, v113
	v_mul_f32_e32 v58, v58, v105
	v_fma_f32 v45, v97, v58, v45
	v_mul_f32_e32 v58, v66, v114
	v_mul_f32_e32 v58, v58, v106
	v_fma_f32 v46, v98, v58, v46
	v_mul_f32_e32 v58, v66, v115
	v_mul_f32_e32 v58, v58, v107
	v_fmac_f32_e32 v47, v99, v58
	ds_read_b128 v[96:99], v144 offset:10256
	v_mul_f32_e32 v58, v66, v116
	v_fmac_f32_e32 v67, v44, v44
	v_fmac_f32_e32 v67, v45, v45
	v_fmac_f32_e32 v67, v46, v46
	s_waitcnt lgkmcnt(0)
	v_mul_f32_e32 v58, v58, v96
	v_fma_f32 v58, v100, v58, v36
	v_mul_f32_e32 v36, v66, v117
	v_mul_f32_e32 v36, v36, v97
	v_fma_f32 v59, v101, v36, v37
	v_mul_f32_e32 v36, v66, v118
	v_fmac_f32_e32 v67, v47, v47
	v_mul_f32_e32 v36, v36, v98
	v_fmac_f32_e32 v67, v58, v58
	v_fma_f32 v89, v102, v36, v38
	v_mul_f32_e32 v36, v66, v119
	v_fmac_f32_e32 v67, v59, v59
	v_mul_f32_e32 v36, v36, v99
	v_fmac_f32_e32 v67, v89, v89
	v_fmac_f32_e32 v39, v103, v36
	v_fmac_f32_e32 v67, v39, v39
	v_cvt_pk_bf16_f32 v36, v44, v45
	v_cvt_pk_bf16_f32 v37, v46, v47
	v_cvt_pk_bf16_f32 v38, v58, v59
	v_cvt_pk_bf16_f32 v39, v89, v39
	global_store_dwordx4 v[56:57], v[36:39], off offset:1024
	ds_read_b128 v[44:47], v144 offset:4096
	ds_read_b128 v[96:99], v144 offset:4112
	ds_read_b128 v[100:103], v144 offset:12288
	v_mul_f32_e32 v58, v66, v129
	v_readlane_b32 s48, v253, 22
	v_readlane_b32 s49, v253, 23
	v_readlane_b32 s50, v253, 24
	s_waitcnt lgkmcnt(0)
	v_mul_f32_e32 v58, v58, v100
	s_waitcnt vmcnt(24)
	v_fma_f32 v28, v44, v58, v28
	v_mul_f32_e32 v44, v66, v157
	v_mul_f32_e32 v44, v44, v101
	v_fma_f32 v29, v45, v44, v29
	v_mul_f32_e32 v44, v66, v158
	v_mul_f32_e32 v44, v44, v102
	v_fma_f32 v30, v46, v44, v30
	v_mul_f32_e32 v44, v66, v159
	v_mul_f32_e32 v44, v44, v103
	v_fmac_f32_e32 v31, v47, v44
	ds_read_b128 v[44:47], v144 offset:12304
	v_mul_f32_e32 v58, v66, v160
	v_fmac_f32_e32 v67, v28, v28
	v_fmac_f32_e32 v67, v29, v29
	v_fmac_f32_e32 v67, v30, v30
	s_waitcnt lgkmcnt(0)
	v_mul_f32_e32 v44, v58, v44
	v_fma_f32 v44, v96, v44, v20
	v_mul_f32_e32 v20, v66, v88
	v_mul_f32_e32 v20, v20, v45
	v_fma_f32 v45, v97, v20, v21
	v_mul_f32_e32 v20, v66, v82
	v_fmac_f32_e32 v67, v31, v31
	v_mul_f32_e32 v20, v20, v46
	v_fmac_f32_e32 v67, v44, v44
	v_fma_f32 v46, v98, v20, v22
	v_mul_f32_e32 v20, v66, v81
	v_fmac_f32_e32 v67, v45, v45
	v_mul_f32_e32 v20, v20, v47
	v_fmac_f32_e32 v67, v46, v46
	v_fmac_f32_e32 v23, v99, v20
	v_fmac_f32_e32 v67, v23, v23
	v_cvt_pk_bf16_f32 v20, v28, v29
	v_cvt_pk_bf16_f32 v21, v30, v31
	v_cvt_pk_bf16_f32 v22, v44, v45
	v_cvt_pk_bf16_f32 v23, v46, v23
	global_store_dwordx4 v[56:57], v[20:23], off offset:2048
	ds_read_b128 v[28:31], v144 offset:6144
	ds_read_b128 v[44:47], v144 offset:6160
	ds_read_b128 v[88:91], v144 offset:14336
	v_mul_f32_e32 v58, v66, v83
	v_readlane_b32 s51, v253, 25
	s_waitcnt lgkmcnt(0)
	v_mul_f32_e32 v58, v58, v88
	s_waitcnt vmcnt(23)
	v_fma_f32 v58, v28, v58, v12
	v_mul_f32_e32 v12, v66, v80
	v_mul_f32_e32 v12, v12, v89
	v_fmac_f32_e32 v67, v58, v58
	v_fma_f32 v59, v29, v12, v13
	v_fmac_f32_e32 v67, v59, v59
	v_pk_mul_f32 v[12:13], v[66:67], v[72:73] op_sel_hi:[0,1]
	v_pk_mul_f32 v[12:13], v[12:13], v[90:91] op_sel:[1,0] op_sel_hi:[0,1]
	v_pk_fma_f32 v[28:29], v[30:31], v[12:13], v[14:15]
	s_nop 0
	v_pk_mul_f32 v[12:13], v[28:29], v[28:29]
	s_nop 0
	v_add_f32_e32 v12, v67, v12
	v_add_f32_e32 v67, v12, v13
	ds_read_b128 v[12:15], v144 offset:14352
	v_pk_mul_f32 v[30:31], v[66:67], v[74:75] op_sel_hi:[0,1]
	s_waitcnt lgkmcnt(0)
	v_pk_mul_f32 v[12:13], v[30:31], v[12:13] op_sel:[1,0] op_sel_hi:[0,1]
	v_pk_fma_f32 v[12:13], v[44:45], v[12:13], v[4:5]
	s_nop 0
	v_pk_mul_f32 v[4:5], v[12:13], v[12:13]
	s_nop 0
	v_add_f32_e32 v4, v67, v4
	v_add_f32_e32 v30, v4, v5
	v_pk_mul_f32 v[4:5], v[66:67], v[64:65] op_sel_hi:[0,1]
	v_pk_mul_f32 v[4:5], v[4:5], v[14:15] op_sel:[1,0] op_sel_hi:[0,1]
	v_pk_fma_f32 v[14:15], v[46:47], v[4:5], v[6:7]
	s_nop 0
	v_pk_mul_f32 v[4:5], v[14:15], v[14:15]
	s_nop 0
	v_add_f32_e32 v4, v30, v4
	v_add_f32_e32 v30, v4, v5
	v_cvt_pk_bf16_f32 v4, v58, v59
	v_cvt_pk_bf16_f32 v5, v28, v29
	v_cvt_pk_bf16_f32 v6, v12, v13
	v_cvt_pk_bf16_f32 v7, v14, v15
	global_store_dwordx4 v[56:57], v[4:7], off offset:3072
	s_nop 0
	v_add_f32_dpp v12, v30, v30 quad_perm:[1,0,3,2] row_mask:0xf bank_mask:0xf bound_ctrl:1
	s_nop 1
	v_add_f32_dpp v12, v12, v12 quad_perm:[2,3,0,1] row_mask:0xf bank_mask:0xf bound_ctrl:1
	s_nop 1
	v_add_f32_dpp v12, v12, v12 row_ror:4 row_mask:0xf bank_mask:0xf bound_ctrl:1
	s_nop 1
	v_add_f32_dpp v12, v12, v12 row_ror:8 row_mask:0xf bank_mask:0xf bound_ctrl:1
	s_nop 0
	v_readlane_b32 s3, v12, 16
	v_readlane_b32 s20, v12, 48
	v_readlane_b32 s8, v12, 0
	v_readlane_b32 s9, v12, 32
	v_mov_b32_e32 v12, s3
	v_mov_b32_e32 v13, s20
	v_pk_add_f32 v[12:13], s[8:9], v[12:13]
	s_nop 0
	v_add_f32_e32 v12, v12, v13
	v_fmamk_f32 v12, v12, 0x3a000000, v151
	v_cmp_gt_f32_e32 vcc, s11, v12
	v_mul_f32_e32 v13, 0x4b800000, v12
	s_nop 0
	v_cndmask_b32_e32 v12, v12, v13, vcc
	v_rsq_f32_e32 v12, v12
	s_nop 0
	v_mul_f32_e32 v13, 0x45800000, v12
	v_cndmask_b32_e32 v14, v12, v13, vcc
	s_and_saveexec_b64 s[8:9], s[6:7]
	v_mov_b32_e32 v12, s10
	ds_write_b32 v12, v14 offset:60688
	s_or_b64 exec, exec, s[8:9]
	v_lshlrev_b32_e32 v12, 16, v48
	v_and_b32_e32 v13, 0xffff0000, v48
	v_lshlrev_b32_e32 v15, 16, v49
	v_and_b32_e32 v56, 0xffff0000, v49
	v_lshlrev_b32_e32 v57, 16, v50
	v_and_b32_e32 v58, 0xffff0000, v50
	v_lshlrev_b32_e32 v59, 16, v51
	v_and_b32_e32 v64, 0xffff0000, v51
	ds_read_b128 v[28:31], v144 offset:16384
	ds_read_b128 v[44:47], v144 offset:16400
	ds_read_b128 v[48:51], v144 offset:32768
	v_mul_f32_e32 v12, v14, v12
	v_mul_f32_e32 v13, v14, v13
	v_mul_f32_e32 v15, v14, v15
	s_lshl_b64 s[8:9], s[22:23], 11
	s_waitcnt lgkmcnt(0)
	v_fma_f32 v12, v12, v28, v48
	v_mul_f32_e32 v28, v14, v56
	v_fma_f32 v13, v13, v29, v49
	v_fma_f32 v15, v15, v30, v50
	v_fmac_f32_e32 v51, v28, v31
	ds_read_b128 v[28:31], v144 offset:32784
	v_mul_f32_e32 v48, v14, v57
	v_med3_f32 v12, v12, s12, v154
	v_med3_f32 v13, v13, s12, v154
	v_med3_f32 v15, v15, s12, v154
	s_waitcnt lgkmcnt(0)
	v_fma_f32 v44, v48, v44, v28
	v_mul_f32_e32 v28, v14, v58
	v_fma_f32 v29, v28, v45, v29
	v_mul_f32_e32 v28, v14, v59
	v_fma_f32 v30, v28, v46, v30
	v_mul_f32_e32 v28, v14, v64
	v_fmac_f32_e32 v31, v28, v47
	v_mov_b32_e32 v28, 0
	v_cvt_pk_fp8_f32 v28, v12, v13
	v_med3_f32 v12, v44, s12, v154
	v_med3_f32 v13, v29, s12, v154
	v_mov_b32_e32 v29, 0
	v_cvt_pk_fp8_f32 v29, v12, v13
	v_med3_f32 v45, v51, s12, v154
	v_cvt_pk_fp8_f32 v28, v15, v45 op_sel:[0,0,1]
	v_med3_f32 v15, v30, s12, v154
	v_med3_f32 v30, v31, s12, v154
	v_cvt_pk_fp8_f32 v29, v15, v30 op_sel:[0,0,1]
	v_lshl_add_u64 v[12:13], v[134:135], 0, s[8:9]
	v_lshlrev_b32_e32 v15, 16, v36
	v_and_b32_e32 v44, 0xffff0000, v36
	global_store_dwordx2 v[12:13], v[28:29], off
	v_lshlrev_b32_e32 v45, 16, v37
	v_and_b32_e32 v46, 0xffff0000, v37
	v_lshlrev_b32_e32 v47, 16, v38
	v_and_b32_e32 v48, 0xffff0000, v38
	v_lshlrev_b32_e32 v49, 16, v39
	v_and_b32_e32 v50, 0xffff0000, v39
	ds_read_b128 v[28:31], v144 offset:18432
	ds_read_b128 v[36:39], v144 offset:34816
	v_mul_f32_e32 v15, v14, v15
	s_waitcnt vmcnt(16)
	v_and_b32_e32 v106, 0xffff0000, v92
	v_lshlrev_b32_e32 v102, 16, v92
	v_lshlrev_b32_e32 v108, 16, v94
	s_waitcnt lgkmcnt(0)
	v_fma_f32 v15, v15, v28, v36
	v_mul_f32_e32 v28, v14, v44
	v_fma_f32 v36, v28, v29, v37
	v_mul_f32_e32 v28, v14, v45
	v_fma_f32 v37, v28, v30, v38
	v_mul_f32_e32 v28, v14, v46
	v_fmac_f32_e32 v39, v28, v31
	v_mul_f32_e32 v38, v14, v47
	ds_read_b128 v[28:31], v144 offset:18448
	ds_read_b128 v[44:47], v144 offset:34832
	v_med3_f32 v15, v15, s12, v154
	v_and_b32_e32 v109, 0xffff0000, v94
	v_mul_f32_e32 v94, v106, v106
	v_lshlrev_b32_e32 v107, 16, v93
	s_waitcnt lgkmcnt(0)
	v_fma_f32 v38, v38, v28, v44
	v_mul_f32_e32 v28, v14, v48
	v_fma_f32 v29, v28, v29, v45
	v_mul_f32_e32 v28, v14, v49
	v_fma_f32 v30, v28, v30, v46
	v_mul_f32_e32 v28, v14, v50
	v_fmac_f32_e32 v47, v28, v31
	v_med3_f32 v31, v36, s12, v154
	v_mov_b32_e32 v28, 0
	v_cvt_pk_fp8_f32 v28, v15, v31
	v_med3_f32 v15, v38, s12, v154
	v_med3_f32 v31, v29, s12, v154
	v_mov_b32_e32 v29, 0
	v_cvt_pk_fp8_f32 v29, v15, v31
	v_med3_f32 v36, v37, s12, v154
	v_med3_f32 v37, v39, s12, v154
	v_cvt_pk_fp8_f32 v28, v36, v37 op_sel:[0,0,1]
	v_med3_f32 v30, v30, s12, v154
	v_med3_f32 v36, v47, s12, v154
	v_cvt_pk_fp8_f32 v29, v30, v36 op_sel:[0,0,1]
	v_lshlrev_b32_e32 v15, 16, v20
	v_and_b32_e32 v36, 0xffff0000, v20
	v_lshlrev_b32_e32 v37, 16, v21
	global_store_dwordx2 v[12:13], v[28:29], off offset:512
	v_and_b32_e32 v38, 0xffff0000, v21
	v_lshlrev_b32_e32 v39, 16, v22
	v_and_b32_e32 v44, 0xffff0000, v22
	v_lshlrev_b32_e32 v45, 16, v23
	v_and_b32_e32 v46, 0xffff0000, v23
	ds_read_b128 v[20:23], v144 offset:20480
	ds_read_b128 v[28:31], v144 offset:36864
	v_mul_f32_e32 v15, v14, v15
	v_fmac_f32_e32 v94, v102, v102
	v_and_b32_e32 v93, 0xffff0000, v93
	v_fmac_f32_e32 v94, v107, v107
	s_waitcnt lgkmcnt(0)
	v_fma_f32 v15, v15, v20, v28
	v_mul_f32_e32 v20, v14, v36
	v_fma_f32 v28, v20, v21, v29
	v_mul_f32_e32 v20, v14, v37
	v_fma_f32 v29, v20, v22, v30
	v_mul_f32_e32 v20, v14, v38
	v_fmac_f32_e32 v31, v20, v23
	v_mul_f32_e32 v30, v14, v39
	ds_read_b128 v[20:23], v144 offset:20496
	ds_read_b128 v[36:39], v144 offset:36880
	v_med3_f32 v15, v15, s12, v154
	v_fmac_f32_e32 v94, v93, v93
	v_fmac_f32_e32 v94, v108, v108
	v_lshlrev_b32_e32 v110, 16, v95
	s_waitcnt lgkmcnt(0)
	v_fma_f32 v30, v30, v20, v36
	v_mul_f32_e32 v20, v14, v44
	v_fma_f32 v21, v20, v21, v37
	v_mul_f32_e32 v20, v14, v45
	v_fma_f32 v22, v20, v22, v38
	v_mul_f32_e32 v20, v14, v46
	v_fmac_f32_e32 v39, v20, v23
	v_med3_f32 v23, v28, s12, v154
	v_mov_b32_e32 v20, 0
	v_cvt_pk_fp8_f32 v20, v15, v23
	v_med3_f32 v15, v30, s12, v154
	v_med3_f32 v23, v21, s12, v154
	v_mov_b32_e32 v21, 0
	v_cvt_pk_fp8_f32 v21, v15, v23
	v_med3_f32 v28, v29, s12, v154
	v_med3_f32 v29, v31, s12, v154
	v_cvt_pk_fp8_f32 v20, v28, v29 op_sel:[0,0,1]
	v_med3_f32 v22, v22, s12, v154
	v_med3_f32 v28, v39, s12, v154
	v_fmac_f32_e32 v94, v109, v109
	v_cvt_pk_fp8_f32 v21, v22, v28 op_sel:[0,0,1]
	v_and_b32_e32 v111, 0xffff0000, v95
	v_fmac_f32_e32 v94, v110, v110
	v_fmac_f32_e32 v94, v111, v111
	s_waitcnt vmcnt(16)
	v_lshlrev_b32_e32 v112, 16, v84
	v_and_b32_e32 v113, 0xffff0000, v84
	v_fmac_f32_e32 v94, v112, v112
	v_lshlrev_b32_e32 v114, 16, v85
	v_fmac_f32_e32 v94, v113, v113
	global_store_dwordx2 v[12:13], v[20:21], off offset:1024
	v_and_b32_e32 v115, 0xffff0000, v85
	v_fmac_f32_e32 v94, v114, v114
	v_lshlrev_b32_e32 v15, 16, v4
	v_and_b32_e32 v28, 0xffff0000, v4
	v_lshlrev_b32_e32 v29, 16, v5
	v_and_b32_e32 v30, 0xffff0000, v5
	v_lshlrev_b32_e32 v31, 16, v6
	v_and_b32_e32 v36, 0xffff0000, v6
	v_lshlrev_b32_e32 v37, 16, v7
	v_and_b32_e32 v38, 0xffff0000, v7
	ds_read_b128 v[4:7], v144 offset:22528
	ds_read_b128 v[20:23], v144 offset:38912
	v_lshlrev_b32_e32 v116, 16, v86
	v_fmac_f32_e32 v94, v115, v115
	v_and_b32_e32 v117, 0xffff0000, v86
	v_fmac_f32_e32 v94, v116, v116
	v_lshlrev_b32_e32 v118, 16, v87
	v_fmac_f32_e32 v94, v117, v117
	v_and_b32_e32 v119, 0xffff0000, v87
	v_fmac_f32_e32 v94, v118, v118
	v_mul_f32_e32 v15, v14, v15
	v_fmac_f32_e32 v94, v119, v119
	s_waitcnt vmcnt(16)
	v_lshlrev_b32_e32 v129, 16, v76
	s_waitcnt lgkmcnt(0)
	v_fma_f32 v15, v15, v4, v20
	v_mul_f32_e32 v4, v14, v28
	v_and_b32_e32 v157, 0xffff0000, v76
	v_fmac_f32_e32 v94, v129, v129
	v_fma_f32 v20, v4, v5, v21
	v_mul_f32_e32 v4, v14, v29
	v_lshlrev_b32_e32 v158, 16, v77
	v_fmac_f32_e32 v94, v157, v157
	v_fma_f32 v21, v4, v6, v22
	v_mul_f32_e32 v4, v14, v30
	v_and_b32_e32 v159, 0xffff0000, v77
	v_fmac_f32_e32 v94, v158, v158
	v_fmac_f32_e32 v23, v4, v7
	v_mul_f32_e32 v22, v14, v31
	ds_read_b128 v[4:7], v144 offset:22544
	ds_read_b128 v[28:31], v144 offset:38928
	v_lshlrev_b32_e32 v160, 16, v78
	v_fmac_f32_e32 v94, v159, v159
	v_and_b32_e32 v92, 0xffff0000, v78
	v_fmac_f32_e32 v94, v160, v160
	v_lshlrev_b32_e32 v86, 16, v79
	v_fmac_f32_e32 v94, v92, v92
	v_and_b32_e32 v85, 0xffff0000, v79
	v_fmac_f32_e32 v94, v86, v86
	v_fmac_f32_e32 v94, v85, v85
	s_waitcnt vmcnt(15)
	v_lshlrev_b32_e32 v87, 16, v68
	s_waitcnt lgkmcnt(0)
	v_fma_f32 v22, v22, v4, v28
	v_mul_f32_e32 v4, v14, v36
	v_and_b32_e32 v84, 0xffff0000, v68
	v_fmac_f32_e32 v94, v87, v87
	v_and_b32_e32 v76, 0xffff0000, v69
	v_lshlrev_b32_e32 v77, 16, v69
	v_fma_f32 v5, v4, v5, v29
	v_mul_f32_e32 v4, v14, v37
	v_fmac_f32_e32 v94, v84, v84
	v_pk_mul_f32 v[68:69], v[76:77], v[76:77]
	v_fma_f32 v6, v4, v6, v30
	v_mul_f32_e32 v4, v14, v38
	v_add_f32_e32 v69, v69, v94
	v_and_b32_e32 v78, 0xffff0000, v70
	v_lshlrev_b32_e32 v79, 16, v70
	v_fmac_f32_e32 v31, v4, v7
	v_med3_f32 v7, v15, s12, v154
	v_med3_f32 v14, v20, s12, v154
	v_mov_b32_e32 v4, 0
	v_add_f32_e32 v94, v68, v69
	v_pk_mul_f32 v[68:69], v[78:79], v[78:79]
	v_cvt_pk_fp8_f32 v4, v7, v14
	v_med3_f32 v7, v22, s12, v154
	v_med3_f32 v14, v5, s12, v154
	v_mov_b32_e32 v5, 0
	v_add_f32_e32 v69, v69, v94
	v_cvt_pk_fp8_f32 v5, v7, v14
	v_add_f32_e32 v94, v68, v69
	v_and_b32_e32 v68, 0xffff0000, v71
	v_lshlrev_b32_e32 v69, 16, v71
	v_pk_mul_f32 v[70:71], v[68:69], v[68:69]
	v_med3_f32 v15, v21, s12, v154
	v_med3_f32 v20, v23, s12, v154
	v_add_f32_e32 v71, v71, v94
	v_cvt_pk_fp8_f32 v4, v15, v20 op_sel:[0,0,1]
	v_med3_f32 v6, v6, s12, v154
	v_med3_f32 v15, v31, s12, v154
	v_add_f32_e32 v70, v70, v71
	v_cvt_pk_fp8_f32 v5, v6, v15 op_sel:[0,0,1]
	s_or_b32 s20, s0, 6
	v_add_f32_dpp v70, v70, v70 quad_perm:[1,0,3,2] row_mask:0xf bank_mask:0xf bound_ctrl:1
	s_mov_b32 s21, s1
	s_lshl_b64 s[8:9], s[20:21], 12
	v_add_f32_dpp v70, v70, v70 quad_perm:[2,3,0,1] row_mask:0xf bank_mask:0xf bound_ctrl:1
	s_lshl_b64 s[22:23], s[20:21], 13
	v_readlane_b32 s36, v253, 10
	v_add_f32_dpp v70, v70, v70 row_ror:4 row_mask:0xf bank_mask:0xf bound_ctrl:1
	v_readlane_b32 s37, v253, 11
	s_add_u32 s22, s36, s22
	v_add_f32_dpp v70, v70, v70 row_ror:8 row_mask:0xf bank_mask:0xf bound_ctrl:1
	global_store_dwordx2 v[12:13], v[4:5], off offset:1536
	v_lshl_add_u64 v[4:5], v[130:131], 0, s[8:9]
	s_addc_u32 s23, s37, s23
	v_readlane_b32 s3, v70, 16
	v_readlane_b32 s28, v70, 48
	global_load_dwordx4 v[88:91], v[4:5], off
	global_load_dwordx4 v[80:83], v[4:5], off offset:1024
	global_load_dwordx4 v[72:75], v[4:5], off offset:2048
	global_load_dwordx4 v[64:67], v[4:5], off offset:3072
	global_load_dwordx4 v[48:51], v122, s[22:23] offset:16
	global_load_dwordx4 v[56:59], v122, s[22:23]
	global_load_dwordx4 v[36:39], v122, s[22:23] offset:2064
	global_load_dwordx4 v[44:47], v122, s[22:23] offset:2048
	global_load_dwordx4 v[20:23], v149, s[22:23] offset:16
	global_load_dwordx4 v[28:31], v149, s[22:23]
	global_load_dwordx4 v[4:7], v150, s[22:23] offset:16
	global_load_dwordx4 v[12:15], v150, s[22:23]
	v_readlane_b32 s22, v70, 0
	v_readlane_b32 s23, v70, 32
	v_mov_b32_e32 v70, s3
	v_mov_b32_e32 v71, s28
	v_pk_add_f32 v[70:71], s[22:23], v[70:71]
	ds_read_b128 v[94:97], v144
	ds_read_b128 v[98:101], v144 offset:16
	v_add_f32_e32 v70, v70, v71
	v_fmamk_f32 v70, v70, 0x3a000000, v151
	v_cmp_gt_f32_e32 vcc, s11, v70
	v_mul_f32_e32 v71, 0x4b800000, v70
	v_readlane_b32 s38, v253, 12
	v_cndmask_b32_e32 v70, v70, v71, vcc
	v_rsq_f32_e32 v70, v70
	v_readlane_b32 s39, v253, 13
	v_readlane_b32 s40, v253, 14
	v_readlane_b32 s41, v253, 15
	v_mul_f32_e32 v71, 0x45800000, v70
	v_cndmask_b32_e32 v70, v70, v71, vcc
	v_mul_f32_e32 v71, v70, v102
	ds_read_b128 v[102:105], v144 offset:8192
	v_mul_f32_e32 v93, v70, v93
	v_readlane_b32 s42, v253, 16
	v_readlane_b32 s43, v253, 17
	v_readlane_b32 s44, v253, 18
	s_waitcnt lgkmcnt(0)
	v_mul_f32_e32 v71, v102, v71
	s_waitcnt vmcnt(26)
	v_fma_f32 v60, v94, v71, v60
	v_mul_f32_e32 v71, v70, v106
	v_mul_f32_e32 v94, v70, v107
	v_mul_f32_e32 v71, v103, v71
	v_mul_f32_e32 v94, v104, v94
	v_mul_f32_e32 v93, v105, v93
	v_fma_f32 v61, v95, v71, v61
	v_fma_f32 v62, v96, v94, v62
	v_fmac_f32_e32 v63, v97, v93
	ds_read_b128 v[94:97], v144 offset:8208
	v_mul_f32_e32 v93, v70, v108
	v_mul_f32_e32 v71, v61, v61
	v_fmac_f32_e32 v71, v60, v60
	v_fmac_f32_e32 v71, v62, v62
	s_waitcnt lgkmcnt(0)
	v_mul_f32_e32 v93, v93, v94
	v_fma_f32 v93, v98, v93, v52
	v_mul_f32_e32 v52, v70, v109
	v_mul_f32_e32 v52, v52, v95
	v_fma_f32 v94, v99, v52, v53
	v_mul_f32_e32 v52, v70, v110
	v_fmac_f32_e32 v71, v63, v63
	v_mul_f32_e32 v52, v52, v96
	v_fmac_f32_e32 v71, v93, v93
	v_fma_f32 v95, v100, v52, v54
	v_mul_f32_e32 v52, v70, v111
	v_fmac_f32_e32 v71, v94, v94
	v_mul_f32_e32 v52, v52, v97
	v_fmac_f32_e32 v71, v95, v95
	v_fmac_f32_e32 v55, v101, v52
	v_cvt_pk_bf16_f32 v52, v60, v61
	v_lshl_add_u64 v[60:61], v[132:133], 0, s[26:27]
	v_fmac_f32_e32 v71, v55, v55
	v_cvt_pk_bf16_f32 v53, v62, v63
	v_cvt_pk_bf16_f32 v54, v93, v94
	v_cvt_pk_bf16_f32 v55, v95, v55
	global_store_dwordx4 v[60:61], v[52:55], off
	ds_read_b128 v[94:97], v144 offset:2048
	ds_read_b128 v[98:101], v144 offset:2064
	ds_read_b128 v[102:105], v144 offset:10240
	v_mul_f32_e32 v62, v70, v112
	v_readlane_b32 s45, v253, 19
	v_readlane_b32 s46, v253, 20
	v_readlane_b32 s47, v253, 21
	s_waitcnt lgkmcnt(0)
	v_mul_f32_e32 v62, v62, v102
	s_waitcnt vmcnt(25)
	v_fma_f32 v40, v94, v62, v40
	v_mul_f32_e32 v62, v70, v113
	v_mul_f32_e32 v62, v62, v103
	v_fma_f32 v41, v95, v62, v41
	v_mul_f32_e32 v62, v70, v114
	v_mul_f32_e32 v62, v62, v104
	v_fma_f32 v42, v96, v62, v42
	v_mul_f32_e32 v62, v70, v115
	v_mul_f32_e32 v62, v62, v105
	v_fmac_f32_e32 v43, v97, v62
	ds_read_b128 v[94:97], v144 offset:10256
	v_mul_f32_e32 v62, v70, v116
	v_fmac_f32_e32 v71, v40, v40
	v_fmac_f32_e32 v71, v41, v41
	v_fmac_f32_e32 v71, v42, v42
	s_waitcnt lgkmcnt(0)
	v_mul_f32_e32 v62, v62, v94
	v_fma_f32 v62, v98, v62, v32
	v_mul_f32_e32 v32, v70, v117
	v_mul_f32_e32 v32, v32, v95
	v_fma_f32 v63, v99, v32, v33
	v_mul_f32_e32 v32, v70, v118
	v_fmac_f32_e32 v71, v43, v43
	v_mul_f32_e32 v32, v32, v96
	v_fmac_f32_e32 v71, v62, v62
	v_fma_f32 v93, v100, v32, v34
	v_mul_f32_e32 v32, v70, v119
	v_fmac_f32_e32 v71, v63, v63
	v_mul_f32_e32 v32, v32, v97
	v_fmac_f32_e32 v71, v93, v93
	v_fmac_f32_e32 v35, v101, v32
	v_fmac_f32_e32 v71, v35, v35
	v_cvt_pk_bf16_f32 v32, v40, v41
	v_cvt_pk_bf16_f32 v33, v42, v43
	v_cvt_pk_bf16_f32 v34, v62, v63
	v_cvt_pk_bf16_f32 v35, v93, v35
	global_store_dwordx4 v[60:61], v[32:35], off offset:1024
	ds_read_b128 v[40:43], v144 offset:4096
	ds_read_b128 v[94:97], v144 offset:4112
	ds_read_b128 v[98:101], v144 offset:12288
	v_mul_f32_e32 v62, v70, v129
	v_readlane_b32 s48, v253, 22
	v_readlane_b32 s49, v253, 23
	v_readlane_b32 s50, v253, 24
	s_waitcnt lgkmcnt(0)
	v_mul_f32_e32 v62, v62, v98
	s_waitcnt vmcnt(24)
	v_fma_f32 v24, v40, v62, v24
	v_mul_f32_e32 v40, v70, v157
	v_mul_f32_e32 v40, v40, v99
	v_fma_f32 v25, v41, v40, v25
	v_mul_f32_e32 v40, v70, v158
	v_mul_f32_e32 v40, v40, v100
	v_fma_f32 v26, v42, v40, v26
	v_mul_f32_e32 v40, v70, v159
	v_mul_f32_e32 v40, v40, v101
	v_fmac_f32_e32 v27, v43, v40
	ds_read_b128 v[40:43], v144 offset:12304
	v_mul_f32_e32 v62, v70, v160
	v_fmac_f32_e32 v71, v24, v24
	v_fmac_f32_e32 v71, v25, v25
	v_fmac_f32_e32 v71, v26, v26
	s_waitcnt lgkmcnt(0)
	v_mul_f32_e32 v40, v62, v40
	v_fma_f32 v40, v94, v40, v16
	v_mul_f32_e32 v16, v70, v92
	v_mul_f32_e32 v16, v16, v41
	v_fma_f32 v41, v95, v16, v17
	v_mul_f32_e32 v16, v70, v86
	v_fmac_f32_e32 v71, v27, v27
	v_mul_f32_e32 v16, v16, v42
	v_fmac_f32_e32 v71, v40, v40
	v_fma_f32 v42, v96, v16, v18
	v_mul_f32_e32 v16, v70, v85
	v_fmac_f32_e32 v71, v41, v41
	v_mul_f32_e32 v16, v16, v43
	v_fmac_f32_e32 v71, v42, v42
	v_fmac_f32_e32 v19, v97, v16
	v_fmac_f32_e32 v71, v19, v19
	v_cvt_pk_bf16_f32 v16, v24, v25
	v_cvt_pk_bf16_f32 v17, v26, v27
	v_cvt_pk_bf16_f32 v18, v40, v41
	v_cvt_pk_bf16_f32 v19, v42, v19
	global_store_dwordx4 v[60:61], v[16:19], off offset:2048
	ds_read_b128 v[24:27], v144 offset:6144
	ds_read_b128 v[40:43], v144 offset:6160
	ds_read_b128 v[92:95], v144 offset:14336
	v_mul_f32_e32 v62, v70, v87
	v_readlane_b32 s51, v253, 25
	s_waitcnt lgkmcnt(0)
	v_mul_f32_e32 v62, v62, v92
	s_waitcnt vmcnt(23)
	v_fma_f32 v62, v24, v62, v8
	v_mul_f32_e32 v8, v70, v84
	v_mul_f32_e32 v8, v8, v93
	v_fmac_f32_e32 v71, v62, v62
	v_fma_f32 v63, v25, v8, v9
	v_fmac_f32_e32 v71, v63, v63
	v_pk_mul_f32 v[8:9], v[70:71], v[76:77] op_sel_hi:[0,1]
	v_pk_mul_f32 v[8:9], v[8:9], v[94:95] op_sel:[1,0] op_sel_hi:[0,1]
	v_pk_fma_f32 v[24:25], v[26:27], v[8:9], v[10:11]
	s_nop 0
	v_pk_mul_f32 v[8:9], v[24:25], v[24:25]
	s_nop 0
	v_add_f32_e32 v8, v71, v8
	v_add_f32_e32 v71, v8, v9
	ds_read_b128 v[8:11], v144 offset:14352
	v_pk_mul_f32 v[26:27], v[70:71], v[78:79] op_sel_hi:[0,1]
	s_waitcnt lgkmcnt(0)
	v_pk_mul_f32 v[8:9], v[26:27], v[8:9] op_sel:[1,0] op_sel_hi:[0,1]
	v_pk_fma_f32 v[8:9], v[40:41], v[8:9], v[0:1]
	s_nop 0
	v_pk_mul_f32 v[0:1], v[8:9], v[8:9]
	s_nop 0
	v_add_f32_e32 v0, v71, v0
	v_add_f32_e32 v26, v0, v1
	v_pk_mul_f32 v[0:1], v[70:71], v[68:69] op_sel_hi:[0,1]
	v_pk_mul_f32 v[0:1], v[0:1], v[10:11] op_sel:[1,0] op_sel_hi:[0,1]
	v_pk_fma_f32 v[10:11], v[42:43], v[0:1], v[2:3]
	s_nop 0
	v_pk_mul_f32 v[0:1], v[10:11], v[10:11]
	s_nop 0
	v_add_f32_e32 v0, v26, v0
	v_add_f32_e32 v26, v0, v1
	v_cvt_pk_bf16_f32 v0, v62, v63
	v_cvt_pk_bf16_f32 v1, v24, v25
	v_cvt_pk_bf16_f32 v2, v8, v9
	v_cvt_pk_bf16_f32 v3, v10, v11
	global_store_dwordx4 v[60:61], v[0:3], off offset:3072
	s_nop 0
	v_add_f32_dpp v8, v26, v26 quad_perm:[1,0,3,2] row_mask:0xf bank_mask:0xf bound_ctrl:1
	s_nop 1
	v_add_f32_dpp v8, v8, v8 quad_perm:[2,3,0,1] row_mask:0xf bank_mask:0xf bound_ctrl:1
	s_nop 1
	v_add_f32_dpp v8, v8, v8 row_ror:4 row_mask:0xf bank_mask:0xf bound_ctrl:1
	s_nop 1
	v_add_f32_dpp v8, v8, v8 row_ror:8 row_mask:0xf bank_mask:0xf bound_ctrl:1
	s_nop 0
	v_readlane_b32 s3, v8, 16
	v_readlane_b32 s26, v8, 48
	v_readlane_b32 s22, v8, 0
	v_readlane_b32 s23, v8, 32
	v_mov_b32_e32 v8, s3
	v_mov_b32_e32 v9, s26
	v_pk_add_f32 v[8:9], s[22:23], v[8:9]
	s_nop 0
	v_add_f32_e32 v8, v8, v9
	v_fmamk_f32 v8, v8, 0x3a000000, v151
	v_cmp_gt_f32_e32 vcc, s11, v8
	v_mul_f32_e32 v9, 0x4b800000, v8
	s_nop 0
	v_cndmask_b32_e32 v8, v8, v9, vcc
	v_rsq_f32_e32 v8, v8
	s_nop 0
	v_mul_f32_e32 v9, 0x45800000, v8
	v_cndmask_b32_e32 v10, v8, v9, vcc
	s_and_saveexec_b64 s[22:23], s[6:7]
	v_mov_b32_e32 v8, s10
	ds_write_b32 v8, v10 offset:60692
	s_or_b64 exec, exec, s[22:23]
	v_lshlrev_b32_e32 v8, 16, v52
	v_and_b32_e32 v9, 0xffff0000, v52
	v_lshlrev_b32_e32 v11, 16, v53
	v_and_b32_e32 v60, 0xffff0000, v53
	v_lshlrev_b32_e32 v61, 16, v54
	v_and_b32_e32 v62, 0xffff0000, v54
	v_lshlrev_b32_e32 v63, 16, v55
	v_and_b32_e32 v68, 0xffff0000, v55
	ds_read_b128 v[24:27], v144 offset:16384
	ds_read_b128 v[40:43], v144 offset:16400
	ds_read_b128 v[52:55], v144 offset:32768
	v_mul_f32_e32 v8, v10, v8
	v_mul_f32_e32 v9, v10, v9
	v_mul_f32_e32 v11, v10, v11
	s_lshl_b64 s[22:23], s[24:25], 11
	s_waitcnt lgkmcnt(0)
	v_fma_f32 v8, v8, v24, v52
	v_mul_f32_e32 v24, v10, v60
	v_fma_f32 v9, v9, v25, v53
	v_fma_f32 v11, v11, v26, v54
	v_fmac_f32_e32 v55, v24, v27
	ds_read_b128 v[24:27], v144 offset:32784
	v_mul_f32_e32 v52, v10, v61
	v_med3_f32 v8, v8, s12, v154
	v_med3_f32 v9, v9, s12, v154
	v_med3_f32 v11, v11, s12, v154
	s_waitcnt lgkmcnt(0)
	v_fma_f32 v40, v52, v40, v24
	v_mul_f32_e32 v24, v10, v62
	v_fma_f32 v25, v24, v41, v25
	v_mul_f32_e32 v24, v10, v63
	v_fma_f32 v26, v24, v42, v26
	v_mul_f32_e32 v24, v10, v68
	v_fmac_f32_e32 v27, v24, v43
	v_mov_b32_e32 v24, 0
	v_cvt_pk_fp8_f32 v24, v8, v9
	v_med3_f32 v8, v40, s12, v154
	v_med3_f32 v9, v25, s12, v154
	v_mov_b32_e32 v25, 0
	v_cvt_pk_fp8_f32 v25, v8, v9
	v_med3_f32 v41, v55, s12, v154
	v_cvt_pk_fp8_f32 v24, v11, v41 op_sel:[0,0,1]
	v_med3_f32 v11, v26, s12, v154
	v_med3_f32 v26, v27, s12, v154
	v_cvt_pk_fp8_f32 v25, v11, v26 op_sel:[0,0,1]
	v_lshl_add_u64 v[8:9], v[134:135], 0, s[22:23]
	v_lshlrev_b32_e32 v11, 16, v32
	v_and_b32_e32 v40, 0xffff0000, v32
	global_store_dwordx2 v[8:9], v[24:25], off
	v_lshlrev_b32_e32 v41, 16, v33
	v_and_b32_e32 v42, 0xffff0000, v33
	v_lshlrev_b32_e32 v43, 16, v34
	v_and_b32_e32 v52, 0xffff0000, v34
	v_lshlrev_b32_e32 v53, 16, v35
	v_and_b32_e32 v54, 0xffff0000, v35
	ds_read_b128 v[24:27], v144 offset:18432
	ds_read_b128 v[32:35], v144 offset:34816
	v_mul_f32_e32 v11, v10, v11
	s_waitcnt vmcnt(16)
	v_and_b32_e32 v108, 0xffff0000, v88
	v_lshlrev_b32_e32 v104, 16, v88
	v_mul_f32_e32 v96, v108, v108
	s_waitcnt lgkmcnt(0)
	v_fma_f32 v11, v11, v24, v32
	v_mul_f32_e32 v24, v10, v40
	v_fma_f32 v32, v24, v25, v33
	v_mul_f32_e32 v24, v10, v41
	v_fma_f32 v33, v24, v26, v34
	v_mul_f32_e32 v24, v10, v42
	v_fmac_f32_e32 v35, v24, v27
	v_mul_f32_e32 v34, v10, v43
	ds_read_b128 v[24:27], v144 offset:18448
	ds_read_b128 v[40:43], v144 offset:34832
	v_med3_f32 v11, v11, s12, v154
	v_lshlrev_b32_e32 v109, 16, v89
	v_fmac_f32_e32 v96, v104, v104
	v_and_b32_e32 v89, 0xffff0000, v89
	s_waitcnt lgkmcnt(0)
	v_fma_f32 v34, v34, v24, v40
	v_mul_f32_e32 v24, v10, v52
	v_fma_f32 v25, v24, v25, v41
	v_mul_f32_e32 v24, v10, v53
	v_fma_f32 v26, v24, v26, v42
	v_mul_f32_e32 v24, v10, v54
	v_fmac_f32_e32 v43, v24, v27
	v_med3_f32 v27, v32, s12, v154
	v_mov_b32_e32 v24, 0
	v_cvt_pk_fp8_f32 v24, v11, v27
	v_med3_f32 v11, v34, s12, v154
	v_med3_f32 v27, v25, s12, v154
	v_mov_b32_e32 v25, 0
	v_cvt_pk_fp8_f32 v25, v11, v27
	v_med3_f32 v32, v33, s12, v154
	v_med3_f32 v33, v35, s12, v154
	v_cvt_pk_fp8_f32 v24, v32, v33 op_sel:[0,0,1]
	v_med3_f32 v26, v26, s12, v154
	v_med3_f32 v32, v43, s12, v154
	v_cvt_pk_fp8_f32 v25, v26, v32 op_sel:[0,0,1]
	v_lshlrev_b32_e32 v11, 16, v16
	v_and_b32_e32 v32, 0xffff0000, v16
	v_lshlrev_b32_e32 v33, 16, v17
	global_store_dwordx2 v[8:9], v[24:25], off offset:512
	v_and_b32_e32 v34, 0xffff0000, v17
	v_lshlrev_b32_e32 v35, 16, v18
	v_and_b32_e32 v40, 0xffff0000, v18
	v_lshlrev_b32_e32 v41, 16, v19
	v_and_b32_e32 v42, 0xffff0000, v19
	ds_read_b128 v[16:19], v144 offset:20480
	ds_read_b128 v[24:27], v144 offset:36864
	v_mul_f32_e32 v11, v10, v11
	v_fmac_f32_e32 v96, v109, v109
	v_lshlrev_b32_e32 v110, 16, v90
	v_fmac_f32_e32 v96, v89, v89
	s_waitcnt lgkmcnt(0)
	v_fma_f32 v11, v11, v16, v24
	v_mul_f32_e32 v16, v10, v32
	v_fma_f32 v24, v16, v17, v25
	v_mul_f32_e32 v16, v10, v33
	v_fma_f32 v25, v16, v18, v26
	v_mul_f32_e32 v16, v10, v34
	v_fmac_f32_e32 v27, v16, v19
	v_mul_f32_e32 v26, v10, v35
	ds_read_b128 v[16:19], v144 offset:20496
	ds_read_b128 v[32:35], v144 offset:36880
	v_med3_f32 v11, v11, s12, v154
	v_and_b32_e32 v90, 0xffff0000, v90
	v_fmac_f32_e32 v96, v110, v110
	v_lshlrev_b32_e32 v111, 16, v91
	s_waitcnt lgkmcnt(0)
	v_fma_f32 v26, v26, v16, v32
	v_mul_f32_e32 v16, v10, v40
	v_fma_f32 v17, v16, v17, v33
	v_mul_f32_e32 v16, v10, v41
	v_fma_f32 v18, v16, v18, v34
	v_mul_f32_e32 v16, v10, v42
	v_fmac_f32_e32 v35, v16, v19
	v_med3_f32 v19, v24, s12, v154
	v_mov_b32_e32 v16, 0
	v_cvt_pk_fp8_f32 v16, v11, v19
	v_med3_f32 v11, v26, s12, v154
	v_med3_f32 v19, v17, s12, v154
	v_mov_b32_e32 v17, 0
	v_cvt_pk_fp8_f32 v17, v11, v19
	v_med3_f32 v24, v25, s12, v154
	v_med3_f32 v25, v27, s12, v154
	v_cvt_pk_fp8_f32 v16, v24, v25 op_sel:[0,0,1]
	v_med3_f32 v18, v18, s12, v154
	v_med3_f32 v24, v35, s12, v154
	v_fmac_f32_e32 v96, v90, v90
	v_cvt_pk_fp8_f32 v17, v18, v24 op_sel:[0,0,1]
	v_and_b32_e32 v91, 0xffff0000, v91
	v_fmac_f32_e32 v96, v111, v111
	v_fmac_f32_e32 v96, v91, v91
	s_waitcnt vmcnt(16)
	v_lshlrev_b32_e32 v112, 16, v80
	v_and_b32_e32 v113, 0xffff0000, v80
	v_fmac_f32_e32 v96, v112, v112
	v_lshlrev_b32_e32 v114, 16, v81
	v_fmac_f32_e32 v96, v113, v113
	global_store_dwordx2 v[8:9], v[16:17], off offset:1024
	v_and_b32_e32 v115, 0xffff0000, v81
	v_fmac_f32_e32 v96, v114, v114
	v_lshlrev_b32_e32 v11, 16, v0
	v_and_b32_e32 v24, 0xffff0000, v0
	v_lshlrev_b32_e32 v25, 16, v1
	v_and_b32_e32 v26, 0xffff0000, v1
	v_lshlrev_b32_e32 v27, 16, v2
	v_and_b32_e32 v32, 0xffff0000, v2
	v_lshlrev_b32_e32 v33, 16, v3
	v_and_b32_e32 v34, 0xffff0000, v3
	ds_read_b128 v[0:3], v144 offset:22528
	ds_read_b128 v[16:19], v144 offset:38912
	v_lshlrev_b32_e32 v116, 16, v82
	v_fmac_f32_e32 v96, v115, v115
	v_and_b32_e32 v117, 0xffff0000, v82
	v_fmac_f32_e32 v96, v116, v116
	v_lshlrev_b32_e32 v118, 16, v83
	v_fmac_f32_e32 v96, v117, v117
	v_and_b32_e32 v119, 0xffff0000, v83
	v_fmac_f32_e32 v96, v118, v118
	v_mul_f32_e32 v11, v10, v11
	v_fmac_f32_e32 v96, v119, v119
	s_waitcnt vmcnt(16)
	v_lshlrev_b32_e32 v129, 16, v72
	s_waitcnt lgkmcnt(0)
	v_fma_f32 v11, v11, v0, v16
	v_mul_f32_e32 v0, v10, v24
	v_and_b32_e32 v157, 0xffff0000, v72
	v_fmac_f32_e32 v96, v129, v129
	v_fma_f32 v16, v0, v1, v17
	v_mul_f32_e32 v0, v10, v25
	v_lshlrev_b32_e32 v158, 16, v73
	v_fmac_f32_e32 v96, v157, v157
	v_fma_f32 v17, v0, v2, v18
	v_mul_f32_e32 v0, v10, v26
	v_and_b32_e32 v159, 0xffff0000, v73
	v_fmac_f32_e32 v96, v158, v158
	v_fmac_f32_e32 v19, v0, v3
	v_mul_f32_e32 v18, v10, v27
	ds_read_b128 v[0:3], v144 offset:22544
	ds_read_b128 v[24:27], v144 offset:38928
	v_lshlrev_b32_e32 v160, 16, v74
	v_fmac_f32_e32 v96, v159, v159
	v_and_b32_e32 v88, 0xffff0000, v74
	v_fmac_f32_e32 v96, v160, v160
	v_lshlrev_b32_e32 v82, 16, v75
	v_fmac_f32_e32 v96, v88, v88
	v_and_b32_e32 v81, 0xffff0000, v75
	v_fmac_f32_e32 v96, v82, v82
	v_fmac_f32_e32 v96, v81, v81
	s_waitcnt vmcnt(15)
	v_lshlrev_b32_e32 v83, 16, v64
	s_waitcnt lgkmcnt(0)
	v_fma_f32 v18, v18, v0, v24
	v_mul_f32_e32 v0, v10, v32
	v_and_b32_e32 v80, 0xffff0000, v64
	v_fmac_f32_e32 v96, v83, v83
	v_and_b32_e32 v72, 0xffff0000, v65
	v_lshlrev_b32_e32 v73, 16, v65
	v_fma_f32 v1, v0, v1, v25
	v_mul_f32_e32 v0, v10, v33
	v_fmac_f32_e32 v96, v80, v80
	v_pk_mul_f32 v[64:65], v[72:73], v[72:73]
	v_fma_f32 v2, v0, v2, v26
	v_mul_f32_e32 v0, v10, v34
	v_add_f32_e32 v65, v65, v96
	v_and_b32_e32 v74, 0xffff0000, v66
	v_lshlrev_b32_e32 v75, 16, v66
	v_fmac_f32_e32 v27, v0, v3
	v_med3_f32 v3, v11, s12, v154
	v_med3_f32 v10, v16, s12, v154
	v_mov_b32_e32 v0, 0
	v_add_f32_e32 v96, v64, v65
	v_pk_mul_f32 v[64:65], v[74:75], v[74:75]
	v_cvt_pk_fp8_f32 v0, v3, v10
	v_med3_f32 v3, v18, s12, v154
	v_med3_f32 v10, v1, s12, v154
	v_mov_b32_e32 v1, 0
	v_add_f32_e32 v65, v65, v96
	v_cvt_pk_fp8_f32 v1, v3, v10
	v_add_f32_e32 v96, v64, v65
	v_and_b32_e32 v64, 0xffff0000, v67
	v_lshlrev_b32_e32 v65, 16, v67
	v_pk_mul_f32 v[66:67], v[64:65], v[64:65]
	v_med3_f32 v11, v17, s12, v154
	v_med3_f32 v16, v19, s12, v154
	v_add_f32_e32 v67, v67, v96
	v_cvt_pk_fp8_f32 v0, v11, v16 op_sel:[0,0,1]
	v_med3_f32 v2, v2, s12, v154
	v_med3_f32 v11, v27, s12, v154
	v_add_f32_e32 v66, v66, v67
	v_cvt_pk_fp8_f32 v1, v2, v11 op_sel:[0,0,1]
	s_or_b32 s0, s0, 7
	v_add_f32_dpp v66, v66, v66 quad_perm:[1,0,3,2] row_mask:0xf bank_mask:0xf bound_ctrl:1
	s_lshl_b64 s[22:23], s[0:1], 12
	s_lshl_b64 s[24:25], s[0:1], 13
	v_add_f32_dpp v66, v66, v66 quad_perm:[2,3,0,1] row_mask:0xf bank_mask:0xf bound_ctrl:1
	v_readlane_b32 s36, v253, 10
	v_readlane_b32 s37, v253, 11
	v_add_f32_dpp v66, v66, v66 row_ror:4 row_mask:0xf bank_mask:0xf bound_ctrl:1
	s_add_u32 s24, s36, s24
	global_store_dwordx2 v[8:9], v[0:1], off offset:1536
	v_add_f32_dpp v66, v66, v66 row_ror:8 row_mask:0xf bank_mask:0xf bound_ctrl:1
	v_lshl_add_u64 v[0:1], v[130:131], 0, s[22:23]
	s_addc_u32 s25, s37, s25
	v_readlane_b32 s3, v66, 16
	v_readlane_b32 s26, v66, 48
	global_load_dwordx4 v[92:95], v[0:1], off
	global_load_dwordx4 v[84:87], v[0:1], off offset:1024
	global_load_dwordx4 v[76:79], v[0:1], off offset:2048
	global_load_dwordx4 v[68:71], v[0:1], off offset:3072
	global_load_dwordx4 v[52:55], v122, s[24:25] offset:16
	global_load_dwordx4 v[60:63], v122, s[24:25]
	global_load_dwordx4 v[32:35], v122, s[24:25] offset:2064
	global_load_dwordx4 v[40:43], v122, s[24:25] offset:2048
	global_load_dwordx4 v[16:19], v149, s[24:25] offset:16
	global_load_dwordx4 v[24:27], v149, s[24:25]
	global_load_dwordx4 v[0:3], v150, s[24:25] offset:16
	global_load_dwordx4 v[8:11], v150, s[24:25]
	v_readlane_b32 s24, v66, 0
	v_readlane_b32 s25, v66, 32
	v_mov_b32_e32 v66, s3
	v_mov_b32_e32 v67, s26
	v_pk_add_f32 v[66:67], s[24:25], v[66:67]
	ds_read_b128 v[96:99], v144
	ds_read_b128 v[100:103], v144 offset:16
	v_add_f32_e32 v66, v66, v67
	v_fmamk_f32 v66, v66, 0x3a000000, v151
	v_cmp_gt_f32_e32 vcc, s11, v66
	v_mul_f32_e32 v67, 0x4b800000, v66
	v_readlane_b32 s38, v253, 12
	v_cndmask_b32_e32 v66, v66, v67, vcc
	v_rsq_f32_e32 v66, v66
	v_readlane_b32 s39, v253, 13
	v_readlane_b32 s40, v253, 14
	v_readlane_b32 s41, v253, 15
	v_mul_f32_e32 v67, 0x45800000, v66
	v_cndmask_b32_e32 v66, v66, v67, vcc
	v_mul_f32_e32 v67, v66, v104
	ds_read_b128 v[104:107], v144 offset:8192
	v_mul_f32_e32 v89, v66, v89
	v_readlane_b32 s42, v253, 16
	v_readlane_b32 s43, v253, 17
	v_readlane_b32 s44, v253, 18
	s_waitcnt lgkmcnt(0)
	v_mul_f32_e32 v67, v104, v67
	s_waitcnt vmcnt(26)
	v_fma_f32 v56, v96, v67, v56
	v_mul_f32_e32 v67, v66, v108
	v_mul_f32_e32 v96, v66, v109
	v_mul_f32_e32 v67, v105, v67
	v_mul_f32_e32 v96, v106, v96
	v_mul_f32_e32 v89, v107, v89
	v_fma_f32 v57, v97, v67, v57
	v_fma_f32 v58, v98, v96, v58
	v_fmac_f32_e32 v59, v99, v89
	ds_read_b128 v[96:99], v144 offset:8208
	v_mul_f32_e32 v89, v66, v110
	v_mul_f32_e32 v67, v57, v57
	v_fmac_f32_e32 v67, v56, v56
	v_fmac_f32_e32 v67, v58, v58
	s_waitcnt lgkmcnt(0)
	v_mul_f32_e32 v89, v89, v96
	v_fma_f32 v89, v100, v89, v48
	v_mul_f32_e32 v48, v66, v90
	v_mul_f32_e32 v48, v48, v97
	v_fma_f32 v90, v101, v48, v49
	v_mul_f32_e32 v48, v66, v111
	v_fmac_f32_e32 v67, v59, v59
	v_mul_f32_e32 v48, v48, v98
	v_fmac_f32_e32 v67, v89, v89
	v_fma_f32 v96, v102, v48, v50
	v_mul_f32_e32 v48, v66, v91
	v_fmac_f32_e32 v67, v90, v90
	v_mul_f32_e32 v48, v48, v99
	v_fmac_f32_e32 v67, v96, v96
	v_fmac_f32_e32 v51, v103, v48
	v_cvt_pk_bf16_f32 v48, v56, v57
	v_lshl_add_u64 v[56:57], v[132:133], 0, s[8:9]
	v_fmac_f32_e32 v67, v51, v51
	v_cvt_pk_bf16_f32 v49, v58, v59
	v_cvt_pk_bf16_f32 v50, v89, v90
	v_cvt_pk_bf16_f32 v51, v96, v51
	global_store_dwordx4 v[56:57], v[48:51], off
	ds_read_b128 v[96:99], v144 offset:2048
	ds_read_b128 v[100:103], v144 offset:2064
	ds_read_b128 v[104:107], v144 offset:10240
	v_mul_f32_e32 v58, v66, v112
	v_readlane_b32 s45, v253, 19
	v_readlane_b32 s46, v253, 20
	v_readlane_b32 s47, v253, 21
	s_waitcnt lgkmcnt(0)
	v_mul_f32_e32 v58, v58, v104
	s_waitcnt vmcnt(25)
	v_fma_f32 v44, v96, v58, v44
	v_mul_f32_e32 v58, v66, v113
	v_mul_f32_e32 v58, v58, v105
	v_fma_f32 v45, v97, v58, v45
	v_mul_f32_e32 v58, v66, v114
	v_mul_f32_e32 v58, v58, v106
	v_fma_f32 v46, v98, v58, v46
	v_mul_f32_e32 v58, v66, v115
	v_mul_f32_e32 v58, v58, v107
	v_fmac_f32_e32 v47, v99, v58
	ds_read_b128 v[96:99], v144 offset:10256
	v_mul_f32_e32 v58, v66, v116
	v_fmac_f32_e32 v67, v44, v44
	v_fmac_f32_e32 v67, v45, v45
	v_fmac_f32_e32 v67, v46, v46
	s_waitcnt lgkmcnt(0)
	v_mul_f32_e32 v58, v58, v96
	v_fma_f32 v58, v100, v58, v36
	v_mul_f32_e32 v36, v66, v117
	v_mul_f32_e32 v36, v36, v97
	v_fma_f32 v59, v101, v36, v37
	v_mul_f32_e32 v36, v66, v118
	v_fmac_f32_e32 v67, v47, v47
	v_mul_f32_e32 v36, v36, v98
	v_fmac_f32_e32 v67, v58, v58
	v_fma_f32 v89, v102, v36, v38
	v_mul_f32_e32 v36, v66, v119
	v_fmac_f32_e32 v67, v59, v59
	v_mul_f32_e32 v36, v36, v99
	v_fmac_f32_e32 v67, v89, v89
	v_fmac_f32_e32 v39, v103, v36
	v_fmac_f32_e32 v67, v39, v39
	v_cvt_pk_bf16_f32 v36, v44, v45
	v_cvt_pk_bf16_f32 v37, v46, v47
	v_cvt_pk_bf16_f32 v38, v58, v59
	v_cvt_pk_bf16_f32 v39, v89, v39
	global_store_dwordx4 v[56:57], v[36:39], off offset:1024
	ds_read_b128 v[44:47], v144 offset:4096
	ds_read_b128 v[96:99], v144 offset:4112
	ds_read_b128 v[100:103], v144 offset:12288
	v_mul_f32_e32 v58, v66, v129
	v_readlane_b32 s48, v253, 22
	v_readlane_b32 s49, v253, 23
	v_readlane_b32 s50, v253, 24
	s_waitcnt lgkmcnt(0)
	v_mul_f32_e32 v58, v58, v100
	s_waitcnt vmcnt(24)
	v_fma_f32 v28, v44, v58, v28
	v_mul_f32_e32 v44, v66, v157
	v_mul_f32_e32 v44, v44, v101
	v_fma_f32 v29, v45, v44, v29
	v_mul_f32_e32 v44, v66, v158
	v_mul_f32_e32 v44, v44, v102
	v_fma_f32 v30, v46, v44, v30
	v_mul_f32_e32 v44, v66, v159
	v_mul_f32_e32 v44, v44, v103
	v_fmac_f32_e32 v31, v47, v44
	ds_read_b128 v[44:47], v144 offset:12304
	v_mul_f32_e32 v58, v66, v160
	v_fmac_f32_e32 v67, v28, v28
	v_fmac_f32_e32 v67, v29, v29
	v_fmac_f32_e32 v67, v30, v30
	s_waitcnt lgkmcnt(0)
	v_mul_f32_e32 v44, v58, v44
	v_fma_f32 v44, v96, v44, v20
	v_mul_f32_e32 v20, v66, v88
	v_mul_f32_e32 v20, v20, v45
	v_fma_f32 v45, v97, v20, v21
	v_mul_f32_e32 v20, v66, v82
	v_fmac_f32_e32 v67, v31, v31
	v_mul_f32_e32 v20, v20, v46
	v_fmac_f32_e32 v67, v44, v44
	v_fma_f32 v46, v98, v20, v22
	v_mul_f32_e32 v20, v66, v81
	v_fmac_f32_e32 v67, v45, v45
	v_mul_f32_e32 v20, v20, v47
	v_fmac_f32_e32 v67, v46, v46
	v_fmac_f32_e32 v23, v99, v20
	v_fmac_f32_e32 v67, v23, v23
	v_cvt_pk_bf16_f32 v20, v28, v29
	v_cvt_pk_bf16_f32 v21, v30, v31
	v_cvt_pk_bf16_f32 v22, v44, v45
	v_cvt_pk_bf16_f32 v23, v46, v23
	global_store_dwordx4 v[56:57], v[20:23], off offset:2048
	ds_read_b128 v[28:31], v144 offset:6144
	ds_read_b128 v[44:47], v144 offset:6160
	ds_read_b128 v[88:91], v144 offset:14336
	v_mul_f32_e32 v58, v66, v83
	v_readlane_b32 s51, v253, 25
	s_waitcnt lgkmcnt(0)
	v_mul_f32_e32 v58, v58, v88
	s_waitcnt vmcnt(23)
	v_fma_f32 v58, v28, v58, v12
	v_mul_f32_e32 v12, v66, v80
	v_mul_f32_e32 v12, v12, v89
	v_fmac_f32_e32 v67, v58, v58
	v_fma_f32 v59, v29, v12, v13
	v_fmac_f32_e32 v67, v59, v59
	v_pk_mul_f32 v[12:13], v[66:67], v[72:73] op_sel_hi:[0,1]
	v_pk_mul_f32 v[12:13], v[12:13], v[90:91] op_sel:[1,0] op_sel_hi:[0,1]
	v_pk_fma_f32 v[28:29], v[30:31], v[12:13], v[14:15]
	s_nop 0
	v_pk_mul_f32 v[12:13], v[28:29], v[28:29]
	s_nop 0
	v_add_f32_e32 v12, v67, v12
	v_add_f32_e32 v67, v12, v13
	ds_read_b128 v[12:15], v144 offset:14352
	v_pk_mul_f32 v[30:31], v[66:67], v[74:75] op_sel_hi:[0,1]
	s_waitcnt lgkmcnt(0)
	v_pk_mul_f32 v[12:13], v[30:31], v[12:13] op_sel:[1,0] op_sel_hi:[0,1]
	v_pk_fma_f32 v[12:13], v[44:45], v[12:13], v[4:5]
	s_nop 0
	v_pk_mul_f32 v[4:5], v[12:13], v[12:13]
	s_nop 0
	v_add_f32_e32 v4, v67, v4
	v_add_f32_e32 v30, v4, v5
	v_pk_mul_f32 v[4:5], v[66:67], v[64:65] op_sel_hi:[0,1]
	v_pk_mul_f32 v[4:5], v[4:5], v[14:15] op_sel:[1,0] op_sel_hi:[0,1]
	v_pk_fma_f32 v[14:15], v[46:47], v[4:5], v[6:7]
	s_nop 0
	v_pk_mul_f32 v[4:5], v[14:15], v[14:15]
	s_nop 0
	v_add_f32_e32 v4, v30, v4
	v_add_f32_e32 v30, v4, v5
	v_cvt_pk_bf16_f32 v4, v58, v59
	v_cvt_pk_bf16_f32 v5, v28, v29
	v_cvt_pk_bf16_f32 v6, v12, v13
	v_cvt_pk_bf16_f32 v7, v14, v15
	global_store_dwordx4 v[56:57], v[4:7], off offset:3072
	s_nop 0
	v_add_f32_dpp v12, v30, v30 quad_perm:[1,0,3,2] row_mask:0xf bank_mask:0xf bound_ctrl:1
	s_nop 1
	v_add_f32_dpp v12, v12, v12 quad_perm:[2,3,0,1] row_mask:0xf bank_mask:0xf bound_ctrl:1
	s_nop 1
	v_add_f32_dpp v12, v12, v12 row_ror:4 row_mask:0xf bank_mask:0xf bound_ctrl:1
	s_nop 1
	v_add_f32_dpp v12, v12, v12 row_ror:8 row_mask:0xf bank_mask:0xf bound_ctrl:1
	s_nop 0
	v_readlane_b32 s3, v12, 16
	v_readlane_b32 s24, v12, 48
	v_readlane_b32 s8, v12, 0
	v_readlane_b32 s9, v12, 32
	v_mov_b32_e32 v12, s3
	v_mov_b32_e32 v13, s24
	v_pk_add_f32 v[12:13], s[8:9], v[12:13]
	s_nop 0
	v_add_f32_e32 v12, v12, v13
	v_fmamk_f32 v12, v12, 0x3a000000, v151
	v_cmp_gt_f32_e32 vcc, s11, v12
	v_mul_f32_e32 v13, 0x4b800000, v12
	s_nop 0
	v_cndmask_b32_e32 v12, v12, v13, vcc
	v_rsq_f32_e32 v12, v12
	s_nop 0
	v_mul_f32_e32 v13, 0x45800000, v12
	v_cndmask_b32_e32 v28, v12, v13, vcc
	s_and_saveexec_b64 s[8:9], s[6:7]
	v_mov_b32_e32 v12, s10
	ds_write_b32 v12, v28 offset:60696
	s_or_b64 exec, exec, s[8:9]
	ds_read_b128 v[12:15], v144 offset:16384
	ds_read_b128 v[44:47], v144 offset:32768
	v_lshlrev_b32_e32 v29, 16, v48
	v_and_b32_e32 v30, 0xffff0000, v48
	v_lshlrev_b32_e32 v31, 16, v49
	v_and_b32_e32 v64, 0xffff0000, v49
	v_lshlrev_b32_e32 v65, 16, v50
	v_and_b32_e32 v66, 0xffff0000, v50
	v_lshlrev_b32_e32 v67, 16, v51
	v_and_b32_e32 v72, 0xffff0000, v51
	v_mul_f32_e32 v29, v28, v29
	ds_read_b128 v[48:51], v144 offset:16400
	ds_read_b128 v[56:59], v144 offset:32784
	s_waitcnt lgkmcnt(2)
	v_fma_f32 v12, v29, v12, v44
	v_mul_f32_e32 v29, v28, v30
	v_fma_f32 v13, v29, v13, v45
	v_mul_f32_e32 v29, v28, v31
	v_fma_f32 v14, v29, v14, v46
	v_mul_f32_e32 v29, v28, v64
	v_fmac_f32_e32 v47, v29, v15
	v_mul_f32_e32 v15, v28, v65
	v_mul_f32_e32 v29, v28, v66
	v_mul_f32_e32 v31, v28, v72
	s_waitcnt lgkmcnt(0)
	v_fma_f32 v15, v15, v48, v56
	v_fma_f32 v29, v29, v49, v57
	v_fmac_f32_e32 v59, v31, v51
	v_med3_f32 v12, v12, s12, v154
	v_med3_f32 v13, v13, s12, v154
	v_med3_f32 v31, v14, s12, v154
	v_mov_b32_e32 v14, 0
	v_cvt_pk_fp8_f32 v14, v12, v13
	v_med3_f32 v12, v15, s12, v154
	v_med3_f32 v13, v29, s12, v154
	v_mov_b32_e32 v15, 0
	v_cvt_pk_fp8_f32 v15, v12, v13
	v_mul_f32_e32 v30, v28, v67
	v_fma_f32 v30, v30, v50, v58
	v_med3_f32 v44, v47, s12, v154
	v_med3_f32 v12, v30, s12, v154
	v_med3_f32 v13, v59, s12, v154
	v_cvt_pk_fp8_f32 v14, v31, v44 op_sel:[0,0,1]
	v_cvt_pk_fp8_f32 v15, v12, v13 op_sel:[0,0,1]
	s_lshl_b64 s[8:9], s[20:21], 11
	v_lshl_add_u64 v[12:13], v[134:135], 0, s[8:9]
	v_lshlrev_b32_e32 v29, 16, v37
	global_store_dwordx2 v[12:13], v[14:15], off
	ds_read_b128 v[44:47], v144 offset:18432
	ds_read_b128 v[48:51], v144 offset:34816
	v_lshlrev_b32_e32 v14, 16, v36
	v_and_b32_e32 v15, 0xffff0000, v36
	v_and_b32_e32 v30, 0xffff0000, v37
	v_lshlrev_b32_e32 v31, 16, v38
	v_and_b32_e32 v64, 0xffff0000, v38
	v_lshlrev_b32_e32 v65, 16, v39
	v_and_b32_e32 v66, 0xffff0000, v39
	ds_read_b128 v[36:39], v144 offset:18448
	ds_read_b128 v[56:59], v144 offset:34832
	v_mul_f32_e32 v30, v28, v30
	v_mul_f32_e32 v14, v28, v14
	v_mul_f32_e32 v15, v28, v15
	s_waitcnt lgkmcnt(2)
	v_fmac_f32_e32 v51, v30, v47
	v_mul_f32_e32 v30, v28, v31
	v_mul_f32_e32 v31, v28, v64
	v_fma_f32 v14, v14, v44, v48
	v_fma_f32 v15, v15, v45, v49
	s_waitcnt lgkmcnt(0)
	v_fma_f32 v31, v31, v37, v57
	v_mul_f32_e32 v37, v28, v66
	v_fmac_f32_e32 v59, v37, v39
	v_med3_f32 v37, v14, s12, v154
	v_med3_f32 v15, v15, s12, v154
	v_mov_b32_e32 v14, 0
	v_fma_f32 v30, v30, v36, v56
	v_cvt_pk_fp8_f32 v14, v37, v15
	v_mul_f32_e32 v29, v28, v29
	v_med3_f32 v30, v30, s12, v154
	v_med3_f32 v31, v31, s12, v154
	v_mov_b32_e32 v15, 0
	v_fma_f32 v29, v29, v46, v50
	v_mul_f32_e32 v36, v28, v65
	v_cvt_pk_fp8_f32 v15, v30, v31
	v_fma_f32 v36, v36, v38, v58
	v_med3_f32 v29, v29, s12, v154
	v_med3_f32 v38, v51, s12, v154
	v_cvt_pk_fp8_f32 v14, v29, v38 op_sel:[0,0,1]
	v_med3_f32 v29, v36, s12, v154
	ds_read_b128 v[36:39], v144 offset:20480
	ds_read_b128 v[44:47], v144 offset:36864
	v_med3_f32 v30, v59, s12, v154
	v_cvt_pk_fp8_f32 v15, v29, v30 op_sel:[0,0,1]
	v_lshlrev_b32_e32 v29, 16, v20
	v_and_b32_e32 v30, 0xffff0000, v20
	v_lshlrev_b32_e32 v31, 16, v21
	v_and_b32_e32 v56, 0xffff0000, v21
	v_lshlrev_b32_e32 v57, 16, v22
	v_and_b32_e32 v58, 0xffff0000, v22
	v_lshlrev_b32_e32 v59, 16, v23
	v_and_b32_e32 v64, 0xffff0000, v23
	ds_read_b128 v[20:23], v144 offset:20496
	ds_read_b128 v[48:51], v144 offset:36880
	v_mul_f32_e32 v29, v28, v29
	s_waitcnt lgkmcnt(2)
	v_fma_f32 v29, v29, v36, v44
	v_mul_f32_e32 v36, v28, v56
	v_fmac_f32_e32 v47, v36, v39
	v_mul_f32_e32 v36, v28, v57
	s_waitcnt lgkmcnt(0)
	v_fma_f32 v20, v36, v20, v48
	v_mul_f32_e32 v36, v28, v58
	v_mul_f32_e32 v30, v28, v30
	v_mul_f32_e32 v31, v28, v31
	v_fma_f32 v21, v36, v21, v49
	v_mul_f32_e32 v36, v28, v59
	v_fma_f32 v30, v30, v37, v45
	v_fma_f32 v31, v31, v38, v46
	v_fma_f32 v22, v36, v22, v50
	v_mul_f32_e32 v36, v28, v64
	v_fmac_f32_e32 v51, v36, v23
	v_med3_f32 v23, v29, s12, v154
	v_med3_f32 v29, v30, s12, v154
	v_med3_f32 v36, v31, s12, v154
	v_mov_b32_e32 v30, 0
	v_med3_f32 v20, v20, s12, v154
	v_med3_f32 v21, v21, s12, v154
	v_mov_b32_e32 v31, 0
	v_cvt_pk_fp8_f32 v30, v23, v29
	v_cvt_pk_fp8_f32 v31, v20, v21
	v_med3_f32 v37, v47, s12, v154
	v_med3_f32 v20, v22, s12, v154
	v_med3_f32 v21, v51, s12, v154
	v_cvt_pk_fp8_f32 v30, v36, v37 op_sel:[0,0,1]
	v_cvt_pk_fp8_f32 v31, v20, v21 op_sel:[0,0,1]
	ds_read_b128 v[20:23], v144 offset:22528
	ds_read_b128 v[36:39], v144 offset:38912
	v_lshlrev_b32_e32 v29, 16, v4
	v_and_b32_e32 v48, 0xffff0000, v4
	v_lshlrev_b32_e32 v49, 16, v5
	v_and_b32_e32 v50, 0xffff0000, v5
	v_lshlrev_b32_e32 v51, 16, v6
	v_and_b32_e32 v56, 0xffff0000, v6
	v_lshlrev_b32_e32 v57, 16, v7
	v_and_b32_e32 v58, 0xffff0000, v7
	v_mul_f32_e32 v29, v28, v29
	ds_read_b128 v[4:7], v144 offset:22544
	ds_read_b128 v[44:47], v144 offset:38928
	s_waitcnt lgkmcnt(2)
	v_fma_f32 v20, v29, v20, v36
	v_mul_f32_e32 v29, v28, v48
	v_fma_f32 v21, v29, v21, v37
	v_mul_f32_e32 v29, v28, v49
	v_fma_f32 v22, v29, v22, v38
	v_mul_f32_e32 v29, v28, v50
	v_fmac_f32_e32 v39, v29, v23
	v_mul_f32_e32 v23, v28, v51
	s_waitcnt lgkmcnt(0)
	v_fma_f32 v23, v23, v4, v44
	v_mul_f32_e32 v4, v28, v56
	v_fma_f32 v5, v4, v5, v45
	v_mul_f32_e32 v4, v28, v57
	v_fma_f32 v6, v4, v6, v46
	v_mul_f32_e32 v4, v28, v58
	v_fmac_f32_e32 v47, v4, v7
	v_med3_f32 v7, v20, s12, v154
	v_med3_f32 v20, v21, s12, v154
	v_mov_b32_e32 v4, 0
	v_cvt_pk_fp8_f32 v4, v7, v20
	v_med3_f32 v7, v23, s12, v154
	v_med3_f32 v20, v5, s12, v154
	v_mov_b32_e32 v5, 0
	s_waitcnt vmcnt(16)
	v_and_b32_e32 v37, 0xffff0000, v92
	v_cvt_pk_fp8_f32 v5, v7, v20
	v_lshlrev_b32_e32 v36, 16, v92
	v_mul_f32_e32 v20, v37, v37
	v_lshlrev_b32_e32 v51, 16, v93
	v_fmac_f32_e32 v20, v36, v36
	v_and_b32_e32 v72, 0xffff0000, v93
	v_fmac_f32_e32 v20, v51, v51
	v_lshlrev_b32_e32 v73, 16, v94
	v_fmac_f32_e32 v20, v72, v72
	v_and_b32_e32 v74, 0xffff0000, v94
	v_fmac_f32_e32 v20, v73, v73
	v_lshlrev_b32_e32 v75, 16, v95
	v_fmac_f32_e32 v20, v74, v74
	v_and_b32_e32 v80, 0xffff0000, v95
	v_fmac_f32_e32 v20, v75, v75
	v_fmac_f32_e32 v20, v80, v80
	s_waitcnt vmcnt(15)
	v_lshlrev_b32_e32 v81, 16, v84
	v_and_b32_e32 v82, 0xffff0000, v84
	v_fmac_f32_e32 v20, v81, v81
	v_lshlrev_b32_e32 v83, 16, v85
	v_fmac_f32_e32 v20, v82, v82
	v_and_b32_e32 v84, 0xffff0000, v85
	v_fmac_f32_e32 v20, v83, v83
	v_lshlrev_b32_e32 v85, 16, v86
	v_fmac_f32_e32 v20, v84, v84
	v_and_b32_e32 v86, 0xffff0000, v86
	v_fmac_f32_e32 v20, v85, v85
	v_lshlrev_b32_e32 v88, 16, v87
	v_fmac_f32_e32 v20, v86, v86
	v_and_b32_e32 v87, 0xffff0000, v87
	v_fmac_f32_e32 v20, v88, v88
	v_fmac_f32_e32 v20, v87, v87
	s_waitcnt vmcnt(14)
	v_lshlrev_b32_e32 v89, 16, v76
	v_and_b32_e32 v50, 0xffff0000, v76
	v_fmac_f32_e32 v20, v89, v89
	v_lshlrev_b32_e32 v49, 16, v77
	v_fmac_f32_e32 v20, v50, v50
	v_and_b32_e32 v48, 0xffff0000, v77
	v_fmac_f32_e32 v20, v49, v49
	v_med3_f32 v7, v47, s12, v154
	v_lshlrev_b32_e32 v47, 16, v78
	v_fmac_f32_e32 v20, v48, v48
	v_and_b32_e32 v46, 0xffff0000, v78
	v_fmac_f32_e32 v20, v47, v47
	v_lshlrev_b32_e32 v45, 16, v79
	v_fmac_f32_e32 v20, v46, v46
	v_and_b32_e32 v44, 0xffff0000, v79
	v_fmac_f32_e32 v20, v45, v45
	v_med3_f32 v21, v22, s12, v154
	v_med3_f32 v22, v39, s12, v154
	v_fmac_f32_e32 v20, v44, v44
	s_waitcnt vmcnt(13)
	v_lshlrev_b32_e32 v39, 16, v68
	v_cvt_pk_fp8_f32 v4, v21, v22 op_sel:[0,0,1]
	v_med3_f32 v6, v6, s12, v154
	v_and_b32_e32 v38, 0xffff0000, v68
	v_fmac_f32_e32 v20, v39, v39
	v_and_b32_e32 v22, 0xffff0000, v69
	v_lshlrev_b32_e32 v23, 16, v69
	v_cvt_pk_fp8_f32 v5, v6, v7 op_sel:[0,0,1]
	v_fmac_f32_e32 v20, v38, v38
	v_pk_mul_f32 v[6:7], v[22:23], v[22:23]
	v_and_b32_e32 v28, 0xffff0000, v70
	v_add_f32_e32 v7, v7, v20
	v_lshlrev_b32_e32 v29, 16, v70
	v_add_f32_e32 v20, v6, v7
	v_pk_mul_f32 v[6:7], v[28:29], v[28:29]
	v_lshlrev_b32_e32 v21, 16, v71
	v_add_f32_e32 v7, v7, v20
	v_and_b32_e32 v20, 0xffff0000, v71
	v_add_f32_e32 v56, v6, v7
	v_pk_mul_f32 v[6:7], v[20:21], v[20:21]
	global_store_dwordx2 v[12:13], v[14:15], off offset:512
	global_store_dwordx2 v[12:13], v[30:31], off offset:1024
	global_store_dwordx2 v[12:13], v[4:5], off offset:1536
	v_add_f32_e32 v7, v7, v56
	v_add_f32_e32 v6, v6, v7
	s_nop 1
	v_add_f32_dpp v6, v6, v6 quad_perm:[1,0,3,2] row_mask:0xf bank_mask:0xf bound_ctrl:1
	s_nop 1
	v_add_f32_dpp v6, v6, v6 quad_perm:[2,3,0,1] row_mask:0xf bank_mask:0xf bound_ctrl:1
	s_nop 1
	v_add_f32_dpp v6, v6, v6 row_ror:4 row_mask:0xf bank_mask:0xf bound_ctrl:1
	s_nop 1
	v_add_f32_dpp v6, v6, v6 row_ror:8 row_mask:0xf bank_mask:0xf bound_ctrl:1
	s_nop 0
	v_readlane_b32 s3, v6, 16
	v_readlane_b32 s20, v6, 48
	v_readlane_b32 s8, v6, 0
	v_readlane_b32 s9, v6, 32
	v_mov_b32_e32 v6, s3
	v_mov_b32_e32 v7, s20
	v_pk_add_f32 v[6:7], s[8:9], v[6:7]
	s_nop 0
	v_add_f32_e32 v6, v6, v7
	v_fmamk_f32 v6, v6, 0x3a000000, v151
	v_mul_f32_e32 v7, 0x4b800000, v6
	v_cmp_gt_f32_e32 vcc, s11, v6
	s_nop 1
	v_cndmask_b32_e32 v6, v6, v7, vcc
	v_rsq_f32_e32 v6, v6
	s_nop 0
	v_mul_f32_e32 v4, 0x45800000, v6
	v_cndmask_b32_e32 v30, v6, v4, vcc
	ds_read_b128 v[4:7], v144 offset:8192
	ds_read_b128 v[12:15], v144
	ds_read_b128 v[56:59], v144 offset:16
	v_mul_f32_e32 v31, v30, v36
	ds_read_b128 v[64:67], v144 offset:8208
	s_waitcnt lgkmcnt(3)
	v_mul_f32_e32 v4, v4, v31
	s_waitcnt vmcnt(14) lgkmcnt(2)
	v_fma_f32 v4, v12, v4, v60
	v_mul_f32_e32 v12, v30, v37
	v_mul_f32_e32 v5, v5, v12
	v_mul_f32_e32 v12, v30, v51
	v_fma_f32 v5, v13, v5, v61
	v_mul_f32_e32 v6, v6, v12
	v_mul_f32_e32 v12, v30, v72
	v_mul_f32_e32 v31, v5, v5
	v_mul_f32_e32 v7, v7, v12
	v_fmac_f32_e32 v31, v4, v4
	v_fma_f32 v6, v14, v6, v62
	v_fmac_f32_e32 v63, v15, v7
	v_mul_f32_e32 v7, v30, v73
	v_fmac_f32_e32 v31, v6, v6
	s_waitcnt lgkmcnt(0)
	v_mul_f32_e32 v7, v7, v64
	v_mul_f32_e32 v12, v30, v74
	v_fmac_f32_e32 v31, v63, v63
	v_fma_f32 v7, v56, v7, v52
	v_mul_f32_e32 v12, v12, v65
	v_mul_f32_e32 v13, v30, v75
	v_fmac_f32_e32 v31, v7, v7
	v_fma_f32 v12, v57, v12, v53
	v_mul_f32_e32 v13, v13, v66
	v_mul_f32_e32 v14, v30, v80
	v_fmac_f32_e32 v31, v12, v12
	v_fma_f32 v13, v58, v13, v54
	v_mul_f32_e32 v14, v14, v67
	v_lshl_add_u64 v[36:37], v[132:133], 0, s[22:23]
	v_fmac_f32_e32 v31, v13, v13
	v_fmac_f32_e32 v55, v59, v14
	v_cvt_pk_bf16_f32 v4, v4, v5
	v_cvt_pk_bf16_f32 v5, v6, v63
	v_cvt_pk_bf16_f32 v6, v7, v12
	v_cvt_pk_bf16_f32 v7, v13, v55
	global_store_dwordx4 v[36:37], v[4:7], off
	v_fmac_f32_e32 v31, v55, v55
	ds_read_b128 v[12:15], v144 offset:10240
	ds_read_b128 v[52:55], v144 offset:2048
	ds_read_b128 v[56:59], v144 offset:2064
	v_mul_f32_e32 v51, v30, v81
	ds_read_b128 v[60:63], v144 offset:10256
	s_waitcnt lgkmcnt(3)
	v_mul_f32_e32 v12, v51, v12
	s_waitcnt vmcnt(13) lgkmcnt(2)
	v_fma_f32 v12, v52, v12, v40
	v_mul_f32_e32 v40, v30, v82
	v_mul_f32_e32 v13, v40, v13
	v_mul_f32_e32 v40, v30, v83
	v_mul_f32_e32 v14, v40, v14
	v_mul_f32_e32 v40, v30, v84
	v_mul_f32_e32 v15, v40, v15
	v_fmac_f32_e32 v43, v55, v15
	v_mul_f32_e32 v15, v30, v85
	s_waitcnt lgkmcnt(0)
	v_mul_f32_e32 v15, v15, v60
	v_fmac_f32_e32 v31, v12, v12
	v_fma_f32 v13, v53, v13, v41
	v_fma_f32 v15, v56, v15, v32
	v_mul_f32_e32 v32, v30, v86
	v_fmac_f32_e32 v31, v13, v13
	v_fma_f32 v14, v54, v14, v42
	v_mul_f32_e32 v32, v32, v61
	v_fmac_f32_e32 v31, v14, v14
	v_fma_f32 v32, v57, v32, v33
	v_mul_f32_e32 v33, v30, v88
	v_fmac_f32_e32 v31, v43, v43
	v_mul_f32_e32 v33, v33, v62
	v_fmac_f32_e32 v31, v15, v15
	v_fma_f32 v33, v58, v33, v34
	v_mul_f32_e32 v34, v30, v87
	v_fmac_f32_e32 v31, v32, v32
	v_mul_f32_e32 v34, v34, v63
	v_fmac_f32_e32 v31, v33, v33
	v_fmac_f32_e32 v35, v59, v34
	v_cvt_pk_bf16_f32 v12, v12, v13
	v_cvt_pk_bf16_f32 v13, v14, v43
	v_cvt_pk_bf16_f32 v14, v15, v32
	v_cvt_pk_bf16_f32 v15, v33, v35
	global_store_dwordx4 v[36:37], v[12:15], off offset:1024
	v_fmac_f32_e32 v31, v35, v35
	ds_read_b128 v[32:35], v144 offset:12288
	ds_read_b128 v[40:43], v144 offset:4096
	ds_read_b128 v[52:55], v144 offset:4112
	v_mul_f32_e32 v51, v30, v89
	ds_read_b128 v[56:59], v144 offset:12304
	s_waitcnt lgkmcnt(3)
	v_mul_f32_e32 v32, v51, v32
	s_waitcnt vmcnt(12) lgkmcnt(2)
	v_fma_f32 v24, v40, v32, v24
	v_mul_f32_e32 v32, v30, v50
	v_mul_f32_e32 v32, v32, v33
	v_fma_f32 v25, v41, v32, v25
	v_mul_f32_e32 v32, v30, v49
	v_mul_f32_e32 v32, v32, v34
	v_fma_f32 v26, v42, v32, v26
	v_mul_f32_e32 v32, v30, v48
	v_mul_f32_e32 v32, v32, v35
	v_fmac_f32_e32 v27, v43, v32
	v_mul_f32_e32 v32, v30, v47
	s_waitcnt lgkmcnt(0)
	v_mul_f32_e32 v32, v32, v56
	v_fmac_f32_e32 v31, v24, v24
	v_fma_f32 v32, v52, v32, v16
	v_mul_f32_e32 v16, v30, v46
	v_fmac_f32_e32 v31, v25, v25
	v_mul_f32_e32 v16, v16, v57
	v_fmac_f32_e32 v31, v26, v26
	v_fma_f32 v33, v53, v16, v17
	v_mul_f32_e32 v16, v30, v45
	v_fmac_f32_e32 v31, v27, v27
	v_mul_f32_e32 v16, v16, v58
	v_fmac_f32_e32 v31, v32, v32
	v_fma_f32 v34, v54, v16, v18
	v_mul_f32_e32 v16, v30, v44
	v_fmac_f32_e32 v31, v33, v33
	v_mul_f32_e32 v16, v16, v59
	v_fmac_f32_e32 v31, v34, v34
	v_fmac_f32_e32 v19, v55, v16
	v_fmac_f32_e32 v31, v19, v19
	v_cvt_pk_bf16_f32 v16, v24, v25
	v_cvt_pk_bf16_f32 v17, v26, v27
	v_cvt_pk_bf16_f32 v18, v32, v33
	v_cvt_pk_bf16_f32 v19, v34, v19
	global_store_dwordx4 v[36:37], v[16:19], off offset:2048
	ds_read_b128 v[24:27], v144 offset:14336
	ds_read_b128 v[32:35], v144 offset:6144
	ds_read_b128 v[40:43], v144 offset:6160
	v_mul_f32_e32 v39, v30, v39
	ds_read_b128 v[44:47], v144 offset:14352
	s_waitcnt lgkmcnt(3)
	v_mul_f32_e32 v24, v39, v24
	s_waitcnt vmcnt(11) lgkmcnt(2)
	v_fma_f32 v24, v32, v24, v8
	v_mul_f32_e32 v8, v30, v38
	v_mul_f32_e32 v8, v8, v25
	v_fmac_f32_e32 v31, v24, v24
	v_fma_f32 v25, v33, v8, v9
	v_fmac_f32_e32 v31, v25, v25
	v_pk_mul_f32 v[8:9], v[30:31], v[22:23] op_sel_hi:[0,1]
	v_pk_mul_f32 v[8:9], v[8:9], v[26:27] op_sel:[1,0] op_sel_hi:[0,1]
	v_pk_fma_f32 v[8:9], v[34:35], v[8:9], v[10:11]
	s_nop 0
	v_pk_mul_f32 v[10:11], v[8:9], v[8:9]
	s_nop 0
	v_add_f32_e32 v10, v31, v10
	v_add_f32_e32 v22, v10, v11
	v_pk_mul_f32 v[10:11], v[30:31], v[28:29] op_sel_hi:[0,1]
	s_waitcnt lgkmcnt(0)
	v_pk_mul_f32 v[10:11], v[10:11], v[44:45] op_sel:[1,0] op_sel_hi:[0,1]
	v_pk_fma_f32 v[10:11], v[40:41], v[10:11], v[0:1]
	s_nop 0
	v_pk_mul_f32 v[0:1], v[10:11], v[10:11]
	s_nop 0
	v_add_f32_e32 v0, v22, v0
	v_add_f32_e32 v22, v0, v1
	v_pk_mul_f32 v[0:1], v[30:31], v[20:21] op_sel_hi:[0,1]
	v_pk_mul_f32 v[0:1], v[0:1], v[46:47] op_sel:[1,0] op_sel_hi:[0,1]
	v_pk_fma_f32 v[20:21], v[42:43], v[0:1], v[2:3]
	s_nop 0
	v_pk_mul_f32 v[0:1], v[20:21], v[20:21]
	s_nop 0
	v_add_f32_e32 v0, v22, v0
	v_add_f32_e32 v2, v0, v1
	v_cvt_pk_bf16_f32 v0, v24, v25
	v_cvt_pk_bf16_f32 v1, v8, v9
	s_nop 1
	v_add_f32_dpp v2, v2, v2 quad_perm:[1,0,3,2] row_mask:0xf bank_mask:0xf bound_ctrl:1
	s_nop 1
	v_add_f32_dpp v2, v2, v2 quad_perm:[2,3,0,1] row_mask:0xf bank_mask:0xf bound_ctrl:1
	s_nop 1
	v_add_f32_dpp v2, v2, v2 row_ror:4 row_mask:0xf bank_mask:0xf bound_ctrl:1
	s_nop 1
	v_add_f32_dpp v2, v2, v2 row_ror:8 row_mask:0xf bank_mask:0xf bound_ctrl:1
	s_nop 0
	v_readlane_b32 s3, v2, 16
	v_readlane_b32 s20, v2, 48
	v_readlane_b32 s8, v2, 0
	v_readlane_b32 s9, v2, 32
	v_mov_b32_e32 v2, s3
	v_mov_b32_e32 v3, s20
	v_pk_add_f32 v[2:3], s[8:9], v[2:3]
	s_nop 0
	v_add_f32_e32 v2, v2, v3
	v_fmamk_f32 v2, v2, 0x3a000000, v151
	v_mul_f32_e32 v3, 0x4b800000, v2
	v_cmp_gt_f32_e32 vcc, s11, v2
	s_nop 1
	v_cndmask_b32_e32 v2, v2, v3, vcc
	v_rsq_f32_e32 v8, v2
	v_cvt_pk_bf16_f32 v2, v10, v11
	v_cvt_pk_bf16_f32 v3, v20, v21
	global_store_dwordx4 v[36:37], v[0:3], off offset:3072
	v_mul_f32_e32 v9, 0x45800000, v8
	v_cndmask_b32_e32 v10, v8, v9, vcc
	s_and_saveexec_b64 s[8:9], s[6:7]
	v_mov_b32_e32 v8, s10
	ds_write_b32 v8, v10 offset:60700
	s_or_b64 exec, exec, s[8:9]
	ds_read_b128 v[20:23], v144 offset:16384
	ds_read_b128 v[24:27], v144 offset:32768
	v_lshlrev_b32_e32 v8, 16, v4
	v_and_b32_e32 v9, 0xffff0000, v4
	v_lshlrev_b32_e32 v11, 16, v5
	v_and_b32_e32 v32, 0xffff0000, v5
	v_lshlrev_b32_e32 v33, 16, v6
	v_and_b32_e32 v34, 0xffff0000, v6
	v_lshlrev_b32_e32 v35, 16, v7
	v_and_b32_e32 v36, 0xffff0000, v7
	ds_read_b128 v[4:7], v144 offset:16400
	ds_read_b128 v[28:31], v144 offset:32784
	v_mul_f32_e32 v8, v10, v8
	s_waitcnt lgkmcnt(2)
	v_fma_f32 v8, v8, v20, v24
	v_mul_f32_e32 v20, v10, v32
	v_fmac_f32_e32 v27, v20, v23
	v_mul_f32_e32 v20, v10, v33
	s_waitcnt lgkmcnt(0)
	v_fma_f32 v20, v20, v4, v28
	v_mul_f32_e32 v4, v10, v34
	v_mul_f32_e32 v9, v10, v9
	v_fma_f32 v5, v4, v5, v29
	v_mul_f32_e32 v4, v10, v35
	v_fma_f32 v9, v9, v21, v25
	v_fma_f32 v6, v4, v6, v30
	v_mul_f32_e32 v4, v10, v36
	v_fmac_f32_e32 v31, v4, v7
	v_med3_f32 v7, v8, s12, v154
	v_med3_f32 v8, v9, s12, v154
	v_mov_b32_e32 v4, 0
	v_mul_f32_e32 v11, v10, v11
	v_cvt_pk_fp8_f32 v4, v7, v8
	v_fma_f32 v11, v11, v22, v26
	v_med3_f32 v9, v11, s12, v154
	v_med3_f32 v11, v27, s12, v154
	v_med3_f32 v7, v20, s12, v154
	ds_read_b128 v[20:23], v144 offset:18432
	ds_read_b128 v[24:27], v144 offset:34816
	v_med3_f32 v8, v5, s12, v154
	v_mov_b32_e32 v5, 0
	v_cvt_pk_fp8_f32 v5, v7, v8
	v_cvt_pk_fp8_f32 v4, v9, v11 op_sel:[0,0,1]
	v_med3_f32 v7, v31, s12, v154
	v_lshlrev_b32_e32 v8, 16, v12
	v_and_b32_e32 v9, 0xffff0000, v12
	v_lshlrev_b32_e32 v11, 16, v13
	v_and_b32_e32 v32, 0xffff0000, v13
	v_lshlrev_b32_e32 v33, 16, v14
	v_and_b32_e32 v34, 0xffff0000, v14
	v_lshlrev_b32_e32 v35, 16, v15
	v_and_b32_e32 v36, 0xffff0000, v15
	ds_read_b128 v[12:15], v144 offset:18448
	ds_read_b128 v[28:31], v144 offset:34832
	v_mul_f32_e32 v8, v10, v8
	s_waitcnt lgkmcnt(2)
	v_fma_f32 v8, v8, v20, v24
	v_mul_f32_e32 v20, v10, v32
	v_fmac_f32_e32 v27, v20, v23
	v_mul_f32_e32 v20, v10, v33
	s_waitcnt lgkmcnt(0)
	v_fma_f32 v12, v20, v12, v28
	v_mul_f32_e32 v20, v10, v34
	v_mul_f32_e32 v9, v10, v9
	v_fma_f32 v13, v20, v13, v29
	v_mul_f32_e32 v20, v10, v35
	v_fma_f32 v9, v9, v21, v25
	v_fma_f32 v14, v20, v14, v30
	v_mul_f32_e32 v20, v10, v36
	v_fmac_f32_e32 v31, v20, v15
	v_med3_f32 v15, v8, s12, v154
	v_med3_f32 v9, v9, s12, v154
	v_mov_b32_e32 v8, 0
	v_cvt_pk_fp8_f32 v8, v15, v9
	v_med3_f32 v12, v12, s12, v154
	v_med3_f32 v13, v13, s12, v154
	v_mov_b32_e32 v9, 0
	v_mul_f32_e32 v11, v10, v11
	v_cvt_pk_fp8_f32 v9, v12, v13
	v_fma_f32 v11, v11, v22, v26
	v_med3_f32 v11, v11, s12, v154
	v_med3_f32 v20, v27, s12, v154
	v_cvt_pk_fp8_f32 v8, v11, v20 op_sel:[0,0,1]
	v_med3_f32 v11, v14, s12, v154
	v_med3_f32 v12, v31, s12, v154
	v_cvt_pk_fp8_f32 v9, v11, v12 op_sel:[0,0,1]
	ds_read_b128 v[12:15], v144 offset:20480
	ds_read_b128 v[20:23], v144 offset:36864
	v_lshlrev_b32_e32 v11, 16, v16
	v_and_b32_e32 v28, 0xffff0000, v16
	v_lshlrev_b32_e32 v29, 16, v17
	v_and_b32_e32 v30, 0xffff0000, v17
	v_lshlrev_b32_e32 v31, 16, v18
	v_and_b32_e32 v32, 0xffff0000, v18
	v_lshlrev_b32_e32 v33, 16, v19
	v_and_b32_e32 v34, 0xffff0000, v19
	v_mul_f32_e32 v11, v10, v11
	ds_read_b128 v[16:19], v144 offset:20496
	ds_read_b128 v[24:27], v144 offset:36880
	s_waitcnt lgkmcnt(2)
	v_fma_f32 v11, v11, v12, v20
	v_mul_f32_e32 v12, v10, v28
	v_fma_f32 v12, v12, v13, v21
	v_mul_f32_e32 v13, v10, v29
	v_fma_f32 v13, v13, v14, v22
	v_mul_f32_e32 v14, v10, v30
	v_fmac_f32_e32 v23, v14, v15
	v_mul_f32_e32 v14, v10, v31
	v_mul_f32_e32 v15, v10, v32
	s_waitcnt lgkmcnt(0)
	v_fma_f32 v14, v14, v16, v24
	v_fma_f32 v15, v15, v17, v25
	v_med3_f32 v11, v11, s12, v154
	v_med3_f32 v12, v12, s12, v154
	v_mov_b32_e32 v24, 0
	v_cvt_pk_fp8_f32 v24, v11, v12
	v_med3_f32 v11, v14, s12, v154
	v_med3_f32 v12, v15, s12, v154
	v_mov_b32_e32 v25, 0
	v_cvt_pk_fp8_f32 v25, v11, v12
	v_mul_f32_e32 v16, v10, v33
	v_mul_f32_e32 v17, v10, v34
	v_fma_f32 v16, v16, v18, v26
	v_fmac_f32_e32 v27, v17, v19
	v_med3_f32 v13, v13, s12, v154
	v_med3_f32 v17, v23, s12, v154
	v_med3_f32 v11, v16, s12, v154
	v_med3_f32 v12, v27, s12, v154
	v_cvt_pk_fp8_f32 v24, v13, v17 op_sel:[0,0,1]
	v_cvt_pk_fp8_f32 v25, v11, v12 op_sel:[0,0,1]
	ds_read_b128 v[12:15], v144 offset:22528
	ds_read_b128 v[16:19], v144 offset:38912
	v_lshlrev_b32_e32 v11, 16, v0
	v_and_b32_e32 v26, 0xffff0000, v0
	v_lshlrev_b32_e32 v27, 16, v1
	v_and_b32_e32 v28, 0xffff0000, v1
	v_lshlrev_b32_e32 v29, 16, v2
	v_and_b32_e32 v30, 0xffff0000, v2
	v_lshlrev_b32_e32 v31, 16, v3
	v_and_b32_e32 v32, 0xffff0000, v3
	v_mul_f32_e32 v11, v10, v11
	ds_read_b128 v[0:3], v144 offset:22544
	ds_read_b128 v[20:23], v144 offset:38928
	s_waitcnt lgkmcnt(2)
	v_fma_f32 v11, v11, v12, v16
	v_mul_f32_e32 v12, v10, v26
	v_fma_f32 v12, v12, v13, v17
	v_mul_f32_e32 v13, v10, v27
	v_fma_f32 v13, v13, v14, v18
	v_mul_f32_e32 v14, v10, v28
	v_fmac_f32_e32 v19, v14, v15
	v_mul_f32_e32 v14, v10, v29
	s_waitcnt lgkmcnt(0)
	v_fma_f32 v14, v14, v0, v20
	v_mul_f32_e32 v0, v10, v30
	v_fma_f32 v1, v0, v1, v21
	v_mul_f32_e32 v0, v10, v31
	v_fma_f32 v2, v0, v2, v22
	v_mul_f32_e32 v0, v10, v32
	v_fmac_f32_e32 v23, v0, v3
	v_med3_f32 v3, v11, s12, v154
	v_med3_f32 v10, v12, s12, v154
	v_mov_b32_e32 v0, 0
	v_cvt_pk_fp8_f32 v0, v3, v10
	v_med3_f32 v3, v14, s12, v154
	v_med3_f32 v10, v1, s12, v154
	v_mov_b32_e32 v1, 0
	v_med3_f32 v6, v6, s12, v154
	v_cvt_pk_fp8_f32 v1, v3, v10
	v_cvt_pk_fp8_f32 v5, v6, v7 op_sel:[0,0,1]
	s_lshl_b64 s[0:1], s[0:1], 11
	v_med3_f32 v11, v13, s12, v154
	v_med3_f32 v12, v19, s12, v154
	v_med3_f32 v2, v2, s12, v154
	v_med3_f32 v3, v23, s12, v154
	v_lshl_add_u64 v[6:7], v[134:135], 0, s[0:1]
	v_cvt_pk_fp8_f32 v0, v11, v12 op_sel:[0,0,1]
	v_cvt_pk_fp8_f32 v1, v2, v3 op_sel:[0,0,1]
	global_store_dwordx2 v[6:7], v[4:5], off
	global_store_dwordx2 v[6:7], v[8:9], off offset:512
	global_store_dwordx2 v[6:7], v[24:25], off offset:1024
	global_store_dwordx2 v[6:7], v[0:1], off offset:1536
	s_mov_b32 s0, s2
	s_waitcnt vmcnt(0)
	s_barrier
	v_mbcnt_lo_u32_b32 v36, -1, 0
	v_mbcnt_hi_u32_b32 v36, -1, v36
	v_and_b32_e32 v37, 15, v36
	v_lshrrev_b32_e32 v38, 4, v36
	v_lshlrev_b32_e32 v39, 12, v37
	v_lshl_or_b32 v39, v38, 4, v39
	s_lshl_b32 s8, s86, 9
	v_add_u32_e32 v40, s8, v39
	v_mov_b32_e32 v41, 0
	s_ashr_i32 s1, s0, 31
	s_lshl_b64 s[0:1], s[0:1], 18
	s_add_u32 s0, s0, 0xb661c00
	s_addc_u32 s1, s1, 0
	s_add_u32 s0, s0, s92
	s_addc_u32 s1, s1, s93
	v_lshl_add_u64 v[64:65], s[0:1], 0, v[40:41]
	s_mov_b64 s[8:9], 0x10000
	v_lshl_add_u64 v[66:67], v[64:65], 0, s[8:9]
	v_lshl_add_u64 v[68:69], v[66:67], 0, s[8:9]
	v_lshl_add_u64 v[70:71], v[68:69], 0, s[8:9]
	s_add_u32 s0, s92, 0x3a0400
	s_addc_u32 s1, s93, 0
	v_lshl_add_u64 v[72:73], s[0:1], 0, v[40:41]
	v_lshl_add_u64 v[74:75], v[72:73], 0, s[8:9]
	v_lshl_add_u64 v[76:77], v[74:75], 0, s[8:9]
	v_lshl_add_u64 v[78:79], v[76:77], 0, s[8:9]
	s_lshl_b32 s8, s86, 10
	v_lshlrev_b32_e32 v32, 5, v38
	v_add_u32_e32 v32, s8, v32
	v_add_u32_e32 v32, 0x4000, v32
	v_lshlrev_b32_e32 v33, 2, v37
	s_lshl_b32 s8, s86, 13
	v_lshlrev_b32_e32 v34, 9, v38
	v_add_u32_e32 v34, s8, v34
	v_add_u32_e32 v34, v34, v33
	v_add_u32_e32 v34, 0x10000, v34
	ds_read_b32 v60, v33 offset:60672
	ds_read_b32 v61, v33 offset:60736
	ds_read_b32 v62, v33 offset:60800
	ds_read_b32 v63, v33 offset:60864
	v_mov_b32_e32 v0, 0
	v_mov_b32_e32 v1, 0
	v_mov_b32_e32 v2, 0
	v_mov_b32_e32 v3, 0
	v_mov_b32_e32 v4, 0
	v_mov_b32_e32 v5, 0
	v_mov_b32_e32 v6, 0
	v_mov_b32_e32 v7, 0
	v_mov_b32_e32 v8, 0
	v_mov_b32_e32 v9, 0
	v_mov_b32_e32 v10, 0
	v_mov_b32_e32 v11, 0
	v_mov_b32_e32 v12, 0
	v_mov_b32_e32 v13, 0
	v_mov_b32_e32 v14, 0
	v_mov_b32_e32 v15, 0
	v_mov_b32_e32 v16, 0
	v_mov_b32_e32 v17, 0
	v_mov_b32_e32 v18, 0
	v_mov_b32_e32 v19, 0
	v_mov_b32_e32 v20, 0
	v_mov_b32_e32 v21, 0
	v_mov_b32_e32 v22, 0
	v_mov_b32_e32 v23, 0
	v_mov_b32_e32 v24, 0
	v_mov_b32_e32 v25, 0
	v_mov_b32_e32 v26, 0
	v_mov_b32_e32 v27, 0
	v_mov_b32_e32 v28, 0
	v_mov_b32_e32 v29, 0
	v_mov_b32_e32 v30, 0
	v_mov_b32_e32 v31, 0
	global_load_dwordx4 v[80:83], v[64:65], off offset:0
	global_load_dwordx4 v[84:87], v[66:67], off offset:0
	global_load_dwordx4 v[88:91], v[68:69], off offset:0
	global_load_dwordx4 v[92:95], v[70:71], off offset:0
	global_load_dwordx4 v[96:99], v[72:73], off offset:0
	global_load_dwordx4 v[100:103], v[74:75], off offset:0
	global_load_dwordx4 v[104:107], v[76:77], off offset:0
	global_load_dwordx4 v[108:111], v[78:79], off offset:0
	global_load_dwordx4 v[112:115], v[64:65], off offset:64
	global_load_dwordx4 v[116:119], v[66:67], off offset:64
	global_load_dwordx4 v[164:167], v[68:69], off offset:64
	global_load_dwordx4 v[168:171], v[70:71], off offset:64
	global_load_dwordx4 v[172:175], v[72:73], off offset:64
	global_load_dwordx4 v[176:179], v[74:75], off offset:64
	global_load_dwordx4 v[180:183], v[76:77], off offset:64
	global_load_dwordx4 v[184:187], v[78:79], off offset:64
	global_load_dwordx4 v[188:191], v[64:65], off offset:128
	global_load_dwordx4 v[192:195], v[66:67], off offset:128
	global_load_dwordx4 v[196:199], v[68:69], off offset:128
	global_load_dwordx4 v[200:203], v[70:71], off offset:128
	global_load_dwordx4 v[204:207], v[72:73], off offset:128
	global_load_dwordx4 v[208:211], v[74:75], off offset:128
	global_load_dwordx4 v[212:215], v[76:77], off offset:128
	global_load_dwordx4 v[216:219], v[78:79], off offset:128
	global_load_dwordx4 v[220:223], v[64:65], off offset:192
	global_load_dwordx4 v[224:227], v[66:67], off offset:192
	global_load_dwordx4 v[228:231], v[68:69], off offset:192
	global_load_dwordx4 v[232:235], v[70:71], off offset:192
	global_load_dwordx4 v[236:239], v[72:73], off offset:192
	global_load_dwordx4 v[240:243], v[74:75], off offset:192
	global_load_dwordx4 v[244:247], v[76:77], off offset:192
	global_load_dwordx4 v[248:251], v[78:79], off offset:192
	ds_read_b128 v[44:47], v32 offset:0
	ds_read_b128 v[48:51], v32 offset:16
	ds_read_b128 v[52:55], v32 offset:16384
	ds_read_b128 v[56:59], v32 offset:16400
	s_waitcnt vmcnt(16)
	s_waitcnt lgkmcnt(0)
	v_lshlrev_b32_e32 v36, 16, v80
	v_and_b32_e32 v37, 0xffff0000, v80
	v_lshlrev_b32_e32 v38, 16, v81
	v_and_b32_e32 v39, 0xffff0000, v81
	v_lshlrev_b32_e32 v40, 16, v82
	v_and_b32_e32 v41, 0xffff0000, v82
	v_lshlrev_b32_e32 v42, 16, v83
	v_and_b32_e32 v43, 0xffff0000, v83
	v_mul_f32_e32 v36, v60, v36
	v_mul_f32_e32 v37, v60, v37
	v_mul_f32_e32 v38, v60, v38
	v_mul_f32_e32 v39, v60, v39
	v_mul_f32_e32 v40, v60, v40
	v_mul_f32_e32 v41, v60, v41
	v_mul_f32_e32 v42, v60, v42
	v_mul_f32_e32 v43, v60, v43
	v_fma_f32 v36, v44, v36, v52
	v_fma_f32 v37, v45, v37, v53
	v_fma_f32 v38, v46, v38, v54
	v_fma_f32 v39, v47, v39, v55
	v_fma_f32 v40, v48, v40, v56
	v_fma_f32 v41, v49, v41, v57
	v_fma_f32 v42, v50, v42, v58
	v_fma_f32 v43, v51, v43, v59
	v_cvt_pk_bf16_f32 v36, v36, v37
	v_cvt_pk_bf16_f32 v37, v38, v39
	v_cvt_pk_bf16_f32 v38, v40, v41
	v_cvt_pk_bf16_f32 v39, v42, v43
	s_nop 1
	v_mfma_f32_16x16x32_bf16 v[0:3], v[36:39], v[96:99], v[0:3]
	v_mfma_f32_16x16x32_bf16 v[4:7], v[36:39], v[100:103], v[4:7]
	v_mfma_f32_16x16x32_bf16 v[0:3], v[36:39], v[104:107], v[0:3]
	v_mfma_f32_16x16x32_bf16 v[4:7], v[36:39], v[108:111], v[4:7]
	s_nop 3
	v_lshlrev_b32_e32 v36, 16, v84
	v_and_b32_e32 v37, 0xffff0000, v84
	v_lshlrev_b32_e32 v38, 16, v85
	v_and_b32_e32 v39, 0xffff0000, v85
	v_lshlrev_b32_e32 v40, 16, v86
	v_and_b32_e32 v41, 0xffff0000, v86
	v_lshlrev_b32_e32 v42, 16, v87
	v_and_b32_e32 v43, 0xffff0000, v87
	v_mul_f32_e32 v36, v61, v36
	v_mul_f32_e32 v37, v61, v37
	v_mul_f32_e32 v38, v61, v38
	v_mul_f32_e32 v39, v61, v39
	v_mul_f32_e32 v40, v61, v40
	v_mul_f32_e32 v41, v61, v41
	v_mul_f32_e32 v42, v61, v42
	v_mul_f32_e32 v43, v61, v43
	v_fma_f32 v36, v44, v36, v52
	v_fma_f32 v37, v45, v37, v53
	v_fma_f32 v38, v46, v38, v54
	v_fma_f32 v39, v47, v39, v55
	v_fma_f32 v40, v48, v40, v56
	v_fma_f32 v41, v49, v41, v57
	v_fma_f32 v42, v50, v42, v58
	v_fma_f32 v43, v51, v43, v59
	v_cvt_pk_bf16_f32 v36, v36, v37
	v_cvt_pk_bf16_f32 v37, v38, v39
	v_cvt_pk_bf16_f32 v38, v40, v41
	v_cvt_pk_bf16_f32 v39, v42, v43
	s_nop 1
	v_mfma_f32_16x16x32_bf16 v[8:11], v[36:39], v[96:99], v[8:11]
	v_mfma_f32_16x16x32_bf16 v[12:15], v[36:39], v[100:103], v[12:15]
	v_mfma_f32_16x16x32_bf16 v[8:11], v[36:39], v[104:107], v[8:11]
	v_mfma_f32_16x16x32_bf16 v[12:15], v[36:39], v[108:111], v[12:15]
	s_nop 3
	v_lshlrev_b32_e32 v36, 16, v88
	v_and_b32_e32 v37, 0xffff0000, v88
	v_lshlrev_b32_e32 v38, 16, v89
	v_and_b32_e32 v39, 0xffff0000, v89
	v_lshlrev_b32_e32 v40, 16, v90
	v_and_b32_e32 v41, 0xffff0000, v90
	v_lshlrev_b32_e32 v42, 16, v91
	v_and_b32_e32 v43, 0xffff0000, v91
	v_mul_f32_e32 v36, v62, v36
	v_mul_f32_e32 v37, v62, v37
	v_mul_f32_e32 v38, v62, v38
	v_mul_f32_e32 v39, v62, v39
	v_mul_f32_e32 v40, v62, v40
	v_mul_f32_e32 v41, v62, v41
	v_mul_f32_e32 v42, v62, v42
	v_mul_f32_e32 v43, v62, v43
	v_fma_f32 v36, v44, v36, v52
	v_fma_f32 v37, v45, v37, v53
	v_fma_f32 v38, v46, v38, v54
	v_fma_f32 v39, v47, v39, v55
	v_fma_f32 v40, v48, v40, v56
	v_fma_f32 v41, v49, v41, v57
	v_fma_f32 v42, v50, v42, v58
	v_fma_f32 v43, v51, v43, v59
	v_cvt_pk_bf16_f32 v36, v36, v37
	v_cvt_pk_bf16_f32 v37, v38, v39
	v_cvt_pk_bf16_f32 v38, v40, v41
	v_cvt_pk_bf16_f32 v39, v42, v43
	s_nop 1
	v_mfma_f32_16x16x32_bf16 v[16:19], v[36:39], v[96:99], v[16:19]
	v_mfma_f32_16x16x32_bf16 v[20:23], v[36:39], v[100:103], v[20:23]
	v_mfma_f32_16x16x32_bf16 v[16:19], v[36:39], v[104:107], v[16:19]
	v_mfma_f32_16x16x32_bf16 v[20:23], v[36:39], v[108:111], v[20:23]
	s_nop 3
	v_lshlrev_b32_e32 v36, 16, v92
	v_and_b32_e32 v37, 0xffff0000, v92
	v_lshlrev_b32_e32 v38, 16, v93
	v_and_b32_e32 v39, 0xffff0000, v93
	v_lshlrev_b32_e32 v40, 16, v94
	v_and_b32_e32 v41, 0xffff0000, v94
	v_lshlrev_b32_e32 v42, 16, v95
	v_and_b32_e32 v43, 0xffff0000, v95
	v_mul_f32_e32 v36, v63, v36
	v_mul_f32_e32 v37, v63, v37
	v_mul_f32_e32 v38, v63, v38
	v_mul_f32_e32 v39, v63, v39
	v_mul_f32_e32 v40, v63, v40
	v_mul_f32_e32 v41, v63, v41
	v_mul_f32_e32 v42, v63, v42
	v_mul_f32_e32 v43, v63, v43
	v_fma_f32 v36, v44, v36, v52
	v_fma_f32 v37, v45, v37, v53
	v_fma_f32 v38, v46, v38, v54
	v_fma_f32 v39, v47, v39, v55
	v_fma_f32 v40, v48, v40, v56
	v_fma_f32 v41, v49, v41, v57
	v_fma_f32 v42, v50, v42, v58
	v_fma_f32 v43, v51, v43, v59
	ds_read_b128 v[44:47], v32 offset:128
	ds_read_b128 v[48:51], v32 offset:144
	ds_read_b128 v[52:55], v32 offset:16512
	ds_read_b128 v[56:59], v32 offset:16528
	v_cvt_pk_bf16_f32 v36, v36, v37
	v_cvt_pk_bf16_f32 v37, v38, v39
	v_cvt_pk_bf16_f32 v38, v40, v41
	v_cvt_pk_bf16_f32 v39, v42, v43
	s_nop 1
	v_mfma_f32_16x16x32_bf16 v[24:27], v[36:39], v[96:99], v[24:27]
	v_mfma_f32_16x16x32_bf16 v[28:31], v[36:39], v[100:103], v[28:31]
	v_mfma_f32_16x16x32_bf16 v[24:27], v[36:39], v[104:107], v[24:27]
	v_mfma_f32_16x16x32_bf16 v[28:31], v[36:39], v[108:111], v[28:31]
	s_nop 3
	s_waitcnt lgkmcnt(0)
	v_lshlrev_b32_e32 v36, 16, v112
	v_and_b32_e32 v37, 0xffff0000, v112
	v_lshlrev_b32_e32 v38, 16, v113
	v_and_b32_e32 v39, 0xffff0000, v113
	v_lshlrev_b32_e32 v40, 16, v114
	v_and_b32_e32 v41, 0xffff0000, v114
	v_lshlrev_b32_e32 v42, 16, v115
	v_and_b32_e32 v43, 0xffff0000, v115
	v_mul_f32_e32 v36, v60, v36
	v_mul_f32_e32 v37, v60, v37
	v_mul_f32_e32 v38, v60, v38
	v_mul_f32_e32 v39, v60, v39
	v_mul_f32_e32 v40, v60, v40
	v_mul_f32_e32 v41, v60, v41
	v_mul_f32_e32 v42, v60, v42
	v_mul_f32_e32 v43, v60, v43
	v_fma_f32 v36, v44, v36, v52
	v_fma_f32 v37, v45, v37, v53
	v_fma_f32 v38, v46, v38, v54
	v_fma_f32 v39, v47, v39, v55
	v_fma_f32 v40, v48, v40, v56
	v_fma_f32 v41, v49, v41, v57
	v_fma_f32 v42, v50, v42, v58
	v_fma_f32 v43, v51, v43, v59
	v_cvt_pk_bf16_f32 v36, v36, v37
	v_cvt_pk_bf16_f32 v37, v38, v39
	v_cvt_pk_bf16_f32 v38, v40, v41
	v_cvt_pk_bf16_f32 v39, v42, v43
	s_nop 1
	v_mfma_f32_16x16x32_bf16 v[0:3], v[36:39], v[172:175], v[0:3]
	v_mfma_f32_16x16x32_bf16 v[4:7], v[36:39], v[176:179], v[4:7]
	v_mfma_f32_16x16x32_bf16 v[0:3], v[36:39], v[180:183], v[0:3]
	v_mfma_f32_16x16x32_bf16 v[4:7], v[36:39], v[184:187], v[4:7]
	s_nop 3
	v_lshlrev_b32_e32 v36, 16, v116
	v_and_b32_e32 v37, 0xffff0000, v116
	v_lshlrev_b32_e32 v38, 16, v117
	v_and_b32_e32 v39, 0xffff0000, v117
	v_lshlrev_b32_e32 v40, 16, v118
	v_and_b32_e32 v41, 0xffff0000, v118
	v_lshlrev_b32_e32 v42, 16, v119
	v_and_b32_e32 v43, 0xffff0000, v119
	v_mul_f32_e32 v36, v61, v36
	v_mul_f32_e32 v37, v61, v37
	v_mul_f32_e32 v38, v61, v38
	v_mul_f32_e32 v39, v61, v39
	v_mul_f32_e32 v40, v61, v40
	v_mul_f32_e32 v41, v61, v41
	v_mul_f32_e32 v42, v61, v42
	v_mul_f32_e32 v43, v61, v43
	v_fma_f32 v36, v44, v36, v52
	v_fma_f32 v37, v45, v37, v53
	v_fma_f32 v38, v46, v38, v54
	v_fma_f32 v39, v47, v39, v55
	v_fma_f32 v40, v48, v40, v56
	v_fma_f32 v41, v49, v41, v57
	v_fma_f32 v42, v50, v42, v58
	v_fma_f32 v43, v51, v43, v59
	v_cvt_pk_bf16_f32 v36, v36, v37
	v_cvt_pk_bf16_f32 v37, v38, v39
	v_cvt_pk_bf16_f32 v38, v40, v41
	v_cvt_pk_bf16_f32 v39, v42, v43
	s_nop 1
	v_mfma_f32_16x16x32_bf16 v[8:11], v[36:39], v[172:175], v[8:11]
	v_mfma_f32_16x16x32_bf16 v[12:15], v[36:39], v[176:179], v[12:15]
	v_mfma_f32_16x16x32_bf16 v[8:11], v[36:39], v[180:183], v[8:11]
	v_mfma_f32_16x16x32_bf16 v[12:15], v[36:39], v[184:187], v[12:15]
	s_nop 3
	v_lshlrev_b32_e32 v36, 16, v164
	v_and_b32_e32 v37, 0xffff0000, v164
	v_lshlrev_b32_e32 v38, 16, v165
	v_and_b32_e32 v39, 0xffff0000, v165
	v_lshlrev_b32_e32 v40, 16, v166
	v_and_b32_e32 v41, 0xffff0000, v166
	v_lshlrev_b32_e32 v42, 16, v167
	v_and_b32_e32 v43, 0xffff0000, v167
	v_mul_f32_e32 v36, v62, v36
	v_mul_f32_e32 v37, v62, v37
	v_mul_f32_e32 v38, v62, v38
	v_mul_f32_e32 v39, v62, v39
	v_mul_f32_e32 v40, v62, v40
	v_mul_f32_e32 v41, v62, v41
	v_mul_f32_e32 v42, v62, v42
	v_mul_f32_e32 v43, v62, v43
	v_fma_f32 v36, v44, v36, v52
	v_fma_f32 v37, v45, v37, v53
	v_fma_f32 v38, v46, v38, v54
	v_fma_f32 v39, v47, v39, v55
	v_fma_f32 v40, v48, v40, v56
	v_fma_f32 v41, v49, v41, v57
	v_fma_f32 v42, v50, v42, v58
	v_fma_f32 v43, v51, v43, v59
	v_cvt_pk_bf16_f32 v36, v36, v37
	v_cvt_pk_bf16_f32 v37, v38, v39
	v_cvt_pk_bf16_f32 v38, v40, v41
	v_cvt_pk_bf16_f32 v39, v42, v43
	s_nop 1
	v_mfma_f32_16x16x32_bf16 v[16:19], v[36:39], v[172:175], v[16:19]
	v_mfma_f32_16x16x32_bf16 v[20:23], v[36:39], v[176:179], v[20:23]
	v_mfma_f32_16x16x32_bf16 v[16:19], v[36:39], v[180:183], v[16:19]
	v_mfma_f32_16x16x32_bf16 v[20:23], v[36:39], v[184:187], v[20:23]
	s_nop 3
	v_lshlrev_b32_e32 v36, 16, v168
	v_and_b32_e32 v37, 0xffff0000, v168
	v_lshlrev_b32_e32 v38, 16, v169
	v_and_b32_e32 v39, 0xffff0000, v169
	v_lshlrev_b32_e32 v40, 16, v170
	v_and_b32_e32 v41, 0xffff0000, v170
	v_lshlrev_b32_e32 v42, 16, v171
	v_and_b32_e32 v43, 0xffff0000, v171
	v_mul_f32_e32 v36, v63, v36
	v_mul_f32_e32 v37, v63, v37
	v_mul_f32_e32 v38, v63, v38
	v_mul_f32_e32 v39, v63, v39
	v_mul_f32_e32 v40, v63, v40
	v_mul_f32_e32 v41, v63, v41
	v_mul_f32_e32 v42, v63, v42
	v_mul_f32_e32 v43, v63, v43
	v_fma_f32 v36, v44, v36, v52
	v_fma_f32 v37, v45, v37, v53
	v_fma_f32 v38, v46, v38, v54
	v_fma_f32 v39, v47, v39, v55
	v_fma_f32 v40, v48, v40, v56
	v_fma_f32 v41, v49, v41, v57
	v_fma_f32 v42, v50, v42, v58
	v_fma_f32 v43, v51, v43, v59
	ds_read_b128 v[44:47], v32 offset:256
	ds_read_b128 v[48:51], v32 offset:272
	ds_read_b128 v[52:55], v32 offset:16640
	ds_read_b128 v[56:59], v32 offset:16656
	v_cvt_pk_bf16_f32 v36, v36, v37
	v_cvt_pk_bf16_f32 v37, v38, v39
	v_cvt_pk_bf16_f32 v38, v40, v41
	v_cvt_pk_bf16_f32 v39, v42, v43
	s_nop 1
	v_mfma_f32_16x16x32_bf16 v[24:27], v[36:39], v[172:175], v[24:27]
	v_mfma_f32_16x16x32_bf16 v[28:31], v[36:39], v[176:179], v[28:31]
	v_mfma_f32_16x16x32_bf16 v[24:27], v[36:39], v[180:183], v[24:27]
	v_mfma_f32_16x16x32_bf16 v[28:31], v[36:39], v[184:187], v[28:31]
	s_nop 3
	global_load_dwordx4 v[80:83], v[64:65], off offset:256
	global_load_dwordx4 v[84:87], v[66:67], off offset:256
	global_load_dwordx4 v[88:91], v[68:69], off offset:256
	global_load_dwordx4 v[92:95], v[70:71], off offset:256
	global_load_dwordx4 v[96:99], v[72:73], off offset:256
	global_load_dwordx4 v[100:103], v[74:75], off offset:256
	global_load_dwordx4 v[104:107], v[76:77], off offset:256
	global_load_dwordx4 v[108:111], v[78:79], off offset:256
	global_load_dwordx4 v[112:115], v[64:65], off offset:320
	global_load_dwordx4 v[116:119], v[66:67], off offset:320
	global_load_dwordx4 v[164:167], v[68:69], off offset:320
	global_load_dwordx4 v[168:171], v[70:71], off offset:320
	global_load_dwordx4 v[172:175], v[72:73], off offset:320
	global_load_dwordx4 v[176:179], v[74:75], off offset:320
	global_load_dwordx4 v[180:183], v[76:77], off offset:320
	global_load_dwordx4 v[184:187], v[78:79], off offset:320
	s_waitcnt vmcnt(16)
	s_waitcnt lgkmcnt(0)
	v_lshlrev_b32_e32 v36, 16, v188
	v_and_b32_e32 v37, 0xffff0000, v188
	v_lshlrev_b32_e32 v38, 16, v189
	v_and_b32_e32 v39, 0xffff0000, v189
	v_lshlrev_b32_e32 v40, 16, v190
	v_and_b32_e32 v41, 0xffff0000, v190
	v_lshlrev_b32_e32 v42, 16, v191
	v_and_b32_e32 v43, 0xffff0000, v191
	v_mul_f32_e32 v36, v60, v36
	v_mul_f32_e32 v37, v60, v37
	v_mul_f32_e32 v38, v60, v38
	v_mul_f32_e32 v39, v60, v39
	v_mul_f32_e32 v40, v60, v40
	v_mul_f32_e32 v41, v60, v41
	v_mul_f32_e32 v42, v60, v42
	v_mul_f32_e32 v43, v60, v43
	v_fma_f32 v36, v44, v36, v52
	v_fma_f32 v37, v45, v37, v53
	v_fma_f32 v38, v46, v38, v54
	v_fma_f32 v39, v47, v39, v55
	v_fma_f32 v40, v48, v40, v56
	v_fma_f32 v41, v49, v41, v57
	v_fma_f32 v42, v50, v42, v58
	v_fma_f32 v43, v51, v43, v59
	v_cvt_pk_bf16_f32 v36, v36, v37
	v_cvt_pk_bf16_f32 v37, v38, v39
	v_cvt_pk_bf16_f32 v38, v40, v41
	v_cvt_pk_bf16_f32 v39, v42, v43
	s_nop 1
	v_mfma_f32_16x16x32_bf16 v[0:3], v[36:39], v[204:207], v[0:3]
	v_mfma_f32_16x16x32_bf16 v[4:7], v[36:39], v[208:211], v[4:7]
	v_mfma_f32_16x16x32_bf16 v[0:3], v[36:39], v[212:215], v[0:3]
	v_mfma_f32_16x16x32_bf16 v[4:7], v[36:39], v[216:219], v[4:7]
	s_nop 3
	v_lshlrev_b32_e32 v36, 16, v192
	v_and_b32_e32 v37, 0xffff0000, v192
	v_lshlrev_b32_e32 v38, 16, v193
	v_and_b32_e32 v39, 0xffff0000, v193
	v_lshlrev_b32_e32 v40, 16, v194
	v_and_b32_e32 v41, 0xffff0000, v194
	v_lshlrev_b32_e32 v42, 16, v195
	v_and_b32_e32 v43, 0xffff0000, v195
	v_mul_f32_e32 v36, v61, v36
	v_mul_f32_e32 v37, v61, v37
	v_mul_f32_e32 v38, v61, v38
	v_mul_f32_e32 v39, v61, v39
	v_mul_f32_e32 v40, v61, v40
	v_mul_f32_e32 v41, v61, v41
	v_mul_f32_e32 v42, v61, v42
	v_mul_f32_e32 v43, v61, v43
	v_fma_f32 v36, v44, v36, v52
	v_fma_f32 v37, v45, v37, v53
	v_fma_f32 v38, v46, v38, v54
	v_fma_f32 v39, v47, v39, v55
	v_fma_f32 v40, v48, v40, v56
	v_fma_f32 v41, v49, v41, v57
	v_fma_f32 v42, v50, v42, v58
	v_fma_f32 v43, v51, v43, v59
	v_cvt_pk_bf16_f32 v36, v36, v37
	v_cvt_pk_bf16_f32 v37, v38, v39
	v_cvt_pk_bf16_f32 v38, v40, v41
	v_cvt_pk_bf16_f32 v39, v42, v43
	s_nop 1
	v_mfma_f32_16x16x32_bf16 v[8:11], v[36:39], v[204:207], v[8:11]
	v_mfma_f32_16x16x32_bf16 v[12:15], v[36:39], v[208:211], v[12:15]
	v_mfma_f32_16x16x32_bf16 v[8:11], v[36:39], v[212:215], v[8:11]
	v_mfma_f32_16x16x32_bf16 v[12:15], v[36:39], v[216:219], v[12:15]
	s_nop 3
	v_lshlrev_b32_e32 v36, 16, v196
	v_and_b32_e32 v37, 0xffff0000, v196
	v_lshlrev_b32_e32 v38, 16, v197
	v_and_b32_e32 v39, 0xffff0000, v197
	v_lshlrev_b32_e32 v40, 16, v198
	v_and_b32_e32 v41, 0xffff0000, v198
	v_lshlrev_b32_e32 v42, 16, v199
	v_and_b32_e32 v43, 0xffff0000, v199
	v_mul_f32_e32 v36, v62, v36
	v_mul_f32_e32 v37, v62, v37
	v_mul_f32_e32 v38, v62, v38
	v_mul_f32_e32 v39, v62, v39
	v_mul_f32_e32 v40, v62, v40
	v_mul_f32_e32 v41, v62, v41
	v_mul_f32_e32 v42, v62, v42
	v_mul_f32_e32 v43, v62, v43
	v_fma_f32 v36, v44, v36, v52
	v_fma_f32 v37, v45, v37, v53
	v_fma_f32 v38, v46, v38, v54
	v_fma_f32 v39, v47, v39, v55
	v_fma_f32 v40, v48, v40, v56
	v_fma_f32 v41, v49, v41, v57
	v_fma_f32 v42, v50, v42, v58
	v_fma_f32 v43, v51, v43, v59
	v_cvt_pk_bf16_f32 v36, v36, v37
	v_cvt_pk_bf16_f32 v37, v38, v39
	v_cvt_pk_bf16_f32 v38, v40, v41
	v_cvt_pk_bf16_f32 v39, v42, v43
	s_nop 1
	v_mfma_f32_16x16x32_bf16 v[16:19], v[36:39], v[204:207], v[16:19]
	v_mfma_f32_16x16x32_bf16 v[20:23], v[36:39], v[208:211], v[20:23]
	v_mfma_f32_16x16x32_bf16 v[16:19], v[36:39], v[212:215], v[16:19]
	v_mfma_f32_16x16x32_bf16 v[20:23], v[36:39], v[216:219], v[20:23]
	s_nop 3
	v_lshlrev_b32_e32 v36, 16, v200
	v_and_b32_e32 v37, 0xffff0000, v200
	v_lshlrev_b32_e32 v38, 16, v201
	v_and_b32_e32 v39, 0xffff0000, v201
	v_lshlrev_b32_e32 v40, 16, v202
	v_and_b32_e32 v41, 0xffff0000, v202
	v_lshlrev_b32_e32 v42, 16, v203
	v_and_b32_e32 v43, 0xffff0000, v203
	v_mul_f32_e32 v36, v63, v36
	v_mul_f32_e32 v37, v63, v37
	v_mul_f32_e32 v38, v63, v38
	v_mul_f32_e32 v39, v63, v39
	v_mul_f32_e32 v40, v63, v40
	v_mul_f32_e32 v41, v63, v41
	v_mul_f32_e32 v42, v63, v42
	v_mul_f32_e32 v43, v63, v43
	v_fma_f32 v36, v44, v36, v52
	v_fma_f32 v37, v45, v37, v53
	v_fma_f32 v38, v46, v38, v54
	v_fma_f32 v39, v47, v39, v55
	v_fma_f32 v40, v48, v40, v56
	v_fma_f32 v41, v49, v41, v57
	v_fma_f32 v42, v50, v42, v58
	v_fma_f32 v43, v51, v43, v59
	ds_read_b128 v[44:47], v32 offset:384
	ds_read_b128 v[48:51], v32 offset:400
	ds_read_b128 v[52:55], v32 offset:16768
	ds_read_b128 v[56:59], v32 offset:16784
	v_cvt_pk_bf16_f32 v36, v36, v37
	v_cvt_pk_bf16_f32 v37, v38, v39
	v_cvt_pk_bf16_f32 v38, v40, v41
	v_cvt_pk_bf16_f32 v39, v42, v43
	s_nop 1
	v_mfma_f32_16x16x32_bf16 v[24:27], v[36:39], v[204:207], v[24:27]
	v_mfma_f32_16x16x32_bf16 v[28:31], v[36:39], v[208:211], v[28:31]
	v_mfma_f32_16x16x32_bf16 v[24:27], v[36:39], v[212:215], v[24:27]
	v_mfma_f32_16x16x32_bf16 v[28:31], v[36:39], v[216:219], v[28:31]
	s_nop 3
	s_waitcnt lgkmcnt(0)
	v_lshlrev_b32_e32 v36, 16, v220
	v_and_b32_e32 v37, 0xffff0000, v220
	v_lshlrev_b32_e32 v38, 16, v221
	v_and_b32_e32 v39, 0xffff0000, v221
	v_lshlrev_b32_e32 v40, 16, v222
	v_and_b32_e32 v41, 0xffff0000, v222
	v_lshlrev_b32_e32 v42, 16, v223
	v_and_b32_e32 v43, 0xffff0000, v223
	v_mul_f32_e32 v36, v60, v36
	v_mul_f32_e32 v37, v60, v37
	v_mul_f32_e32 v38, v60, v38
	v_mul_f32_e32 v39, v60, v39
	v_mul_f32_e32 v40, v60, v40
	v_mul_f32_e32 v41, v60, v41
	v_mul_f32_e32 v42, v60, v42
	v_mul_f32_e32 v43, v60, v43
	v_fma_f32 v36, v44, v36, v52
	v_fma_f32 v37, v45, v37, v53
	v_fma_f32 v38, v46, v38, v54
	v_fma_f32 v39, v47, v39, v55
	v_fma_f32 v40, v48, v40, v56
	v_fma_f32 v41, v49, v41, v57
	v_fma_f32 v42, v50, v42, v58
	v_fma_f32 v43, v51, v43, v59
	v_cvt_pk_bf16_f32 v36, v36, v37
	v_cvt_pk_bf16_f32 v37, v38, v39
	v_cvt_pk_bf16_f32 v38, v40, v41
	v_cvt_pk_bf16_f32 v39, v42, v43
	s_nop 1
	v_mfma_f32_16x16x32_bf16 v[0:3], v[36:39], v[236:239], v[0:3]
	v_mfma_f32_16x16x32_bf16 v[4:7], v[36:39], v[240:243], v[4:7]
	v_mfma_f32_16x16x32_bf16 v[0:3], v[36:39], v[244:247], v[0:3]
	v_mfma_f32_16x16x32_bf16 v[4:7], v[36:39], v[248:251], v[4:7]
	s_nop 3
	v_lshlrev_b32_e32 v36, 16, v224
	v_and_b32_e32 v37, 0xffff0000, v224
	v_lshlrev_b32_e32 v38, 16, v225
	v_and_b32_e32 v39, 0xffff0000, v225
	v_lshlrev_b32_e32 v40, 16, v226
	v_and_b32_e32 v41, 0xffff0000, v226
	v_lshlrev_b32_e32 v42, 16, v227
	v_and_b32_e32 v43, 0xffff0000, v227
	v_mul_f32_e32 v36, v61, v36
	v_mul_f32_e32 v37, v61, v37
	v_mul_f32_e32 v38, v61, v38
	v_mul_f32_e32 v39, v61, v39
	v_mul_f32_e32 v40, v61, v40
	v_mul_f32_e32 v41, v61, v41
	v_mul_f32_e32 v42, v61, v42
	v_mul_f32_e32 v43, v61, v43
	v_fma_f32 v36, v44, v36, v52
	v_fma_f32 v37, v45, v37, v53
	v_fma_f32 v38, v46, v38, v54
	v_fma_f32 v39, v47, v39, v55
	v_fma_f32 v40, v48, v40, v56
	v_fma_f32 v41, v49, v41, v57
	v_fma_f32 v42, v50, v42, v58
	v_fma_f32 v43, v51, v43, v59
	v_cvt_pk_bf16_f32 v36, v36, v37
	v_cvt_pk_bf16_f32 v37, v38, v39
	v_cvt_pk_bf16_f32 v38, v40, v41
	v_cvt_pk_bf16_f32 v39, v42, v43
	s_nop 1
	v_mfma_f32_16x16x32_bf16 v[8:11], v[36:39], v[236:239], v[8:11]
	v_mfma_f32_16x16x32_bf16 v[12:15], v[36:39], v[240:243], v[12:15]
	v_mfma_f32_16x16x32_bf16 v[8:11], v[36:39], v[244:247], v[8:11]
	v_mfma_f32_16x16x32_bf16 v[12:15], v[36:39], v[248:251], v[12:15]
	s_nop 3
	v_lshlrev_b32_e32 v36, 16, v228
	v_and_b32_e32 v37, 0xffff0000, v228
	v_lshlrev_b32_e32 v38, 16, v229
	v_and_b32_e32 v39, 0xffff0000, v229
	v_lshlrev_b32_e32 v40, 16, v230
	v_and_b32_e32 v41, 0xffff0000, v230
	v_lshlrev_b32_e32 v42, 16, v231
	v_and_b32_e32 v43, 0xffff0000, v231
	v_mul_f32_e32 v36, v62, v36
	v_mul_f32_e32 v37, v62, v37
	v_mul_f32_e32 v38, v62, v38
	v_mul_f32_e32 v39, v62, v39
	v_mul_f32_e32 v40, v62, v40
	v_mul_f32_e32 v41, v62, v41
	v_mul_f32_e32 v42, v62, v42
	v_mul_f32_e32 v43, v62, v43
	v_fma_f32 v36, v44, v36, v52
	v_fma_f32 v37, v45, v37, v53
	v_fma_f32 v38, v46, v38, v54
	v_fma_f32 v39, v47, v39, v55
	v_fma_f32 v40, v48, v40, v56
	v_fma_f32 v41, v49, v41, v57
	v_fma_f32 v42, v50, v42, v58
	v_fma_f32 v43, v51, v43, v59
	v_cvt_pk_bf16_f32 v36, v36, v37
	v_cvt_pk_bf16_f32 v37, v38, v39
	v_cvt_pk_bf16_f32 v38, v40, v41
	v_cvt_pk_bf16_f32 v39, v42, v43
	s_nop 1
	v_mfma_f32_16x16x32_bf16 v[16:19], v[36:39], v[236:239], v[16:19]
	v_mfma_f32_16x16x32_bf16 v[20:23], v[36:39], v[240:243], v[20:23]
	v_mfma_f32_16x16x32_bf16 v[16:19], v[36:39], v[244:247], v[16:19]
	v_mfma_f32_16x16x32_bf16 v[20:23], v[36:39], v[248:251], v[20:23]
	s_nop 3
	v_lshlrev_b32_e32 v36, 16, v232
	v_and_b32_e32 v37, 0xffff0000, v232
	v_lshlrev_b32_e32 v38, 16, v233
	v_and_b32_e32 v39, 0xffff0000, v233
	v_lshlrev_b32_e32 v40, 16, v234
	v_and_b32_e32 v41, 0xffff0000, v234
	v_lshlrev_b32_e32 v42, 16, v235
	v_and_b32_e32 v43, 0xffff0000, v235
	v_mul_f32_e32 v36, v63, v36
	v_mul_f32_e32 v37, v63, v37
	v_mul_f32_e32 v38, v63, v38
	v_mul_f32_e32 v39, v63, v39
	v_mul_f32_e32 v40, v63, v40
	v_mul_f32_e32 v41, v63, v41
	v_mul_f32_e32 v42, v63, v42
	v_mul_f32_e32 v43, v63, v43
	v_fma_f32 v36, v44, v36, v52
	v_fma_f32 v37, v45, v37, v53
	v_fma_f32 v38, v46, v38, v54
	v_fma_f32 v39, v47, v39, v55
	v_fma_f32 v40, v48, v40, v56
	v_fma_f32 v41, v49, v41, v57
	v_fma_f32 v42, v50, v42, v58
	v_fma_f32 v43, v51, v43, v59
	ds_read_b128 v[44:47], v32 offset:512
	ds_read_b128 v[48:51], v32 offset:528
	ds_read_b128 v[52:55], v32 offset:16896
	ds_read_b128 v[56:59], v32 offset:16912
	v_cvt_pk_bf16_f32 v36, v36, v37
	v_cvt_pk_bf16_f32 v37, v38, v39
	v_cvt_pk_bf16_f32 v38, v40, v41
	v_cvt_pk_bf16_f32 v39, v42, v43
	s_nop 1
	v_mfma_f32_16x16x32_bf16 v[24:27], v[36:39], v[236:239], v[24:27]
	v_mfma_f32_16x16x32_bf16 v[28:31], v[36:39], v[240:243], v[28:31]
	v_mfma_f32_16x16x32_bf16 v[24:27], v[36:39], v[244:247], v[24:27]
	v_mfma_f32_16x16x32_bf16 v[28:31], v[36:39], v[248:251], v[28:31]
	s_nop 3
	global_load_dwordx4 v[188:191], v[64:65], off offset:384
	global_load_dwordx4 v[192:195], v[66:67], off offset:384
	global_load_dwordx4 v[196:199], v[68:69], off offset:384
	global_load_dwordx4 v[200:203], v[70:71], off offset:384
	global_load_dwordx4 v[204:207], v[72:73], off offset:384
	global_load_dwordx4 v[208:211], v[74:75], off offset:384
	global_load_dwordx4 v[212:215], v[76:77], off offset:384
	global_load_dwordx4 v[216:219], v[78:79], off offset:384
	global_load_dwordx4 v[220:223], v[64:65], off offset:448
	global_load_dwordx4 v[224:227], v[66:67], off offset:448
	global_load_dwordx4 v[228:231], v[68:69], off offset:448
	global_load_dwordx4 v[232:235], v[70:71], off offset:448
	global_load_dwordx4 v[236:239], v[72:73], off offset:448
	global_load_dwordx4 v[240:243], v[74:75], off offset:448
	global_load_dwordx4 v[244:247], v[76:77], off offset:448
	global_load_dwordx4 v[248:251], v[78:79], off offset:448
	s_waitcnt vmcnt(16)
	s_waitcnt lgkmcnt(0)
	v_lshlrev_b32_e32 v36, 16, v80
	v_and_b32_e32 v37, 0xffff0000, v80
	v_lshlrev_b32_e32 v38, 16, v81
	v_and_b32_e32 v39, 0xffff0000, v81
	v_lshlrev_b32_e32 v40, 16, v82
	v_and_b32_e32 v41, 0xffff0000, v82
	v_lshlrev_b32_e32 v42, 16, v83
	v_and_b32_e32 v43, 0xffff0000, v83
	v_mul_f32_e32 v36, v60, v36
	v_mul_f32_e32 v37, v60, v37
	v_mul_f32_e32 v38, v60, v38
	v_mul_f32_e32 v39, v60, v39
	v_mul_f32_e32 v40, v60, v40
	v_mul_f32_e32 v41, v60, v41
	v_mul_f32_e32 v42, v60, v42
	v_mul_f32_e32 v43, v60, v43
	v_fma_f32 v36, v44, v36, v52
	v_fma_f32 v37, v45, v37, v53
	v_fma_f32 v38, v46, v38, v54
	v_fma_f32 v39, v47, v39, v55
	v_fma_f32 v40, v48, v40, v56
	v_fma_f32 v41, v49, v41, v57
	v_fma_f32 v42, v50, v42, v58
	v_fma_f32 v43, v51, v43, v59
	v_cvt_pk_bf16_f32 v36, v36, v37
	v_cvt_pk_bf16_f32 v37, v38, v39
	v_cvt_pk_bf16_f32 v38, v40, v41
	v_cvt_pk_bf16_f32 v39, v42, v43
	s_nop 1
	v_mfma_f32_16x16x32_bf16 v[0:3], v[36:39], v[96:99], v[0:3]
	v_mfma_f32_16x16x32_bf16 v[4:7], v[36:39], v[100:103], v[4:7]
	v_mfma_f32_16x16x32_bf16 v[0:3], v[36:39], v[104:107], v[0:3]
	v_mfma_f32_16x16x32_bf16 v[4:7], v[36:39], v[108:111], v[4:7]
	s_nop 3
	v_lshlrev_b32_e32 v36, 16, v84
	v_and_b32_e32 v37, 0xffff0000, v84
	v_lshlrev_b32_e32 v38, 16, v85
	v_and_b32_e32 v39, 0xffff0000, v85
	v_lshlrev_b32_e32 v40, 16, v86
	v_and_b32_e32 v41, 0xffff0000, v86
	v_lshlrev_b32_e32 v42, 16, v87
	v_and_b32_e32 v43, 0xffff0000, v87
	v_mul_f32_e32 v36, v61, v36
	v_mul_f32_e32 v37, v61, v37
	v_mul_f32_e32 v38, v61, v38
	v_mul_f32_e32 v39, v61, v39
	v_mul_f32_e32 v40, v61, v40
	v_mul_f32_e32 v41, v61, v41
	v_mul_f32_e32 v42, v61, v42
	v_mul_f32_e32 v43, v61, v43
	v_fma_f32 v36, v44, v36, v52
	v_fma_f32 v37, v45, v37, v53
	v_fma_f32 v38, v46, v38, v54
	v_fma_f32 v39, v47, v39, v55
	v_fma_f32 v40, v48, v40, v56
	v_fma_f32 v41, v49, v41, v57
	v_fma_f32 v42, v50, v42, v58
	v_fma_f32 v43, v51, v43, v59
	v_cvt_pk_bf16_f32 v36, v36, v37
	v_cvt_pk_bf16_f32 v37, v38, v39
	v_cvt_pk_bf16_f32 v38, v40, v41
	v_cvt_pk_bf16_f32 v39, v42, v43
	s_nop 1
	v_mfma_f32_16x16x32_bf16 v[8:11], v[36:39], v[96:99], v[8:11]
	v_mfma_f32_16x16x32_bf16 v[12:15], v[36:39], v[100:103], v[12:15]
	v_mfma_f32_16x16x32_bf16 v[8:11], v[36:39], v[104:107], v[8:11]
	v_mfma_f32_16x16x32_bf16 v[12:15], v[36:39], v[108:111], v[12:15]
	s_nop 3
	v_lshlrev_b32_e32 v36, 16, v88
	v_and_b32_e32 v37, 0xffff0000, v88
	v_lshlrev_b32_e32 v38, 16, v89
	v_and_b32_e32 v39, 0xffff0000, v89
	v_lshlrev_b32_e32 v40, 16, v90
	v_and_b32_e32 v41, 0xffff0000, v90
	v_lshlrev_b32_e32 v42, 16, v91
	v_and_b32_e32 v43, 0xffff0000, v91
	v_mul_f32_e32 v36, v62, v36
	v_mul_f32_e32 v37, v62, v37
	v_mul_f32_e32 v38, v62, v38
	v_mul_f32_e32 v39, v62, v39
	v_mul_f32_e32 v40, v62, v40
	v_mul_f32_e32 v41, v62, v41
	v_mul_f32_e32 v42, v62, v42
	v_mul_f32_e32 v43, v62, v43
	v_fma_f32 v36, v44, v36, v52
	v_fma_f32 v37, v45, v37, v53
	v_fma_f32 v38, v46, v38, v54
	v_fma_f32 v39, v47, v39, v55
	v_fma_f32 v40, v48, v40, v56
	v_fma_f32 v41, v49, v41, v57
	v_fma_f32 v42, v50, v42, v58
	v_fma_f32 v43, v51, v43, v59
	v_cvt_pk_bf16_f32 v36, v36, v37
	v_cvt_pk_bf16_f32 v37, v38, v39
	v_cvt_pk_bf16_f32 v38, v40, v41
	v_cvt_pk_bf16_f32 v39, v42, v43
	s_nop 1
	v_mfma_f32_16x16x32_bf16 v[16:19], v[36:39], v[96:99], v[16:19]
	v_mfma_f32_16x16x32_bf16 v[20:23], v[36:39], v[100:103], v[20:23]
	v_mfma_f32_16x16x32_bf16 v[16:19], v[36:39], v[104:107], v[16:19]
	v_mfma_f32_16x16x32_bf16 v[20:23], v[36:39], v[108:111], v[20:23]
	s_nop 3
	v_lshlrev_b32_e32 v36, 16, v92
	v_and_b32_e32 v37, 0xffff0000, v92
	v_lshlrev_b32_e32 v38, 16, v93
	v_and_b32_e32 v39, 0xffff0000, v93
	v_lshlrev_b32_e32 v40, 16, v94
	v_and_b32_e32 v41, 0xffff0000, v94
	v_lshlrev_b32_e32 v42, 16, v95
	v_and_b32_e32 v43, 0xffff0000, v95
	v_mul_f32_e32 v36, v63, v36
	v_mul_f32_e32 v37, v63, v37
	v_mul_f32_e32 v38, v63, v38
	v_mul_f32_e32 v39, v63, v39
	v_mul_f32_e32 v40, v63, v40
	v_mul_f32_e32 v41, v63, v41
	v_mul_f32_e32 v42, v63, v42
	v_mul_f32_e32 v43, v63, v43
	v_fma_f32 v36, v44, v36, v52
	v_fma_f32 v37, v45, v37, v53
	v_fma_f32 v38, v46, v38, v54
	v_fma_f32 v39, v47, v39, v55
	v_fma_f32 v40, v48, v40, v56
	v_fma_f32 v41, v49, v41, v57
	v_fma_f32 v42, v50, v42, v58
	v_fma_f32 v43, v51, v43, v59
	ds_read_b128 v[44:47], v32 offset:640
	ds_read_b128 v[48:51], v32 offset:656
	ds_read_b128 v[52:55], v32 offset:17024
	ds_read_b128 v[56:59], v32 offset:17040
	v_cvt_pk_bf16_f32 v36, v36, v37
	v_cvt_pk_bf16_f32 v37, v38, v39
	v_cvt_pk_bf16_f32 v38, v40, v41
	v_cvt_pk_bf16_f32 v39, v42, v43
	s_nop 1
	v_mfma_f32_16x16x32_bf16 v[24:27], v[36:39], v[96:99], v[24:27]
	v_mfma_f32_16x16x32_bf16 v[28:31], v[36:39], v[100:103], v[28:31]
	v_mfma_f32_16x16x32_bf16 v[24:27], v[36:39], v[104:107], v[24:27]
	v_mfma_f32_16x16x32_bf16 v[28:31], v[36:39], v[108:111], v[28:31]
	s_nop 3
	s_waitcnt lgkmcnt(0)
	v_lshlrev_b32_e32 v36, 16, v112
	v_and_b32_e32 v37, 0xffff0000, v112
	v_lshlrev_b32_e32 v38, 16, v113
	v_and_b32_e32 v39, 0xffff0000, v113
	v_lshlrev_b32_e32 v40, 16, v114
	v_and_b32_e32 v41, 0xffff0000, v114
	v_lshlrev_b32_e32 v42, 16, v115
	v_and_b32_e32 v43, 0xffff0000, v115
	v_mul_f32_e32 v36, v60, v36
	v_mul_f32_e32 v37, v60, v37
	v_mul_f32_e32 v38, v60, v38
	v_mul_f32_e32 v39, v60, v39
	v_mul_f32_e32 v40, v60, v40
	v_mul_f32_e32 v41, v60, v41
	v_mul_f32_e32 v42, v60, v42
	v_mul_f32_e32 v43, v60, v43
	v_fma_f32 v36, v44, v36, v52
	v_fma_f32 v37, v45, v37, v53
	v_fma_f32 v38, v46, v38, v54
	v_fma_f32 v39, v47, v39, v55
	v_fma_f32 v40, v48, v40, v56
	v_fma_f32 v41, v49, v41, v57
	v_fma_f32 v42, v50, v42, v58
	v_fma_f32 v43, v51, v43, v59
	v_cvt_pk_bf16_f32 v36, v36, v37
	v_cvt_pk_bf16_f32 v37, v38, v39
	v_cvt_pk_bf16_f32 v38, v40, v41
	v_cvt_pk_bf16_f32 v39, v42, v43
	s_nop 1
	v_mfma_f32_16x16x32_bf16 v[0:3], v[36:39], v[172:175], v[0:3]
	v_mfma_f32_16x16x32_bf16 v[4:7], v[36:39], v[176:179], v[4:7]
	v_mfma_f32_16x16x32_bf16 v[0:3], v[36:39], v[180:183], v[0:3]
	v_mfma_f32_16x16x32_bf16 v[4:7], v[36:39], v[184:187], v[4:7]
	s_nop 3
	v_lshlrev_b32_e32 v36, 16, v116
	v_and_b32_e32 v37, 0xffff0000, v116
	v_lshlrev_b32_e32 v38, 16, v117
	v_and_b32_e32 v39, 0xffff0000, v117
	v_lshlrev_b32_e32 v40, 16, v118
	v_and_b32_e32 v41, 0xffff0000, v118
	v_lshlrev_b32_e32 v42, 16, v119
	v_and_b32_e32 v43, 0xffff0000, v119
	v_mul_f32_e32 v36, v61, v36
	v_mul_f32_e32 v37, v61, v37
	v_mul_f32_e32 v38, v61, v38
	v_mul_f32_e32 v39, v61, v39
	v_mul_f32_e32 v40, v61, v40
	v_mul_f32_e32 v41, v61, v41
	v_mul_f32_e32 v42, v61, v42
	v_mul_f32_e32 v43, v61, v43
	v_fma_f32 v36, v44, v36, v52
	v_fma_f32 v37, v45, v37, v53
	v_fma_f32 v38, v46, v38, v54
	v_fma_f32 v39, v47, v39, v55
	v_fma_f32 v40, v48, v40, v56
	v_fma_f32 v41, v49, v41, v57
	v_fma_f32 v42, v50, v42, v58
	v_fma_f32 v43, v51, v43, v59
	v_cvt_pk_bf16_f32 v36, v36, v37
	v_cvt_pk_bf16_f32 v37, v38, v39
	v_cvt_pk_bf16_f32 v38, v40, v41
	v_cvt_pk_bf16_f32 v39, v42, v43
	s_nop 1
	v_mfma_f32_16x16x32_bf16 v[8:11], v[36:39], v[172:175], v[8:11]
	v_mfma_f32_16x16x32_bf16 v[12:15], v[36:39], v[176:179], v[12:15]
	v_mfma_f32_16x16x32_bf16 v[8:11], v[36:39], v[180:183], v[8:11]
	v_mfma_f32_16x16x32_bf16 v[12:15], v[36:39], v[184:187], v[12:15]
	s_nop 3
	v_lshlrev_b32_e32 v36, 16, v164
	v_and_b32_e32 v37, 0xffff0000, v164
	v_lshlrev_b32_e32 v38, 16, v165
	v_and_b32_e32 v39, 0xffff0000, v165
	v_lshlrev_b32_e32 v40, 16, v166
	v_and_b32_e32 v41, 0xffff0000, v166
	v_lshlrev_b32_e32 v42, 16, v167
	v_and_b32_e32 v43, 0xffff0000, v167
	v_mul_f32_e32 v36, v62, v36
	v_mul_f32_e32 v37, v62, v37
	v_mul_f32_e32 v38, v62, v38
	v_mul_f32_e32 v39, v62, v39
	v_mul_f32_e32 v40, v62, v40
	v_mul_f32_e32 v41, v62, v41
	v_mul_f32_e32 v42, v62, v42
	v_mul_f32_e32 v43, v62, v43
	v_fma_f32 v36, v44, v36, v52
	v_fma_f32 v37, v45, v37, v53
	v_fma_f32 v38, v46, v38, v54
	v_fma_f32 v39, v47, v39, v55
	v_fma_f32 v40, v48, v40, v56
	v_fma_f32 v41, v49, v41, v57
	v_fma_f32 v42, v50, v42, v58
	v_fma_f32 v43, v51, v43, v59
	v_cvt_pk_bf16_f32 v36, v36, v37
	v_cvt_pk_bf16_f32 v37, v38, v39
	v_cvt_pk_bf16_f32 v38, v40, v41
	v_cvt_pk_bf16_f32 v39, v42, v43
	s_nop 1
	v_mfma_f32_16x16x32_bf16 v[16:19], v[36:39], v[172:175], v[16:19]
	v_mfma_f32_16x16x32_bf16 v[20:23], v[36:39], v[176:179], v[20:23]
	v_mfma_f32_16x16x32_bf16 v[16:19], v[36:39], v[180:183], v[16:19]
	v_mfma_f32_16x16x32_bf16 v[20:23], v[36:39], v[184:187], v[20:23]
	s_nop 3
	v_lshlrev_b32_e32 v36, 16, v168
	v_and_b32_e32 v37, 0xffff0000, v168
	v_lshlrev_b32_e32 v38, 16, v169
	v_and_b32_e32 v39, 0xffff0000, v169
	v_lshlrev_b32_e32 v40, 16, v170
	v_and_b32_e32 v41, 0xffff0000, v170
	v_lshlrev_b32_e32 v42, 16, v171
	v_and_b32_e32 v43, 0xffff0000, v171
	v_mul_f32_e32 v36, v63, v36
	v_mul_f32_e32 v37, v63, v37
	v_mul_f32_e32 v38, v63, v38
	v_mul_f32_e32 v39, v63, v39
	v_mul_f32_e32 v40, v63, v40
	v_mul_f32_e32 v41, v63, v41
	v_mul_f32_e32 v42, v63, v42
	v_mul_f32_e32 v43, v63, v43
	v_fma_f32 v36, v44, v36, v52
	v_fma_f32 v37, v45, v37, v53
	v_fma_f32 v38, v46, v38, v54
	v_fma_f32 v39, v47, v39, v55
	v_fma_f32 v40, v48, v40, v56
	v_fma_f32 v41, v49, v41, v57
	v_fma_f32 v42, v50, v42, v58
	v_fma_f32 v43, v51, v43, v59
	ds_read_b128 v[44:47], v32 offset:768
	ds_read_b128 v[48:51], v32 offset:784
	ds_read_b128 v[52:55], v32 offset:17152
	ds_read_b128 v[56:59], v32 offset:17168
	v_cvt_pk_bf16_f32 v36, v36, v37
	v_cvt_pk_bf16_f32 v37, v38, v39
	v_cvt_pk_bf16_f32 v38, v40, v41
	v_cvt_pk_bf16_f32 v39, v42, v43
	s_nop 1
	v_mfma_f32_16x16x32_bf16 v[24:27], v[36:39], v[172:175], v[24:27]
	v_mfma_f32_16x16x32_bf16 v[28:31], v[36:39], v[176:179], v[28:31]
	v_mfma_f32_16x16x32_bf16 v[24:27], v[36:39], v[180:183], v[24:27]
	v_mfma_f32_16x16x32_bf16 v[28:31], v[36:39], v[184:187], v[28:31]
	s_nop 3
	s_waitcnt vmcnt(0)
	s_waitcnt lgkmcnt(0)
	v_lshlrev_b32_e32 v36, 16, v188
	v_and_b32_e32 v37, 0xffff0000, v188
	v_lshlrev_b32_e32 v38, 16, v189
	v_and_b32_e32 v39, 0xffff0000, v189
	v_lshlrev_b32_e32 v40, 16, v190
	v_and_b32_e32 v41, 0xffff0000, v190
	v_lshlrev_b32_e32 v42, 16, v191
	v_and_b32_e32 v43, 0xffff0000, v191
	v_mul_f32_e32 v36, v60, v36
	v_mul_f32_e32 v37, v60, v37
	v_mul_f32_e32 v38, v60, v38
	v_mul_f32_e32 v39, v60, v39
	v_mul_f32_e32 v40, v60, v40
	v_mul_f32_e32 v41, v60, v41
	v_mul_f32_e32 v42, v60, v42
	v_mul_f32_e32 v43, v60, v43
	v_fma_f32 v36, v44, v36, v52
	v_fma_f32 v37, v45, v37, v53
	v_fma_f32 v38, v46, v38, v54
	v_fma_f32 v39, v47, v39, v55
	v_fma_f32 v40, v48, v40, v56
	v_fma_f32 v41, v49, v41, v57
	v_fma_f32 v42, v50, v42, v58
	v_fma_f32 v43, v51, v43, v59
	v_cvt_pk_bf16_f32 v36, v36, v37
	v_cvt_pk_bf16_f32 v37, v38, v39
	v_cvt_pk_bf16_f32 v38, v40, v41
	v_cvt_pk_bf16_f32 v39, v42, v43
	s_nop 1
	v_mfma_f32_16x16x32_bf16 v[0:3], v[36:39], v[204:207], v[0:3]
	v_mfma_f32_16x16x32_bf16 v[4:7], v[36:39], v[208:211], v[4:7]
	v_mfma_f32_16x16x32_bf16 v[0:3], v[36:39], v[212:215], v[0:3]
	v_mfma_f32_16x16x32_bf16 v[4:7], v[36:39], v[216:219], v[4:7]
	s_nop 3
	v_lshlrev_b32_e32 v36, 16, v192
	v_and_b32_e32 v37, 0xffff0000, v192
	v_lshlrev_b32_e32 v38, 16, v193
	v_and_b32_e32 v39, 0xffff0000, v193
	v_lshlrev_b32_e32 v40, 16, v194
	v_and_b32_e32 v41, 0xffff0000, v194
	v_lshlrev_b32_e32 v42, 16, v195
	v_and_b32_e32 v43, 0xffff0000, v195
	v_mul_f32_e32 v36, v61, v36
	v_mul_f32_e32 v37, v61, v37
	v_mul_f32_e32 v38, v61, v38
	v_mul_f32_e32 v39, v61, v39
	v_mul_f32_e32 v40, v61, v40
	v_mul_f32_e32 v41, v61, v41
	v_mul_f32_e32 v42, v61, v42
	v_mul_f32_e32 v43, v61, v43
	v_fma_f32 v36, v44, v36, v52
	v_fma_f32 v37, v45, v37, v53
	v_fma_f32 v38, v46, v38, v54
	v_fma_f32 v39, v47, v39, v55
	v_fma_f32 v40, v48, v40, v56
	v_fma_f32 v41, v49, v41, v57
	v_fma_f32 v42, v50, v42, v58
	v_fma_f32 v43, v51, v43, v59
	v_cvt_pk_bf16_f32 v36, v36, v37
	v_cvt_pk_bf16_f32 v37, v38, v39
	v_cvt_pk_bf16_f32 v38, v40, v41
	v_cvt_pk_bf16_f32 v39, v42, v43
	s_nop 1
	v_mfma_f32_16x16x32_bf16 v[8:11], v[36:39], v[204:207], v[8:11]
	v_mfma_f32_16x16x32_bf16 v[12:15], v[36:39], v[208:211], v[12:15]
	v_mfma_f32_16x16x32_bf16 v[8:11], v[36:39], v[212:215], v[8:11]
	v_mfma_f32_16x16x32_bf16 v[12:15], v[36:39], v[216:219], v[12:15]
	s_nop 3
	v_lshlrev_b32_e32 v36, 16, v196
	v_and_b32_e32 v37, 0xffff0000, v196
	v_lshlrev_b32_e32 v38, 16, v197
	v_and_b32_e32 v39, 0xffff0000, v197
	v_lshlrev_b32_e32 v40, 16, v198
	v_and_b32_e32 v41, 0xffff0000, v198
	v_lshlrev_b32_e32 v42, 16, v199
	v_and_b32_e32 v43, 0xffff0000, v199
	v_mul_f32_e32 v36, v62, v36
	v_mul_f32_e32 v37, v62, v37
	v_mul_f32_e32 v38, v62, v38
	v_mul_f32_e32 v39, v62, v39
	v_mul_f32_e32 v40, v62, v40
	v_mul_f32_e32 v41, v62, v41
	v_mul_f32_e32 v42, v62, v42
	v_mul_f32_e32 v43, v62, v43
	v_fma_f32 v36, v44, v36, v52
	v_fma_f32 v37, v45, v37, v53
	v_fma_f32 v38, v46, v38, v54
	v_fma_f32 v39, v47, v39, v55
	v_fma_f32 v40, v48, v40, v56
	v_fma_f32 v41, v49, v41, v57
	v_fma_f32 v42, v50, v42, v58
	v_fma_f32 v43, v51, v43, v59
	v_cvt_pk_bf16_f32 v36, v36, v37
	v_cvt_pk_bf16_f32 v37, v38, v39
	v_cvt_pk_bf16_f32 v38, v40, v41
	v_cvt_pk_bf16_f32 v39, v42, v43
	s_nop 1
	v_mfma_f32_16x16x32_bf16 v[16:19], v[36:39], v[204:207], v[16:19]
	v_mfma_f32_16x16x32_bf16 v[20:23], v[36:39], v[208:211], v[20:23]
	v_mfma_f32_16x16x32_bf16 v[16:19], v[36:39], v[212:215], v[16:19]
	v_mfma_f32_16x16x32_bf16 v[20:23], v[36:39], v[216:219], v[20:23]
	s_nop 3
	v_lshlrev_b32_e32 v36, 16, v200
	v_and_b32_e32 v37, 0xffff0000, v200
	v_lshlrev_b32_e32 v38, 16, v201
	v_and_b32_e32 v39, 0xffff0000, v201
	v_lshlrev_b32_e32 v40, 16, v202
	v_and_b32_e32 v41, 0xffff0000, v202
	v_lshlrev_b32_e32 v42, 16, v203
	v_and_b32_e32 v43, 0xffff0000, v203
	v_mul_f32_e32 v36, v63, v36
	v_mul_f32_e32 v37, v63, v37
	v_mul_f32_e32 v38, v63, v38
	v_mul_f32_e32 v39, v63, v39
	v_mul_f32_e32 v40, v63, v40
	v_mul_f32_e32 v41, v63, v41
	v_mul_f32_e32 v42, v63, v42
	v_mul_f32_e32 v43, v63, v43
	v_fma_f32 v36, v44, v36, v52
	v_fma_f32 v37, v45, v37, v53
	v_fma_f32 v38, v46, v38, v54
	v_fma_f32 v39, v47, v39, v55
	v_fma_f32 v40, v48, v40, v56
	v_fma_f32 v41, v49, v41, v57
	v_fma_f32 v42, v50, v42, v58
	v_fma_f32 v43, v51, v43, v59
	ds_read_b128 v[44:47], v32 offset:896
	ds_read_b128 v[48:51], v32 offset:912
	ds_read_b128 v[52:55], v32 offset:17280
	ds_read_b128 v[56:59], v32 offset:17296
	v_cvt_pk_bf16_f32 v36, v36, v37
	v_cvt_pk_bf16_f32 v37, v38, v39
	v_cvt_pk_bf16_f32 v38, v40, v41
	v_cvt_pk_bf16_f32 v39, v42, v43
	s_nop 1
	v_mfma_f32_16x16x32_bf16 v[24:27], v[36:39], v[204:207], v[24:27]
	v_mfma_f32_16x16x32_bf16 v[28:31], v[36:39], v[208:211], v[28:31]
	v_mfma_f32_16x16x32_bf16 v[24:27], v[36:39], v[212:215], v[24:27]
	v_mfma_f32_16x16x32_bf16 v[28:31], v[36:39], v[216:219], v[28:31]
	s_nop 3
	s_waitcnt lgkmcnt(0)
	v_lshlrev_b32_e32 v36, 16, v220
	v_and_b32_e32 v37, 0xffff0000, v220
	v_lshlrev_b32_e32 v38, 16, v221
	v_and_b32_e32 v39, 0xffff0000, v221
	v_lshlrev_b32_e32 v40, 16, v222
	v_and_b32_e32 v41, 0xffff0000, v222
	v_lshlrev_b32_e32 v42, 16, v223
	v_and_b32_e32 v43, 0xffff0000, v223
	v_mul_f32_e32 v36, v60, v36
	v_mul_f32_e32 v37, v60, v37
	v_mul_f32_e32 v38, v60, v38
	v_mul_f32_e32 v39, v60, v39
	v_mul_f32_e32 v40, v60, v40
	v_mul_f32_e32 v41, v60, v41
	v_mul_f32_e32 v42, v60, v42
	v_mul_f32_e32 v43, v60, v43
	v_fma_f32 v36, v44, v36, v52
	v_fma_f32 v37, v45, v37, v53
	v_fma_f32 v38, v46, v38, v54
	v_fma_f32 v39, v47, v39, v55
	v_fma_f32 v40, v48, v40, v56
	v_fma_f32 v41, v49, v41, v57
	v_fma_f32 v42, v50, v42, v58
	v_fma_f32 v43, v51, v43, v59
	v_cvt_pk_bf16_f32 v36, v36, v37
	v_cvt_pk_bf16_f32 v37, v38, v39
	v_cvt_pk_bf16_f32 v38, v40, v41
	v_cvt_pk_bf16_f32 v39, v42, v43
	s_nop 1
	v_mfma_f32_16x16x32_bf16 v[0:3], v[36:39], v[236:239], v[0:3]
	v_mfma_f32_16x16x32_bf16 v[4:7], v[36:39], v[240:243], v[4:7]
	v_mfma_f32_16x16x32_bf16 v[0:3], v[36:39], v[244:247], v[0:3]
	v_mfma_f32_16x16x32_bf16 v[4:7], v[36:39], v[248:251], v[4:7]
	s_nop 3
	v_lshlrev_b32_e32 v36, 16, v224
	v_and_b32_e32 v37, 0xffff0000, v224
	v_lshlrev_b32_e32 v38, 16, v225
	v_and_b32_e32 v39, 0xffff0000, v225
	v_lshlrev_b32_e32 v40, 16, v226
	v_and_b32_e32 v41, 0xffff0000, v226
	v_lshlrev_b32_e32 v42, 16, v227
	v_and_b32_e32 v43, 0xffff0000, v227
	v_mul_f32_e32 v36, v61, v36
	v_mul_f32_e32 v37, v61, v37
	v_mul_f32_e32 v38, v61, v38
	v_mul_f32_e32 v39, v61, v39
	v_mul_f32_e32 v40, v61, v40
	v_mul_f32_e32 v41, v61, v41
	v_mul_f32_e32 v42, v61, v42
	v_mul_f32_e32 v43, v61, v43
	v_fma_f32 v36, v44, v36, v52
	v_fma_f32 v37, v45, v37, v53
	v_fma_f32 v38, v46, v38, v54
	v_fma_f32 v39, v47, v39, v55
	v_fma_f32 v40, v48, v40, v56
	v_fma_f32 v41, v49, v41, v57
	v_fma_f32 v42, v50, v42, v58
	v_fma_f32 v43, v51, v43, v59
	v_cvt_pk_bf16_f32 v36, v36, v37
	v_cvt_pk_bf16_f32 v37, v38, v39
	v_cvt_pk_bf16_f32 v38, v40, v41
	v_cvt_pk_bf16_f32 v39, v42, v43
	s_nop 1
	v_mfma_f32_16x16x32_bf16 v[8:11], v[36:39], v[236:239], v[8:11]
	v_mfma_f32_16x16x32_bf16 v[12:15], v[36:39], v[240:243], v[12:15]
	v_mfma_f32_16x16x32_bf16 v[8:11], v[36:39], v[244:247], v[8:11]
	v_mfma_f32_16x16x32_bf16 v[12:15], v[36:39], v[248:251], v[12:15]
	s_nop 3
	v_lshlrev_b32_e32 v36, 16, v228
	v_and_b32_e32 v37, 0xffff0000, v228
	v_lshlrev_b32_e32 v38, 16, v229
	v_and_b32_e32 v39, 0xffff0000, v229
	v_lshlrev_b32_e32 v40, 16, v230
	v_and_b32_e32 v41, 0xffff0000, v230
	v_lshlrev_b32_e32 v42, 16, v231
	v_and_b32_e32 v43, 0xffff0000, v231
	v_mul_f32_e32 v36, v62, v36
	v_mul_f32_e32 v37, v62, v37
	v_mul_f32_e32 v38, v62, v38
	v_mul_f32_e32 v39, v62, v39
	v_mul_f32_e32 v40, v62, v40
	v_mul_f32_e32 v41, v62, v41
	v_mul_f32_e32 v42, v62, v42
	v_mul_f32_e32 v43, v62, v43
	v_fma_f32 v36, v44, v36, v52
	v_fma_f32 v37, v45, v37, v53
	v_fma_f32 v38, v46, v38, v54
	v_fma_f32 v39, v47, v39, v55
	v_fma_f32 v40, v48, v40, v56
	v_fma_f32 v41, v49, v41, v57
	v_fma_f32 v42, v50, v42, v58
	v_fma_f32 v43, v51, v43, v59
	v_cvt_pk_bf16_f32 v36, v36, v37
	v_cvt_pk_bf16_f32 v37, v38, v39
	v_cvt_pk_bf16_f32 v38, v40, v41
	v_cvt_pk_bf16_f32 v39, v42, v43
	s_nop 1
	v_mfma_f32_16x16x32_bf16 v[16:19], v[36:39], v[236:239], v[16:19]
	v_mfma_f32_16x16x32_bf16 v[20:23], v[36:39], v[240:243], v[20:23]
	v_mfma_f32_16x16x32_bf16 v[16:19], v[36:39], v[244:247], v[16:19]
	v_mfma_f32_16x16x32_bf16 v[20:23], v[36:39], v[248:251], v[20:23]
	s_nop 3
	v_lshlrev_b32_e32 v36, 16, v232
	v_and_b32_e32 v37, 0xffff0000, v232
	v_lshlrev_b32_e32 v38, 16, v233
	v_and_b32_e32 v39, 0xffff0000, v233
	v_lshlrev_b32_e32 v40, 16, v234
	v_and_b32_e32 v41, 0xffff0000, v234
	v_lshlrev_b32_e32 v42, 16, v235
	v_and_b32_e32 v43, 0xffff0000, v235
	v_mul_f32_e32 v36, v63, v36
	v_mul_f32_e32 v37, v63, v37
	v_mul_f32_e32 v38, v63, v38
	v_mul_f32_e32 v39, v63, v39
	v_mul_f32_e32 v40, v63, v40
	v_mul_f32_e32 v41, v63, v41
	v_mul_f32_e32 v42, v63, v42
	v_mul_f32_e32 v43, v63, v43
	v_fma_f32 v36, v44, v36, v52
	v_fma_f32 v37, v45, v37, v53
	v_fma_f32 v38, v46, v38, v54
	v_fma_f32 v39, v47, v39, v55
	v_fma_f32 v40, v48, v40, v56
	v_fma_f32 v41, v49, v41, v57
	v_fma_f32 v42, v50, v42, v58
	v_fma_f32 v43, v51, v43, v59
	v_cvt_pk_bf16_f32 v36, v36, v37
	v_cvt_pk_bf16_f32 v37, v38, v39
	v_cvt_pk_bf16_f32 v38, v40, v41
	v_cvt_pk_bf16_f32 v39, v42, v43
	s_nop 1
	v_mfma_f32_16x16x32_bf16 v[24:27], v[36:39], v[236:239], v[24:27]
	v_mfma_f32_16x16x32_bf16 v[28:31], v[36:39], v[240:243], v[28:31]
	v_mfma_f32_16x16x32_bf16 v[24:27], v[36:39], v[244:247], v[24:27]
	v_mfma_f32_16x16x32_bf16 v[28:31], v[36:39], v[248:251], v[28:31]
	s_nop 3
	s_nop 7
	s_nop 7
	ds_write_b32 v34, v0 offset:0
	ds_write_b32 v34, v1 offset:128
	ds_write_b32 v34, v2 offset:256
	ds_write_b32 v34, v3 offset:384
	ds_write_b32 v34, v4 offset:64
	ds_write_b32 v34, v5 offset:192
	ds_write_b32 v34, v6 offset:320
	ds_write_b32 v34, v7 offset:448
	ds_write_b32 v34, v8 offset:2048
	ds_write_b32 v34, v9 offset:2176
	ds_write_b32 v34, v10 offset:2304
	ds_write_b32 v34, v11 offset:2432
	ds_write_b32 v34, v12 offset:2112
	ds_write_b32 v34, v13 offset:2240
	ds_write_b32 v34, v14 offset:2368
	ds_write_b32 v34, v15 offset:2496
	ds_write_b32 v34, v16 offset:4096
	ds_write_b32 v34, v17 offset:4224
	ds_write_b32 v34, v18 offset:4352
	ds_write_b32 v34, v19 offset:4480
	ds_write_b32 v34, v20 offset:4160
	ds_write_b32 v34, v21 offset:4288
	ds_write_b32 v34, v22 offset:4416
	ds_write_b32 v34, v23 offset:4544
	ds_write_b32 v34, v24 offset:6144
	ds_write_b32 v34, v25 offset:6272
	ds_write_b32 v34, v26 offset:6400
	ds_write_b32 v34, v27 offset:6528
	ds_write_b32 v34, v28 offset:6208
	ds_write_b32 v34, v29 offset:6336
	ds_write_b32 v34, v30 offset:6464
	ds_write_b32 v34, v31 offset:6592
	s_waitcnt lgkmcnt(0)
	s_barrier
	v_lshlrev_b32_e32 v33, 4, v120
	v_add_u32_e32 v32, 0x10000, v33
	ds_read_b128 v[36:39], v32 offset:0
	ds_read_b128 v[40:43], v32 offset:8192
	ds_read_b128 v[44:47], v32 offset:16384
	ds_read_b128 v[48:51], v32 offset:24576
	ds_read_b128 v[52:55], v32 offset:32768
	ds_read_b128 v[56:59], v32 offset:40960
	ds_read_b128 v[60:63], v32 offset:49152
	ds_read_b128 v[0:3], v32 offset:57344
	s_waitcnt lgkmcnt(0)
	v_add_f32_e32 v36, v36, v40
	v_add_f32_e32 v37, v37, v41
	v_add_f32_e32 v38, v38, v42
	v_add_f32_e32 v39, v39, v43
	v_add_f32_e32 v36, v36, v44
	v_add_f32_e32 v37, v37, v45
	v_add_f32_e32 v38, v38, v46
	v_add_f32_e32 v39, v39, v47
	v_add_f32_e32 v36, v36, v48
	v_add_f32_e32 v37, v37, v49
	v_add_f32_e32 v38, v38, v50
	v_add_f32_e32 v39, v39, v51
	v_add_f32_e32 v36, v36, v52
	v_add_f32_e32 v37, v37, v53
	v_add_f32_e32 v38, v38, v54
	v_add_f32_e32 v39, v39, v55
	v_add_f32_e32 v36, v36, v56
	v_add_f32_e32 v37, v37, v57
	v_add_f32_e32 v38, v38, v58
	v_add_f32_e32 v39, v39, v59
	v_add_f32_e32 v36, v36, v60
	v_add_f32_e32 v37, v37, v61
	v_add_f32_e32 v38, v38, v62
	v_add_f32_e32 v39, v39, v63
	v_add_f32_e32 v36, v36, v0
	v_add_f32_e32 v37, v37, v1
	v_add_f32_e32 v38, v38, v2
	v_add_f32_e32 v39, v39, v3
	v_mov_b32_e32 v40, 0
	v_mov_b32_e32 v41, 0
	v_mov_b32_e32 v42, 0
	v_mov_b32_e32 v43, 0
	ds_write_b128 v33, v[36:39] offset:40960
	ds_write_b128 v33, v[40:43] offset:49152
	s_mov_b32 s88, s2
	s_waitcnt lgkmcnt(0)
	s_barrier
	s_and_saveexec_b64 s[8:9], s[52:53]
	s_cbranch_execz .LBB0_1076
	ds_read_b128 v[0:3], v143 offset:40960
	ds_read_b128 v[4:7], v143 offset:40976
	ds_read_b128 v[8:11], v143 offset:40992
	ds_read_b128 v[28:31], v143 offset:41008
	ds_read_b128 v[12:15], v143 offset:49152
	global_load_dwordx4 v[32:35], v123, s[68:69] offset:48
	global_load_dwordx4 v[36:39], v123, s[68:69] offset:32
	global_load_dwordx4 v[16:19], v123, s[68:69] offset:16
	global_load_dwordx4 v[20:23], v123, s[68:69]
	s_mov_b32 s20, 0xff800000
	s_mov_b32 s3, s34
	s_mov_b64 s[18:19], s[16:17]
	s_waitcnt lgkmcnt(0)
	v_add_f32_e32 v0, v0, v12
	s_mov_b64 s[16:17], s[4:5]
	s_mov_b64 s[4:5], s[52:53]
	s_ashr_i32 s89, s88, 31
	s_waitcnt vmcnt(0)
	v_add_f32_e32 v27, v0, v20
	v_add_f32_e32 v0, v1, v13
	v_add_f32_e32 v26, v0, v21
	v_add_f32_e32 v0, v2, v14
	v_add_f32_e32 v25, v0, v22
	v_add_f32_e32 v0, v3, v15
	v_add_f32_e32 v24, v0, v23
	ds_read_b128 v[0:3], v143 offset:49168
	v_cmp_lg_f32_e32 vcc, s20, v27
	s_waitcnt lgkmcnt(0)
	v_add_f32_e32 v0, v4, v0
	v_add_f32_e32 v23, v0, v16
	v_add_f32_e32 v0, v5, v1
	v_add_f32_e32 v22, v0, v17
	v_add_f32_e32 v0, v6, v2
	v_add_f32_e32 v21, v0, v18
	v_add_f32_e32 v0, v7, v3
	v_add_f32_e32 v20, v0, v19
	ds_read_b128 v[0:3], v143 offset:49184
	s_waitcnt lgkmcnt(0)
	v_add_f32_e32 v0, v8, v0
	v_add_f32_e32 v19, v0, v36
	v_add_f32_e32 v0, v9, v1
	v_add_f32_e32 v18, v0, v37
	v_add_f32_e32 v0, v10, v2
	v_add_f32_e32 v17, v0, v38
	v_add_f32_e32 v0, v11, v3
	v_add_f32_e32 v16, v0, v39
	ds_read_b128 v[0:3], v143 offset:49200
	s_waitcnt lgkmcnt(0)
	v_add_f32_e32 v0, v28, v0
	v_add_f32_e32 v15, v0, v32
	v_add_f32_e32 v0, v29, v1
	v_add_f32_e32 v14, v0, v33
	v_add_f32_e32 v0, v30, v2
	v_add_f32_e32 v13, v0, v34
	v_add_f32_e32 v0, v31, v3
	v_add_f32_e32 v12, v0, v35
	ds_read_b128 v[32:35], v143 offset:41024
	ds_read_b128 v[36:39], v143 offset:49216
	global_load_dwordx4 v[0:3], v123, s[68:69] offset:112
	global_load_dwordx4 v[4:7], v123, s[68:69] offset:96
	global_load_dwordx4 v[8:11], v123, s[68:69] offset:80
	global_load_dwordx4 v[40:43], v123, s[68:69] offset:64
	s_waitcnt lgkmcnt(0)
	v_add_f32_e32 v28, v32, v36
	s_waitcnt vmcnt(0)
	v_add_f32_e32 v31, v28, v40
	v_add_f32_e32 v28, v33, v37
	v_add_f32_e32 v30, v28, v41
	v_add_f32_e32 v28, v34, v38
	v_add_f32_e32 v29, v28, v42
	v_add_f32_e32 v28, v35, v39
	ds_read_b128 v[34:37], v143 offset:41040
	ds_read_b128 v[38:41], v143 offset:49232
	v_add_f32_e32 v28, v28, v43
	s_waitcnt lgkmcnt(0)
	v_add_f32_e32 v32, v34, v38
	v_add_f32_e32 v33, v32, v8
	v_add_f32_e32 v8, v35, v39
	v_add_f32_e32 v32, v8, v9
	v_add_f32_e32 v8, v36, v40
	v_add_f32_e32 v9, v8, v10
	v_add_f32_e32 v8, v37, v41
	ds_read_b128 v[34:37], v143 offset:41056
	ds_read_b128 v[38:41], v143 offset:49248
	v_add_f32_e32 v8, v8, v11
	s_waitcnt lgkmcnt(0)
	v_add_f32_e32 v10, v34, v38
	v_add_f32_e32 v11, v10, v4
	v_add_f32_e32 v4, v35, v39
	v_add_f32_e32 v10, v4, v5
	v_add_f32_e32 v4, v36, v40
	v_add_f32_e32 v5, v4, v6
	v_add_f32_e32 v4, v37, v41
	ds_read_b128 v[36:39], v143 offset:41072
	ds_read_b128 v[40:43], v143 offset:49264
	v_add_f32_e32 v4, v4, v7
	s_waitcnt lgkmcnt(0)
	v_add_f32_e32 v6, v36, v40
	v_add_f32_e32 v36, v6, v0
	v_add_f32_e32 v0, v37, v41
	v_add_f32_e32 v35, v0, v1
	v_add_f32_e32 v0, v38, v42
	v_add_f32_e32 v2, v0, v2
	v_add_f32_e32 v0, v39, v43
	v_add_f32_e32 v1, v0, v3
	v_cndmask_b32_e32 v0, v155, v27, vcc
	v_cmp_gt_f32_e32 vcc, v26, v0
	s_nop 1
	v_cndmask_b32_e32 v0, v0, v26, vcc
	v_cndmask_b32_e64 v3, 0, 1, vcc
	v_cmp_gt_f32_e32 vcc, v25, v0
	s_nop 1
	v_cndmask_b32_e32 v0, v0, v25, vcc
	v_cndmask_b32_e64 v3, v3, 2, vcc
	v_cmp_gt_f32_e32 vcc, v24, v0
	s_nop 1
	v_cndmask_b32_e32 v0, v0, v24, vcc
	v_cndmask_b32_e64 v3, v3, 3, vcc
	v_cmp_gt_f32_e32 vcc, v23, v0
	s_nop 1
	v_cndmask_b32_e32 v0, v0, v23, vcc
	v_cndmask_b32_e64 v3, v3, 4, vcc
	v_cmp_gt_f32_e32 vcc, v22, v0
	s_nop 1
	v_cndmask_b32_e32 v0, v0, v22, vcc
	v_cndmask_b32_e64 v3, v3, 5, vcc
	v_cmp_gt_f32_e32 vcc, v21, v0
	s_nop 1
	v_cndmask_b32_e32 v0, v0, v21, vcc
	v_cndmask_b32_e64 v3, v3, 6, vcc
	v_cmp_gt_f32_e32 vcc, v20, v0
	s_nop 1
	v_cndmask_b32_e32 v0, v0, v20, vcc
	v_cndmask_b32_e64 v3, v3, 7, vcc
	v_cmp_gt_f32_e32 vcc, v19, v0
	s_nop 1
	v_cndmask_b32_e32 v0, v0, v19, vcc
	v_cndmask_b32_e64 v3, v3, 8, vcc
	v_cmp_gt_f32_e32 vcc, v18, v0
	s_nop 1
	v_cndmask_b32_e32 v0, v0, v18, vcc
	v_cndmask_b32_e64 v3, v3, 9, vcc
	v_cmp_gt_f32_e32 vcc, v17, v0
	s_nop 1
	v_cndmask_b32_e32 v0, v0, v17, vcc
	v_cndmask_b32_e64 v3, v3, 10, vcc
	v_cmp_gt_f32_e32 vcc, v16, v0
	s_nop 1
	v_cndmask_b32_e32 v0, v0, v16, vcc
	v_cndmask_b32_e64 v3, v3, 11, vcc
	v_cmp_gt_f32_e32 vcc, v15, v0
	s_nop 1
	v_cndmask_b32_e32 v0, v0, v15, vcc
	v_cndmask_b32_e64 v3, v3, 12, vcc
	v_cmp_gt_f32_e32 vcc, v14, v0
	s_nop 1
	v_cndmask_b32_e32 v0, v0, v14, vcc
	v_cndmask_b32_e64 v3, v3, 13, vcc
	v_cmp_gt_f32_e32 vcc, v13, v0
	s_nop 1
	v_cndmask_b32_e32 v0, v0, v13, vcc
	v_cndmask_b32_e64 v3, v3, 14, vcc
	v_cmp_gt_f32_e32 vcc, v12, v0
	s_nop 1
	v_cndmask_b32_e32 v0, v0, v12, vcc
	v_cndmask_b32_e64 v3, v3, 15, vcc
	v_cmp_gt_f32_e32 vcc, v31, v0
	s_nop 1
	v_cndmask_b32_e32 v0, v0, v31, vcc
	v_cndmask_b32_e64 v3, v3, 16, vcc
	v_cmp_gt_f32_e32 vcc, v30, v0
	s_nop 1
	v_cndmask_b32_e32 v0, v0, v30, vcc
	v_cndmask_b32_e64 v3, v3, 17, vcc
	v_cmp_gt_f32_e32 vcc, v29, v0
	s_nop 1
	v_cndmask_b32_e32 v0, v0, v29, vcc
	v_cndmask_b32_e64 v3, v3, 18, vcc
	v_cmp_gt_f32_e32 vcc, v28, v0
	s_nop 1
	v_cndmask_b32_e32 v0, v0, v28, vcc
	v_cndmask_b32_e64 v3, v3, 19, vcc
	v_cmp_gt_f32_e32 vcc, v33, v0
	s_nop 1
	v_cndmask_b32_e32 v0, v0, v33, vcc
	v_cndmask_b32_e64 v3, v3, 20, vcc
	v_cmp_gt_f32_e32 vcc, v32, v0
	s_nop 1
	v_cndmask_b32_e32 v0, v0, v32, vcc
	v_cndmask_b32_e64 v3, v3, 21, vcc
	v_cmp_gt_f32_e32 vcc, v9, v0
	s_nop 1
	v_cndmask_b32_e32 v0, v0, v9, vcc
	v_cndmask_b32_e64 v3, v3, 22, vcc
	v_cmp_gt_f32_e32 vcc, v8, v0
	s_nop 1
	v_cndmask_b32_e32 v0, v0, v8, vcc
	v_cndmask_b32_e64 v3, v3, 23, vcc
	v_cmp_gt_f32_e32 vcc, v11, v0
	s_nop 1
	v_cndmask_b32_e32 v0, v0, v11, vcc
	v_cndmask_b32_e64 v3, v3, 24, vcc
	v_cmp_gt_f32_e32 vcc, v10, v0
	s_nop 1
	v_cndmask_b32_e32 v0, v0, v10, vcc
	v_cndmask_b32_e64 v3, v3, 25, vcc
	v_cmp_gt_f32_e32 vcc, v5, v0
	s_nop 1
	v_cndmask_b32_e32 v0, v0, v5, vcc
	v_cndmask_b32_e64 v3, v3, 26, vcc
	v_cmp_gt_f32_e32 vcc, v4, v0
	s_nop 1
	v_cndmask_b32_e32 v0, v0, v4, vcc
	v_cndmask_b32_e64 v3, v3, 27, vcc
	v_cmp_gt_f32_e32 vcc, v36, v0
	s_nop 1
	v_cndmask_b32_e32 v0, v0, v36, vcc
	v_cndmask_b32_e64 v3, v3, 28, vcc
	v_cmp_gt_f32_e32 vcc, v35, v0
	s_nop 1
	v_cndmask_b32_e32 v0, v0, v35, vcc
	v_cndmask_b32_e64 v3, v3, 29, vcc
	v_cmp_gt_f32_e32 vcc, v2, v0
	s_nop 1
	v_cndmask_b32_e32 v0, v0, v2, vcc
	v_cndmask_b32_e64 v3, v3, 30, vcc
	v_cmp_gt_f32_e32 vcc, v1, v0
	s_nop 1
	v_cndmask_b32_e64 v6, v3, 31, vcc
	v_cndmask_b32_e32 v0, v0, v1, vcc
	v_cmp_eq_u32_e64 s[0:1], 0, v6
	v_cmp_nlg_f32_e32 vcc, s20, v27
	v_lshlrev_b32_e64 v34, v6, 1
	s_or_b64 s[0:1], s[0:1], vcc
	v_cndmask_b32_e64 v3, v27, v155, s[0:1]
	v_and_b32_e32 v7, 2, v34
	v_cmp_eq_u32_e64 s[0:1], 0, v7
	v_cmp_gt_f32_e64 s[20:21], v26, v3
	s_and_b64 s[0:1], s[0:1], s[20:21]
	v_cndmask_b32_e64 v3, v3, v26, s[0:1]
	v_and_b32_e32 v37, 4, v34
	v_cndmask_b32_e64 v7, 0, 1, s[0:1]
	v_cmp_eq_u32_e64 s[0:1], 0, v37
	v_cmp_gt_f32_e64 s[20:21], v25, v3
	s_and_b64 s[0:1], s[0:1], s[20:21]
	v_cndmask_b32_e64 v3, v3, v25, s[0:1]
	v_and_b32_e32 v37, 8, v34
	v_cndmask_b32_e64 v7, v7, 2, s[0:1]
	v_cmp_eq_u32_e64 s[0:1], 0, v37
	v_cmp_gt_f32_e64 s[20:21], v24, v3
	s_and_b64 s[0:1], s[0:1], s[20:21]
	v_cndmask_b32_e64 v3, v3, v24, s[0:1]
	v_and_b32_e32 v37, 16, v34
	v_cndmask_b32_e64 v7, v7, 3, s[0:1]
	v_cmp_eq_u32_e64 s[0:1], 0, v37
	v_cmp_gt_f32_e64 s[20:21], v23, v3
	s_and_b64 s[0:1], s[0:1], s[20:21]
	v_cndmask_b32_e64 v3, v3, v23, s[0:1]
	v_and_b32_e32 v37, 32, v34
	v_cndmask_b32_e64 v7, v7, 4, s[0:1]
	v_cmp_eq_u32_e64 s[0:1], 0, v37
	v_cmp_gt_f32_e64 s[20:21], v22, v3
	s_and_b64 s[0:1], s[0:1], s[20:21]
	v_cndmask_b32_e64 v3, v3, v22, s[0:1]
	v_and_b32_e32 v37, 64, v34
	v_cndmask_b32_e64 v7, v7, 5, s[0:1]
	v_cmp_eq_u32_e64 s[0:1], 0, v37
	v_cmp_gt_f32_e64 s[20:21], v21, v3
	s_and_b64 s[0:1], s[0:1], s[20:21]
	v_cndmask_b32_e64 v3, v3, v21, s[0:1]
	v_and_b32_e32 v37, 0x80, v34
	v_cndmask_b32_e64 v7, v7, 6, s[0:1]
	v_cmp_eq_u32_e64 s[0:1], 0, v37
	v_cmp_gt_f32_e64 s[20:21], v20, v3
	s_and_b64 s[0:1], s[0:1], s[20:21]
	v_cndmask_b32_e64 v3, v3, v20, s[0:1]
	v_and_b32_e32 v37, 0x100, v34
	v_cndmask_b32_e64 v7, v7, 7, s[0:1]
	v_cmp_eq_u32_e64 s[0:1], 0, v37
	v_cmp_gt_f32_e64 s[20:21], v19, v3
	s_and_b64 s[0:1], s[0:1], s[20:21]
	v_cndmask_b32_e64 v3, v3, v19, s[0:1]
	v_and_b32_e32 v37, 0x200, v34
	v_cndmask_b32_e64 v7, v7, 8, s[0:1]
	v_cmp_eq_u32_e64 s[0:1], 0, v37
	v_cmp_gt_f32_e64 s[20:21], v18, v3
	s_and_b64 s[0:1], s[0:1], s[20:21]
	v_cndmask_b32_e64 v3, v3, v18, s[0:1]
	v_and_b32_e32 v37, 0x400, v34
	v_cndmask_b32_e64 v7, v7, 9, s[0:1]
	v_cmp_eq_u32_e64 s[0:1], 0, v37
	v_cmp_gt_f32_e64 s[20:21], v17, v3
	s_and_b64 s[0:1], s[0:1], s[20:21]
	v_cndmask_b32_e64 v3, v3, v17, s[0:1]
	v_and_b32_e32 v37, 0x800, v34
	v_cndmask_b32_e64 v7, v7, 10, s[0:1]
	v_cmp_eq_u32_e64 s[0:1], 0, v37
	v_cmp_gt_f32_e64 s[20:21], v16, v3
	s_and_b64 s[0:1], s[0:1], s[20:21]
	v_cndmask_b32_e64 v3, v3, v16, s[0:1]
	v_and_b32_e32 v37, 0x1000, v34
	v_cndmask_b32_e64 v7, v7, 11, s[0:1]
	v_cmp_eq_u32_e64 s[0:1], 0, v37
	v_cmp_gt_f32_e64 s[20:21], v15, v3
	s_and_b64 s[0:1], s[0:1], s[20:21]
	v_cndmask_b32_e64 v3, v3, v15, s[0:1]
	v_and_b32_e32 v37, 0x2000, v34
	v_cndmask_b32_e64 v7, v7, 12, s[0:1]
	v_cmp_eq_u32_e64 s[0:1], 0, v37
	v_cmp_gt_f32_e64 s[20:21], v14, v3
	s_and_b64 s[0:1], s[0:1], s[20:21]
	v_cndmask_b32_e64 v3, v3, v14, s[0:1]
	v_and_b32_e32 v37, 0x4000, v34
	v_cndmask_b32_e64 v7, v7, 13, s[0:1]
	v_cmp_eq_u32_e64 s[0:1], 0, v37
	v_cmp_gt_f32_e64 s[20:21], v13, v3
	s_and_b64 s[0:1], s[0:1], s[20:21]
	v_cndmask_b32_e64 v3, v3, v13, s[0:1]
	v_and_b32_e32 v37, 0x8000, v34
	v_cndmask_b32_e64 v7, v7, 14, s[0:1]
	v_cmp_eq_u32_e64 s[0:1], 0, v37
	v_cmp_gt_f32_e64 s[20:21], v12, v3
	s_and_b64 s[0:1], s[0:1], s[20:21]
	v_cndmask_b32_e64 v3, v3, v12, s[0:1]
	v_and_b32_e32 v37, 0x10000, v34
	v_cndmask_b32_e64 v7, v7, 15, s[0:1]
	v_cmp_eq_u32_e64 s[0:1], 0, v37
	v_cmp_gt_f32_e64 s[20:21], v31, v3
	s_and_b64 s[0:1], s[0:1], s[20:21]
	v_cndmask_b32_e64 v3, v3, v31, s[0:1]
	v_and_b32_e32 v37, 0x20000, v34
	v_cndmask_b32_e64 v7, v7, 16, s[0:1]
	v_cmp_eq_u32_e64 s[0:1], 0, v37
	v_cmp_gt_f32_e64 s[20:21], v30, v3
	s_and_b64 s[0:1], s[0:1], s[20:21]
	v_cndmask_b32_e64 v3, v3, v30, s[0:1]
	v_and_b32_e32 v37, 0x40000, v34
	v_cndmask_b32_e64 v7, v7, 17, s[0:1]
	v_cmp_eq_u32_e64 s[0:1], 0, v37
	v_cmp_gt_f32_e64 s[20:21], v29, v3
	s_and_b64 s[0:1], s[0:1], s[20:21]
	v_cndmask_b32_e64 v3, v3, v29, s[0:1]
	v_and_b32_e32 v37, 0x80000, v34
	v_cndmask_b32_e64 v7, v7, 18, s[0:1]
	v_cmp_eq_u32_e64 s[0:1], 0, v37
	v_cmp_gt_f32_e64 s[20:21], v28, v3
	s_and_b64 s[0:1], s[0:1], s[20:21]
	v_cndmask_b32_e64 v3, v3, v28, s[0:1]
	v_and_b32_e32 v37, 0x100000, v34
	v_cndmask_b32_e64 v7, v7, 19, s[0:1]
	v_cmp_eq_u32_e64 s[0:1], 0, v37
	v_cmp_gt_f32_e64 s[20:21], v33, v3
	s_and_b64 s[0:1], s[0:1], s[20:21]
	v_cndmask_b32_e64 v3, v3, v33, s[0:1]
	v_and_b32_e32 v37, 0x200000, v34
	v_cndmask_b32_e64 v7, v7, 20, s[0:1]
	v_cmp_eq_u32_e64 s[0:1], 0, v37
	v_cmp_gt_f32_e64 s[20:21], v32, v3
	s_and_b64 s[0:1], s[0:1], s[20:21]
	v_cndmask_b32_e64 v3, v3, v32, s[0:1]
	v_and_b32_e32 v37, 0x400000, v34
	v_cndmask_b32_e64 v7, v7, 21, s[0:1]
	v_cmp_eq_u32_e64 s[0:1], 0, v37
	v_cmp_gt_f32_e64 s[20:21], v9, v3
	s_and_b64 s[0:1], s[0:1], s[20:21]
	v_cndmask_b32_e64 v3, v3, v9, s[0:1]
	v_and_b32_e32 v37, 0x800000, v34
	v_cndmask_b32_e64 v7, v7, 22, s[0:1]
	v_cmp_eq_u32_e64 s[0:1], 0, v37
	v_cmp_gt_f32_e64 s[20:21], v8, v3
	s_and_b64 s[0:1], s[0:1], s[20:21]
	v_cndmask_b32_e64 v3, v3, v8, s[0:1]
	v_and_b32_e32 v37, 0x1000000, v34
	v_cndmask_b32_e64 v7, v7, 23, s[0:1]
	v_cmp_eq_u32_e64 s[0:1], 0, v37
	v_cmp_gt_f32_e64 s[20:21], v11, v3
	s_and_b64 s[0:1], s[0:1], s[20:21]
	v_cndmask_b32_e64 v3, v3, v11, s[0:1]
	v_and_b32_e32 v37, 0x2000000, v34
	v_cndmask_b32_e64 v7, v7, 24, s[0:1]
	v_cmp_eq_u32_e64 s[0:1], 0, v37
	v_cmp_gt_f32_e64 s[20:21], v10, v3
	s_and_b64 s[0:1], s[0:1], s[20:21]
	v_cndmask_b32_e64 v3, v3, v10, s[0:1]
	v_and_b32_e32 v37, 0x4000000, v34
	v_cndmask_b32_e64 v7, v7, 25, s[0:1]
	v_cmp_eq_u32_e64 s[0:1], 0, v37
	v_cmp_gt_f32_e64 s[20:21], v5, v3
	s_and_b64 s[0:1], s[0:1], s[20:21]
	v_cndmask_b32_e64 v3, v3, v5, s[0:1]
	v_and_b32_e32 v37, 0x8000000, v34
	v_cndmask_b32_e64 v7, v7, 26, s[0:1]
	v_cmp_eq_u32_e64 s[0:1], 0, v37
	v_cmp_gt_f32_e64 s[20:21], v4, v3
	s_and_b64 s[0:1], s[0:1], s[20:21]
	v_cndmask_b32_e64 v3, v3, v4, s[0:1]
	v_and_b32_e32 v37, 0x10000000, v34
	v_cndmask_b32_e64 v7, v7, 27, s[0:1]
	v_cmp_eq_u32_e64 s[0:1], 0, v37
	v_cmp_gt_f32_e64 s[20:21], v36, v3
	s_and_b64 s[0:1], s[0:1], s[20:21]
	v_cndmask_b32_e64 v3, v3, v36, s[0:1]
	v_and_b32_e32 v37, 0x20000000, v34
	v_cndmask_b32_e64 v7, v7, 28, s[0:1]
	v_cmp_eq_u32_e64 s[0:1], 0, v37
	v_cmp_gt_f32_e64 s[20:21], v35, v3
	s_and_b64 s[0:1], s[0:1], s[20:21]
	v_cndmask_b32_e64 v3, v3, v35, s[0:1]
	v_and_b32_e32 v37, 2.0, v34
	v_cndmask_b32_e64 v7, v7, 29, s[0:1]
	v_cmp_eq_u32_e64 s[0:1], 0, v37
	v_cmp_gt_f32_e64 s[20:21], v2, v3
	s_and_b64 s[0:1], s[0:1], s[20:21]
	v_cndmask_b32_e64 v3, v3, v2, s[0:1]
	v_cndmask_b32_e64 v7, v7, 30, s[0:1]
	v_cmp_ne_u32_e64 s[0:1], 31, v6
	v_cmp_gt_f32_e64 s[20:21], v1, v3
	s_and_b64 s[0:1], s[0:1], s[20:21]
	v_cndmask_b32_e64 v7, v7, 31, s[0:1]
	v_lshl_or_b32 v37, 1, v7, v34
	v_and_b32_e32 v34, 1, v37
	v_cndmask_b32_e64 v3, v3, v1, s[0:1]
	v_cmp_eq_u32_e64 s[0:1], 1, v34
	s_or_b64 s[0:1], s[0:1], vcc
	v_and_b32_e32 v38, 2, v37
	v_cndmask_b32_e64 v34, v27, v155, s[0:1]
	v_cmp_eq_u32_e64 s[0:1], 0, v38
	v_cmp_gt_f32_e64 s[20:21], v26, v34
	s_and_b64 s[0:1], s[0:1], s[20:21]
	v_cndmask_b32_e64 v34, v34, v26, s[0:1]
	v_and_b32_e32 v39, 4, v37
	v_cndmask_b32_e64 v38, 0, 1, s[0:1]
	v_cmp_eq_u32_e64 s[0:1], 0, v39
	v_cmp_gt_f32_e64 s[20:21], v25, v34
	s_and_b64 s[0:1], s[0:1], s[20:21]
	v_cndmask_b32_e64 v34, v34, v25, s[0:1]
	v_and_b32_e32 v39, 8, v37
	v_cndmask_b32_e64 v38, v38, 2, s[0:1]
	v_cmp_eq_u32_e64 s[0:1], 0, v39
	v_cmp_gt_f32_e64 s[20:21], v24, v34
	s_and_b64 s[0:1], s[0:1], s[20:21]
	v_cndmask_b32_e64 v34, v34, v24, s[0:1]
	v_and_b32_e32 v39, 16, v37
	v_cndmask_b32_e64 v38, v38, 3, s[0:1]
	v_cmp_eq_u32_e64 s[0:1], 0, v39
	v_cmp_gt_f32_e64 s[20:21], v23, v34
	s_and_b64 s[0:1], s[0:1], s[20:21]
	v_cndmask_b32_e64 v34, v34, v23, s[0:1]
	v_and_b32_e32 v39, 32, v37
	v_cndmask_b32_e64 v38, v38, 4, s[0:1]
	v_cmp_eq_u32_e64 s[0:1], 0, v39
	v_cmp_gt_f32_e64 s[20:21], v22, v34
	s_and_b64 s[0:1], s[0:1], s[20:21]
	v_cndmask_b32_e64 v34, v34, v22, s[0:1]
	v_and_b32_e32 v39, 64, v37
	v_cndmask_b32_e64 v38, v38, 5, s[0:1]
	v_cmp_eq_u32_e64 s[0:1], 0, v39
	v_cmp_gt_f32_e64 s[20:21], v21, v34
	s_and_b64 s[0:1], s[0:1], s[20:21]
	v_cndmask_b32_e64 v34, v34, v21, s[0:1]
	v_and_b32_e32 v39, 0x80, v37
	v_cndmask_b32_e64 v38, v38, 6, s[0:1]
	v_cmp_eq_u32_e64 s[0:1], 0, v39
	v_cmp_gt_f32_e64 s[20:21], v20, v34
	s_and_b64 s[0:1], s[0:1], s[20:21]
	v_cndmask_b32_e64 v34, v34, v20, s[0:1]
	v_and_b32_e32 v39, 0x100, v37
	v_cndmask_b32_e64 v38, v38, 7, s[0:1]
	v_cmp_eq_u32_e64 s[0:1], 0, v39
	v_cmp_gt_f32_e64 s[20:21], v19, v34
	s_and_b64 s[0:1], s[0:1], s[20:21]
	v_cndmask_b32_e64 v34, v34, v19, s[0:1]
	v_and_b32_e32 v39, 0x200, v37
	v_cndmask_b32_e64 v38, v38, 8, s[0:1]
	v_cmp_eq_u32_e64 s[0:1], 0, v39
	v_cmp_gt_f32_e64 s[20:21], v18, v34
	s_and_b64 s[0:1], s[0:1], s[20:21]
	v_cndmask_b32_e64 v34, v34, v18, s[0:1]
	v_and_b32_e32 v39, 0x400, v37
	v_cndmask_b32_e64 v38, v38, 9, s[0:1]
	v_cmp_eq_u32_e64 s[0:1], 0, v39
	v_cmp_gt_f32_e64 s[20:21], v17, v34
	s_and_b64 s[0:1], s[0:1], s[20:21]
	v_cndmask_b32_e64 v34, v34, v17, s[0:1]
	v_and_b32_e32 v39, 0x800, v37
	v_cndmask_b32_e64 v38, v38, 10, s[0:1]
	v_cmp_eq_u32_e64 s[0:1], 0, v39
	v_cmp_gt_f32_e64 s[20:21], v16, v34
	s_and_b64 s[0:1], s[0:1], s[20:21]
	v_cndmask_b32_e64 v34, v34, v16, s[0:1]
	v_and_b32_e32 v39, 0x1000, v37
	v_cndmask_b32_e64 v38, v38, 11, s[0:1]
	v_cmp_eq_u32_e64 s[0:1], 0, v39
	v_cmp_gt_f32_e64 s[20:21], v15, v34
	s_and_b64 s[0:1], s[0:1], s[20:21]
	v_cndmask_b32_e64 v34, v34, v15, s[0:1]
	v_and_b32_e32 v39, 0x2000, v37
	v_cndmask_b32_e64 v38, v38, 12, s[0:1]
	v_cmp_eq_u32_e64 s[0:1], 0, v39
	v_cmp_gt_f32_e64 s[20:21], v14, v34
	s_and_b64 s[0:1], s[0:1], s[20:21]
	v_cndmask_b32_e64 v34, v34, v14, s[0:1]
	v_and_b32_e32 v39, 0x4000, v37
	v_cndmask_b32_e64 v38, v38, 13, s[0:1]
	v_cmp_eq_u32_e64 s[0:1], 0, v39
	v_cmp_gt_f32_e64 s[20:21], v13, v34
	s_and_b64 s[0:1], s[0:1], s[20:21]
	v_cndmask_b32_e64 v34, v34, v13, s[0:1]
	v_and_b32_e32 v39, 0x8000, v37
	v_cndmask_b32_e64 v38, v38, 14, s[0:1]
	v_cmp_eq_u32_e64 s[0:1], 0, v39
	v_cmp_gt_f32_e64 s[20:21], v12, v34
	s_and_b64 s[0:1], s[0:1], s[20:21]
	v_cndmask_b32_e64 v34, v34, v12, s[0:1]
	v_and_b32_e32 v39, 0x10000, v37
	v_cndmask_b32_e64 v38, v38, 15, s[0:1]
	v_cmp_eq_u32_e64 s[0:1], 0, v39
	v_cmp_gt_f32_e64 s[20:21], v31, v34
	s_and_b64 s[0:1], s[0:1], s[20:21]
	v_cndmask_b32_e64 v34, v34, v31, s[0:1]
	v_and_b32_e32 v39, 0x20000, v37
	v_cndmask_b32_e64 v38, v38, 16, s[0:1]
	v_cmp_eq_u32_e64 s[0:1], 0, v39
	v_cmp_gt_f32_e64 s[20:21], v30, v34
	s_and_b64 s[0:1], s[0:1], s[20:21]
	v_cndmask_b32_e64 v34, v34, v30, s[0:1]
	v_and_b32_e32 v39, 0x40000, v37
	v_cndmask_b32_e64 v38, v38, 17, s[0:1]
	v_cmp_eq_u32_e64 s[0:1], 0, v39
	v_cmp_gt_f32_e64 s[20:21], v29, v34
	s_and_b64 s[0:1], s[0:1], s[20:21]
	v_cndmask_b32_e64 v34, v34, v29, s[0:1]
	v_and_b32_e32 v39, 0x80000, v37
	v_cndmask_b32_e64 v38, v38, 18, s[0:1]
	v_cmp_eq_u32_e64 s[0:1], 0, v39
	v_cmp_gt_f32_e64 s[20:21], v28, v34
	s_and_b64 s[0:1], s[0:1], s[20:21]
	v_cndmask_b32_e64 v34, v34, v28, s[0:1]
	v_and_b32_e32 v39, 0x100000, v37
	v_cndmask_b32_e64 v38, v38, 19, s[0:1]
	v_cmp_eq_u32_e64 s[0:1], 0, v39
	v_cmp_gt_f32_e64 s[20:21], v33, v34
	s_and_b64 s[0:1], s[0:1], s[20:21]
	v_cndmask_b32_e64 v34, v34, v33, s[0:1]
	v_and_b32_e32 v39, 0x200000, v37
	v_cndmask_b32_e64 v38, v38, 20, s[0:1]
	v_cmp_eq_u32_e64 s[0:1], 0, v39
	v_cmp_gt_f32_e64 s[20:21], v32, v34
	s_and_b64 s[0:1], s[0:1], s[20:21]
	v_cndmask_b32_e64 v34, v34, v32, s[0:1]
	v_and_b32_e32 v39, 0x400000, v37
	v_cndmask_b32_e64 v38, v38, 21, s[0:1]
	v_cmp_eq_u32_e64 s[0:1], 0, v39
	v_cmp_gt_f32_e64 s[20:21], v9, v34
	s_and_b64 s[0:1], s[0:1], s[20:21]
	v_cndmask_b32_e64 v34, v34, v9, s[0:1]
	v_and_b32_e32 v39, 0x800000, v37
	v_cndmask_b32_e64 v38, v38, 22, s[0:1]
	v_cmp_eq_u32_e64 s[0:1], 0, v39
	v_cmp_gt_f32_e64 s[20:21], v8, v34
	s_and_b64 s[0:1], s[0:1], s[20:21]
	v_cndmask_b32_e64 v34, v34, v8, s[0:1]
	v_and_b32_e32 v39, 0x1000000, v37
	v_cndmask_b32_e64 v38, v38, 23, s[0:1]
	v_cmp_eq_u32_e64 s[0:1], 0, v39
	v_cmp_gt_f32_e64 s[20:21], v11, v34
	s_and_b64 s[0:1], s[0:1], s[20:21]
	v_cndmask_b32_e64 v34, v34, v11, s[0:1]
	v_and_b32_e32 v39, 0x2000000, v37
	v_cndmask_b32_e64 v38, v38, 24, s[0:1]
	v_cmp_eq_u32_e64 s[0:1], 0, v39
	v_cmp_gt_f32_e64 s[20:21], v10, v34
	s_and_b64 s[0:1], s[0:1], s[20:21]
	v_cndmask_b32_e64 v34, v34, v10, s[0:1]
	v_and_b32_e32 v39, 0x4000000, v37
	v_cndmask_b32_e64 v38, v38, 25, s[0:1]
	v_cmp_eq_u32_e64 s[0:1], 0, v39
	v_cmp_gt_f32_e64 s[20:21], v5, v34
	s_and_b64 s[0:1], s[0:1], s[20:21]
	v_cndmask_b32_e64 v34, v34, v5, s[0:1]
	v_and_b32_e32 v39, 0x8000000, v37
	v_cndmask_b32_e64 v38, v38, 26, s[0:1]
	v_cmp_eq_u32_e64 s[0:1], 0, v39
	v_cmp_gt_f32_e64 s[20:21], v4, v34
	s_and_b64 s[0:1], s[0:1], s[20:21]
	v_cndmask_b32_e64 v34, v34, v4, s[0:1]
	v_and_b32_e32 v39, 0x10000000, v37
	v_cndmask_b32_e64 v38, v38, 27, s[0:1]
	v_cmp_eq_u32_e64 s[0:1], 0, v39
	v_cmp_gt_f32_e64 s[20:21], v36, v34
	s_and_b64 s[0:1], s[0:1], s[20:21]
	v_cndmask_b32_e64 v34, v34, v36, s[0:1]
	v_and_b32_e32 v39, 0x20000000, v37
	v_cndmask_b32_e64 v38, v38, 28, s[0:1]
	v_cmp_eq_u32_e64 s[0:1], 0, v39
	v_cmp_gt_f32_e64 s[20:21], v35, v34
	s_and_b64 s[0:1], s[0:1], s[20:21]
	v_cndmask_b32_e64 v34, v34, v35, s[0:1]
	v_and_b32_e32 v39, 2.0, v37
	v_cndmask_b32_e64 v38, v38, 29, s[0:1]
	v_cmp_eq_u32_e64 s[0:1], 0, v39
	v_cmp_gt_f32_e64 s[20:21], v2, v34
	s_and_b64 s[0:1], s[0:1], s[20:21]
	v_cndmask_b32_e64 v39, v34, v2, s[0:1]
	v_cndmask_b32_e64 v38, v38, 30, s[0:1]
	v_cmp_lt_i32_e64 s[0:1], -1, v37
	v_cmp_gt_f32_e64 s[20:21], v1, v39
	s_and_b64 s[0:1], s[0:1], s[20:21]
	v_cndmask_b32_e64 v34, v38, 31, s[0:1]
	v_cndmask_b32_e64 v38, v39, v1, s[0:1]
	v_lshlrev_b32_e64 v39, v34, 1
	v_or_b32_e32 v40, v39, v37
	v_and_b32_e32 v41, 1, v40
	v_cmp_eq_u32_e64 s[0:1], 1, v41
	s_or_b64 vcc, s[0:1], vcc
	v_cndmask_b32_e32 v27, v27, v155, vcc
	v_bitop3_b32 v41, v39, 2, v37 bitop3:0xc8
	v_cmp_eq_u32_e32 vcc, 0, v41
	v_cmp_gt_f32_e64 s[0:1], v26, v27
	s_and_b64 s[20:21], vcc, s[0:1]
	v_cndmask_b32_e64 v26, v27, v26, s[20:21]
	v_bitop3_b32 v27, v39, 4, v37 bitop3:0xc8
	v_cmp_eq_u32_e32 vcc, 0, v27
	v_cmp_gt_f32_e64 s[0:1], v25, v26
	s_and_b64 s[22:23], vcc, s[0:1]
	v_cndmask_b32_e64 v25, v26, v25, s[22:23]
	v_bitop3_b32 v26, v39, 8, v37 bitop3:0xc8
	v_cmp_eq_u32_e32 vcc, 0, v26
	v_cmp_gt_f32_e64 s[0:1], v24, v25
	s_and_b64 s[24:25], vcc, s[0:1]
	v_cndmask_b32_e64 v24, v25, v24, s[24:25]
	v_bitop3_b32 v25, v39, 16, v37 bitop3:0xc8
	v_cmp_eq_u32_e32 vcc, 0, v25
	v_cmp_gt_f32_e64 s[0:1], v23, v24
	s_and_b64 s[26:27], vcc, s[0:1]
	v_cndmask_b32_e64 v23, v24, v23, s[26:27]
	v_bitop3_b32 v24, v39, 32, v37 bitop3:0xc8
	v_cmp_eq_u32_e32 vcc, 0, v24
	v_cmp_gt_f32_e64 s[0:1], v22, v23
	s_and_b64 s[28:29], vcc, s[0:1]
	v_cndmask_b32_e64 v22, v23, v22, s[28:29]
	v_bitop3_b32 v23, v39, 64, v37 bitop3:0xc8
	v_cmp_eq_u32_e32 vcc, 0, v23
	v_cmp_gt_f32_e64 s[0:1], v21, v22
	s_and_b64 s[30:31], vcc, s[0:1]
	s_movk_i32 s0, 0x80
	v_cndmask_b32_e64 v21, v22, v21, s[30:31]
	v_bitop3_b32 v22, v39, s0, v37 bitop3:0xc8
	v_cmp_eq_u32_e32 vcc, 0, v22
	v_cmp_gt_f32_e64 s[0:1], v20, v21
	s_and_b64 s[34:35], vcc, s[0:1]
	v_cndmask_b32_e64 v20, v21, v20, s[34:35]
	v_bitop3_b32 v21, v39, s33, v37 bitop3:0xc8
	v_cmp_eq_u32_e32 vcc, 0, v21
	v_cmp_gt_f32_e64 s[0:1], v19, v20
	s_and_b64 s[36:37], vcc, s[0:1]
	s_movk_i32 s0, 0x200
	v_cndmask_b32_e64 v19, v20, v19, s[36:37]
	v_bitop3_b32 v20, v39, s0, v37 bitop3:0xc8
	v_cmp_eq_u32_e32 vcc, 0, v20
	v_cmp_gt_f32_e64 s[0:1], v18, v19
	s_and_b64 s[38:39], vcc, s[0:1]
	s_movk_i32 s0, 0x400
	v_cndmask_b32_e64 v18, v19, v18, s[38:39]
	v_bitop3_b32 v19, v39, s0, v37 bitop3:0xc8
	v_cmp_eq_u32_e32 vcc, 0, v19
	v_cmp_gt_f32_e64 s[0:1], v17, v18
	s_and_b64 s[40:41], vcc, s[0:1]
	s_movk_i32 s0, 0x800
	v_cndmask_b32_e64 v17, v18, v17, s[40:41]
	v_bitop3_b32 v18, v39, s0, v37 bitop3:0xc8
	v_cmp_eq_u32_e32 vcc, 0, v18
	v_cmp_gt_f32_e64 s[0:1], v16, v17
	s_and_b64 s[42:43], vcc, s[0:1]
	s_movk_i32 s0, 0x1000
	v_cndmask_b32_e64 v16, v17, v16, s[42:43]
	v_bitop3_b32 v17, v39, s0, v37 bitop3:0xc8
	v_cmp_eq_u32_e32 vcc, 0, v17
	v_cmp_gt_f32_e64 s[0:1], v15, v16
	s_and_b64 s[44:45], vcc, s[0:1]
	s_movk_i32 s0, 0x2000
	v_cndmask_b32_e64 v15, v16, v15, s[44:45]
	v_bitop3_b32 v16, v39, s0, v37 bitop3:0xc8
	v_cmp_eq_u32_e32 vcc, 0, v16
	v_cmp_gt_f32_e64 s[0:1], v14, v15
	s_and_b64 s[46:47], vcc, s[0:1]
	s_movk_i32 s0, 0x4000
	v_cndmask_b32_e64 v14, v15, v14, s[46:47]
	v_bitop3_b32 v15, v39, s0, v37 bitop3:0xc8
	v_cmp_eq_u32_e32 vcc, 0, v15
	v_cmp_gt_f32_e64 s[0:1], v13, v14
	s_and_b64 s[48:49], vcc, s[0:1]
	s_mov_b32 s0, 0x8000
	v_cndmask_b32_e64 v13, v14, v13, s[48:49]
	v_bitop3_b32 v14, v39, s0, v37 bitop3:0xc8
	v_cmp_eq_u32_e32 vcc, 0, v14
	v_cmp_gt_f32_e64 s[0:1], v12, v13
	s_and_b64 s[50:51], vcc, s[0:1]
	s_mov_b32 s0, 0x10000
	v_cndmask_b32_e64 v12, v13, v12, s[50:51]
	v_bitop3_b32 v13, v39, s0, v37 bitop3:0xc8
	v_cmp_eq_u32_e32 vcc, 0, v13
	v_cmp_gt_f32_e64 s[0:1], v31, v12
	s_and_b64 s[52:53], vcc, s[0:1]
	s_mov_b32 s0, 0x20000
	v_cndmask_b32_e64 v12, v12, v31, s[52:53]
	v_bitop3_b32 v13, v39, s0, v37 bitop3:0xc8
	v_cmp_eq_u32_e32 vcc, 0, v13
	v_cmp_gt_f32_e64 s[0:1], v30, v12
	s_and_b64 s[54:55], vcc, s[0:1]
	s_mov_b32 s0, 0x40000
	v_cndmask_b32_e64 v12, v12, v30, s[54:55]
	v_bitop3_b32 v13, v39, s0, v37 bitop3:0xc8
	v_cmp_eq_u32_e32 vcc, 0, v13
	v_cmp_gt_f32_e64 s[0:1], v29, v12
	s_and_b64 s[56:57], vcc, s[0:1]
	s_mov_b32 s0, 0x80000
	v_cndmask_b32_e64 v12, v12, v29, s[56:57]
	v_bitop3_b32 v13, v39, s0, v37 bitop3:0xc8
	v_cmp_eq_u32_e32 vcc, 0, v13
	v_cmp_gt_f32_e64 s[0:1], v28, v12
	s_and_b64 s[58:59], vcc, s[0:1]
	s_mov_b32 s0, 0x100000
	v_cndmask_b32_e64 v12, v12, v28, s[58:59]
	v_bitop3_b32 v13, v39, s0, v37 bitop3:0xc8
	v_cmp_eq_u32_e32 vcc, 0, v13
	v_cmp_gt_f32_e64 s[0:1], v33, v12
	s_and_b64 s[60:61], vcc, s[0:1]
	s_mov_b32 s0, 0x200000
	v_cndmask_b32_e64 v12, v12, v33, s[60:61]
	v_bitop3_b32 v13, v39, s0, v37 bitop3:0xc8
	v_cmp_eq_u32_e32 vcc, 0, v13
	v_cmp_gt_f32_e64 s[0:1], v32, v12
	s_and_b64 s[62:63], vcc, s[0:1]
	s_mov_b32 s0, 0x400000
	v_cndmask_b32_e64 v12, v12, v32, s[62:63]
	v_bitop3_b32 v13, v39, s0, v37 bitop3:0xc8
	v_cmp_eq_u32_e32 vcc, 0, v13
	v_cmp_gt_f32_e64 s[0:1], v9, v12
	s_and_b64 s[64:65], vcc, s[0:1]
	v_cndmask_b32_e64 v9, v12, v9, s[64:65]
	v_bitop3_b32 v12, v39, s11, v37 bitop3:0xc8
	v_cmp_eq_u32_e32 vcc, 0, v12
	v_cmp_gt_f32_e64 s[0:1], v8, v9
	s_and_b64 s[66:67], vcc, s[0:1]
	s_mov_b32 s0, 0x1000000
	v_cndmask_b32_e64 v8, v9, v8, s[66:67]
	v_bitop3_b32 v9, v39, s0, v37 bitop3:0xc8
	v_cmp_eq_u32_e32 vcc, 0, v9
	v_cmp_gt_f32_e64 s[0:1], v11, v8
	s_and_b64 s[68:69], vcc, s[0:1]
	s_brev_b32 s0, 64
	v_cndmask_b32_e64 v8, v8, v11, s[68:69]
	v_bitop3_b32 v9, v39, s0, v37 bitop3:0xc8
	v_cmp_eq_u32_e32 vcc, 0, v9
	v_cmp_gt_f32_e64 s[0:1], v10, v8
	s_and_b64 s[70:71], vcc, s[0:1]
	s_brev_b32 s0, 32
	v_cndmask_b32_e64 v8, v8, v10, s[70:71]
	v_bitop3_b32 v9, v39, s0, v37 bitop3:0xc8
	v_cmp_eq_u32_e32 vcc, 0, v9
	v_cmp_gt_f32_e64 s[0:1], v5, v8
	s_and_b64 s[72:73], vcc, s[0:1]
	s_brev_b32 s0, 16
	v_cndmask_b32_e64 v5, v8, v5, s[72:73]
	v_bitop3_b32 v8, v39, s0, v37 bitop3:0xc8
	v_cmp_eq_u32_e32 vcc, 0, v8
	v_cmp_gt_f32_e64 s[0:1], v4, v5
	s_and_b64 s[76:77], vcc, s[0:1]
	s_brev_b32 s0, 8
	v_cndmask_b32_e64 v4, v5, v4, s[76:77]
	v_bitop3_b32 v5, v39, s0, v37 bitop3:0xc8
	v_cmp_eq_u32_e32 vcc, 0, v5
	v_cmp_gt_f32_e64 s[0:1], v36, v4
	s_and_b64 s[74:75], vcc, s[0:1]
	s_brev_b32 s0, 4
	v_cndmask_b32_e64 v4, v4, v36, s[74:75]
	v_bitop3_b32 v5, v39, s0, v37 bitop3:0xc8
	v_cmp_eq_u32_e32 vcc, 0, v5
	v_cmp_gt_f32_e64 s[0:1], v35, v4
	s_and_b64 s[78:79], vcc, s[0:1]
	v_cndmask_b32_e64 v4, v4, v35, s[78:79]
	v_bitop3_b32 v5, v39, 2.0, v37 bitop3:0xc8
	v_cmp_eq_u32_e32 vcc, 0, v5
	v_cmp_gt_f32_e64 s[0:1], v2, v4
	s_and_b64 s[80:81], vcc, s[0:1]
	v_cndmask_b32_e64 v2, v4, v2, s[80:81]
	v_cmp_lt_i32_e32 vcc, -1, v40
	v_cmp_gt_f32_e64 s[0:1], v1, v2
	s_and_b64 s[82:83], vcc, s[0:1]
	v_cndmask_b32_e64 v1, v2, v1, s[82:83]
	v_sub_f32_e32 v2, v0, v0
	v_mul_f32_e32 v4, 0x3fb8aa3b, v2
	s_mov_b32 s0, 0x3fb8aa3b
	v_fma_f32 v5, v2, s0, -v4
	v_rndne_f32_e32 v8, v4
	v_fmac_f32_e32 v5, 0x32a5705f, v2
	v_sub_f32_e32 v4, v4, v8
	v_add_f32_e32 v4, v4, v5
	v_exp_f32_e32 v4, v4
	v_cvt_i32_f32_e32 v5, v8
	s_mov_b32 s1, 0xc2ce8ed0
	v_cmp_ngt_f32_e32 vcc, s1, v2
	v_ldexp_f32 v4, v4, v5
	s_nop 0
	v_cndmask_b32_e32 v4, 0, v4, vcc
	v_cmp_nlt_f32_e32 vcc, s13, v2
	v_sub_f32_e32 v2, v3, v0
	v_mul_f32_e32 v3, 0x3fb8aa3b, v2
	v_cndmask_b32_e32 v12, v156, v4, vcc
	v_fma_f32 v4, v2, s0, -v3
	v_rndne_f32_e32 v5, v3
	v_fmac_f32_e32 v4, 0x32a5705f, v2
	v_sub_f32_e32 v3, v3, v5
	v_add_f32_e32 v3, v3, v4
	v_exp_f32_e32 v3, v3
	v_cvt_i32_f32_e32 v4, v5
	v_cmp_ngt_f32_e32 vcc, s1, v2
	v_ldexp_f32 v3, v3, v4
	s_nop 0
	v_cndmask_b32_e32 v3, 0, v3, vcc
	v_cmp_nlt_f32_e32 vcc, s13, v2
	s_nop 1
	v_cndmask_b32_e32 v9, v156, v3, vcc
	v_sub_f32_e32 v3, v38, v0
	v_mul_f32_e32 v4, 0x3fb8aa3b, v3
	v_fma_f32 v5, v3, s0, -v4
	v_rndne_f32_e32 v8, v4
	v_fmac_f32_e32 v5, 0x32a5705f, v3
	v_sub_f32_e32 v4, v4, v8
	v_add_f32_e32 v4, v4, v5
	v_exp_f32_e32 v4, v4
	v_cvt_i32_f32_e32 v5, v8
	v_cmp_ngt_f32_e32 vcc, s1, v3
	v_sub_f32_e32 v0, v1, v0
	v_mul_f32_e32 v1, 0x3fb8aa3b, v0
	v_ldexp_f32 v4, v4, v5
	v_cndmask_b32_e32 v4, 0, v4, vcc
	v_cmp_nlt_f32_e32 vcc, s13, v3
	v_fma_f32 v3, v0, s0, -v1
	v_fmac_f32_e32 v3, 0x32a5705f, v0
	v_cndmask_b32_e32 v8, v156, v4, vcc
	v_rndne_f32_e32 v4, v1
	v_sub_f32_e32 v1, v1, v4
	v_add_f32_e32 v1, v1, v3
	v_exp_f32_e32 v1, v1
	v_cvt_i32_f32_e32 v3, v4
	v_cmp_ngt_f32_e32 vcc, s1, v0
	s_lshl_b64 s[0:1], s[88:89], 8
	v_add_f32_e32 v2, v12, v9
	v_ldexp_f32 v1, v1, v3
	v_cndmask_b32_e32 v1, 0, v1, vcc
	v_cmp_nlt_f32_e32 vcc, s13, v0
	v_lshl_add_u64 v[4:5], s[0:1], 0, v[124:125]
	v_readlane_b32 s0, v253, 4
	v_add_f32_e32 v2, v2, v8
	v_cndmask_b32_e32 v10, v156, v1, vcc
	v_lshlrev_b64 v[0:1], 2, v[4:5]
	v_readlane_b32 s1, v253, 5
	v_add_f32_e32 v11, v2, v10
	s_nop 0
	v_lshl_add_u64 v[2:3], s[0:1], 0, v[0:1]
	global_store_dword v[2:3], v6, off
	v_div_scale_f32 v2, s[0:1], v11, v11, v12
	v_rcp_f32_e32 v3, v2
	v_readlane_b32 s0, v252, 4
	v_readlane_b32 s1, v252, 5
	v_fma_f32 v13, -v2, v3, 1.0
	v_fmac_f32_e32 v3, v13, v3
	v_div_scale_f32 v13, vcc, v12, v11, v12
	v_mul_f32_e32 v14, v13, v3
	v_fma_f32 v15, -v2, v14, v13
	v_fmac_f32_e32 v14, v15, v3
	v_fma_f32 v2, -v2, v14, v13
	v_div_fmas_f32 v2, v2, v3, v14
	v_div_fixup_f32 v12, v2, v11, v12
	v_lshl_add_u64 v[2:3], s[0:1], 0, v[0:1]
	v_readlane_b32 s0, v252, 12
	v_readlane_b32 s1, v252, 13
	global_store_dword v[2:3], v12, off
	s_andn2_b64 vcc, exec, s[0:1]
	v_cndmask_b32_e64 v2, 0, 1, s[0:1]
	v_cmp_ne_u32_e64 s[84:85], 1, v2
	v_lshl_add_u64 v[2:3], v[4:5], 2, s[94:95]
	s_cbranch_vccnz .LBB0_1061
	global_load_dword v6, v[2:3], off
